# code placement: every GEMM MMA segment's 8-byte MFMA encodings put on an 8-byte boundary via a pad s_nop in front of the preceding load segment's closing wait
# baseline (speedup 1.0000x reference)
; #define PG8_STAGE(bufoff, gbase, voff) do { _Pragma("unroll") for (int _i = 0; _i < 2; ++_i) \
;         __builtin_amdgcn_global_load_lds((const unsigned*)((const char*)(gbase) + (voff)[_i]), (LAS unsigned*)(lds + (bufoff) + ldsw + _i * 8192), 16, 0, 0); } while (0)
; #define PG8_LDA(dst, b, h) do { _Pragma("unroll") for (int m = 0; m < 4; ++m) dst[m] = PG8_LD32(lds + PG8_SA(b, h) + aoff + m * 2048); } while (0)
; #define PG8_LDB(dst, b, h) do { _Pragma("unroll") for (int n = 0; n < 2; ++n) dst[n] = PG8_LD32(lds + PG8_SB(b, h) + boff + n * 2048); } while (0)
; #define PG8_WAIT_V(n) asm volatile("s_waitcnt vmcnt(" #n ")" ::: "memory")
; #define PG8_WAIT_L(n) asm volatile("s_waitcnt lgkmcnt(" #n ")" ::: "memory")
; #define PG8_BAR __builtin_amdgcn_s_barrier()
; #define PG8_SCHED __builtin_amdgcn_sched_barrier(0)
; #define PG8_STA(bufoff, nextflag, h, koff) do { if constexpr (Sched::GATHER) { unsigned _o[2]; _o[0] = (nextflag) ? nxtA[h][0] : curA[h][0]; _o[1] = (nextflag) ? nxtA[h][1] : curA[h][1]; PG8_STAGE(bufoff, Ab + (koff), _o); } \
;         else { PG8_STAGE(bufoff, ((nextflag) ? nA : cA) + (size_t)(h) * hstep + (koff), voffA); } } while (0)
; template <class Epi, class Sched, bool ALIGN_EPI, int DT>
; __device__ __forceinline__ void gemm_phase(LAS unsigned char* lds, const int KB, const Sched& S, const Epi& E) {
;     ...
;         for (int t = 0; t < nt; t += 2) {
;             const bool last = (t == nt - 2);
;             const size_t k1 = (size_t)(t + 1) * kstep, k2 = last ? 0 : (size_t)(t + 2) * kstep, k3 = k2 + kstep;
;             const char* b2 = last ? nB : cB + (size_t)(t + 2) * kstep; const char* b3 = b2 + kstep;
;             PG8_LDB(B0, 0, 0); PG8_LDB(B1, 0, 1); PG8_SCHED; PG8_LDA(At, 0, 0); PG8_STA(PG8_SA(1, 1), false, 1, k1);
;             PG8_WAIT_V(8); PG8_WAIT_L(0); PG8_BAR; PG8_MMA(0, 0, At, B0); PG8_MMA(0, 1, At, B1); PG8_BAR; PG8_SCHED;
;             PG8_LDA(At, 0, 1); PG8_STAGE(PG8_SB(0, 0), b2, voffB); PG8_STAGE(PG8_SB(0, 1), b2 + hstep, voffB); PG8_STA(PG8_SA(0, 0), last, 0, k2);
;             PG8_WAIT_V(8); PG8_WAIT_L(0); PG8_BAR; PG8_MMA(1, 0, At, B0); PG8_MMA(1, 1, At, B1); PG8_BAR; PG8_SCHED;
.LBB0_193:
	ds_read_b128 v[152:155], v175
	ds_read_b128 v[156:159], v175 offset:1024
	ds_read_b128 v[160:163], v175 offset:2048
	ds_read_b128 v[164:167], v175 offset:3072
	ds_read_b128 v[168:171], v176
	ds_read_b128 v[182:185], v176 offset:1024
	ds_read_b128 v[186:189], v176 offset:2048
	ds_read_b128 v[190:193], v176 offset:3072
	s_add_u32 s38, s36, 0x100
	s_addc_u32 s39, s37, 0
	s_add_u32 s68, s25, s36
	s_addc_u32 s69, s66, s37
	s_cmp_eq_u32 s67, 12
	s_cselect_b64 s[42:43], -1, 0
	s_and_b64 s[40:41], s[42:43], exec
	s_cselect_b32 s70, 0, s38
	s_cselect_b32 s41, s0, s69
	s_cselect_b32 s40, s23, s68
	v_lshl_add_u64 v[228:229], v[148:149], 0, s[36:37]
	s_add_i32 m0, s45, 0xc000
	ds_read_b128 v[196:199], v177
	ds_read_b128 v[200:203], v177 offset:1024
	ds_read_b128 v[204:207], v177 offset:2048
	ds_read_b128 v[208:211], v177 offset:3072
	ds_read_b128 v[212:215], v177 offset:4096
	ds_read_b128 v[216:219], v177 offset:5120
	ds_read_b128 v[220:223], v177 offset:6144
	ds_read_b128 v[224:227], v177 offset:7168
	global_load_lds_dwordx4 v[228:229], off
	v_lshl_add_u64 v[228:229], v[150:151], 0, s[36:37]
	s_add_i32 m0, s45, 0xe000
	s_nop 0
	global_load_lds_dwordx4 v[228:229], off
	s_waitcnt vmcnt(8)
	s_waitcnt lgkmcnt(0)
	s_barrier
	s_setprio 1
	s_waitcnt lgkmcnt(0)
	v_mfma_i32_16x16x64_i8 v[126:129], v[152:155], v[196:199], v[126:129]
	v_mfma_i32_16x16x64_i8 v[122:125], v[160:163], v[196:199], v[122:125]
	v_mfma_i32_16x16x64_i8 v[110:113], v[152:155], v[204:207], v[110:113]
	v_mfma_i32_16x16x64_i8 v[106:109], v[160:163], v[204:207], v[106:109]
	v_mfma_i32_16x16x64_i8 v[94:97], v[152:155], v[212:215], v[94:97]
	v_mfma_i32_16x16x64_i8 v[90:93], v[160:163], v[212:215], v[90:93]
	v_mfma_i32_16x16x64_i8 v[78:81], v[152:155], v[220:223], v[78:81]
	v_mfma_i32_16x16x64_i8 v[74:77], v[160:163], v[220:223], v[74:77]
	v_mfma_i32_16x16x64_i8 v[126:129], v[156:159], v[200:203], v[126:129]
	v_mfma_i32_16x16x64_i8 v[122:125], v[164:167], v[200:203], v[122:125]
	v_mfma_i32_16x16x64_i8 v[110:113], v[156:159], v[208:211], v[110:113]
	v_mfma_i32_16x16x64_i8 v[106:109], v[164:167], v[208:211], v[106:109]
	v_mfma_i32_16x16x64_i8 v[94:97], v[156:159], v[216:219], v[94:97]
	v_mfma_i32_16x16x64_i8 v[90:93], v[164:167], v[216:219], v[90:93]
	v_mfma_i32_16x16x64_i8 v[78:81], v[156:159], v[224:227], v[78:81]
	v_mfma_i32_16x16x64_i8 v[74:77], v[164:167], v[224:227], v[74:77]
	s_setprio 0
	s_setprio 1
	v_mfma_i32_16x16x64_i8 v[118:121], v[168:171], v[196:199], v[118:121]
	v_mfma_i32_16x16x64_i8 v[114:117], v[186:189], v[196:199], v[114:117]
	v_mfma_i32_16x16x64_i8 v[102:105], v[168:171], v[204:207], v[102:105]
	v_mfma_i32_16x16x64_i8 v[98:101], v[186:189], v[204:207], v[98:101]
	v_mfma_i32_16x16x64_i8 v[86:89], v[168:171], v[212:215], v[86:89]
	v_mfma_i32_16x16x64_i8 v[82:85], v[186:189], v[212:215], v[82:85]
	v_mfma_i32_16x16x64_i8 v[70:73], v[168:171], v[220:223], v[70:73]
	v_mfma_i32_16x16x64_i8 v[66:69], v[186:189], v[220:223], v[66:69]
	v_mfma_i32_16x16x64_i8 v[118:121], v[182:185], v[200:203], v[118:121]
	v_mfma_i32_16x16x64_i8 v[114:117], v[190:193], v[200:203], v[114:117]
	v_mfma_i32_16x16x64_i8 v[102:105], v[182:185], v[208:211], v[102:105]
	v_mfma_i32_16x16x64_i8 v[98:101], v[190:193], v[208:211], v[98:101]
	v_mfma_i32_16x16x64_i8 v[86:89], v[182:185], v[216:219], v[86:89]
	v_mfma_i32_16x16x64_i8 v[82:85], v[190:193], v[216:219], v[82:85]
	v_mfma_i32_16x16x64_i8 v[70:73], v[182:185], v[224:227], v[70:73]
	v_mfma_i32_16x16x64_i8 v[66:69], v[190:193], v[224:227], v[66:69]
	s_setprio 0
	s_barrier
	s_add_i32 s36, s62, s5
	v_lshl_add_u64 v[228:229], s[40:41], 0, v[134:135]
	s_mov_b32 m0, s36
	ds_read_b128 v[196:199], v177 offset:16384
	ds_read_b128 v[200:203], v177 offset:17408
	ds_read_b128 v[204:207], v177 offset:18432
	ds_read_b128 v[208:211], v177 offset:19456
	ds_read_b128 v[212:215], v177 offset:20480
	ds_read_b128 v[216:219], v177 offset:21504
	ds_read_b128 v[220:223], v177 offset:22528
	ds_read_b128 v[224:227], v177 offset:23552
	global_load_lds_dwordx4 v[228:229], off
	s_add_i32 m0, s36, 0x2000
	s_add_u32 s36, s40, 0x40000
	v_lshl_add_u64 v[230:231], s[40:41], 0, v[132:133]
	s_addc_u32 s37, s41, 0
	s_add_i32 s68, s63, s5
	global_load_lds_dwordx4 v[230:231], off
	v_lshl_add_u64 v[232:233], s[36:37], 0, v[134:135]
	s_mov_b32 m0, s68
	s_nop 0
	global_load_lds_dwordx4 v[232:233], off
	v_lshl_add_u64 v[232:233], s[36:37], 0, v[132:133]
	s_add_i32 m0, s68, 0x2000
	s_and_b64 s[36:37], s[8:9], s[42:43]
	s_and_b64 s[36:37], s[36:37], exec
	s_cselect_b32 s36, s26, s34
	s_cselect_b32 s37, s27, s35
	s_add_u32 s36, s36, s70
	s_addc_u32 s37, s37, 0
	global_load_lds_dwordx4 v[232:233], off
	v_lshl_add_u64 v[232:233], s[36:37], 0, v[136:137]
	s_mov_b32 m0, s45
	v_lshl_add_u64 v[234:235], s[36:37], 0, v[138:139]
	global_load_lds_dwordx4 v[232:233], off
	s_mov_b32 m0, s46
	s_nop 0
	global_load_lds_dwordx4 v[234:235], off
	s_waitcnt vmcnt(8)
	s_waitcnt lgkmcnt(0)
	s_barrier
; #define PG8_LDA(dst, b, h) do { _Pragma("unroll") for (int m = 0; m < 4; ++m) dst[m] = PG8_LD32(lds + PG8_SA(b, h) + aoff + m * 2048); } while (0)
; #define PG8_LDB(dst, b, h) do { _Pragma("unroll") for (int n = 0; n < 2; ++n) dst[n] = PG8_LD32(lds + PG8_SB(b, h) + boff + n * 2048); } while (0)
; #define PG8_WAIT_V(n) asm volatile("s_waitcnt vmcnt(" #n ")" ::: "memory")
; #define PG8_WAIT_L(n) asm volatile("s_waitcnt lgkmcnt(" #n ")" ::: "memory")
; #define PG8_BAR __builtin_amdgcn_s_barrier()
; #define PG8_SCHED __builtin_amdgcn_sched_barrier(0)
; #define PG8_STA(bufoff, nextflag, h, koff) do { if constexpr (Sched::GATHER) { unsigned _o[2]; _o[0] = (nextflag) ? nxtA[h][0] : curA[h][0]; _o[1] = (nextflag) ? nxtA[h][1] : curA[h][1]; PG8_STAGE(bufoff, Ab + (koff), _o); } \
;         else { PG8_STAGE(bufoff, ((nextflag) ? nA : cA) + (size_t)(h) * hstep + (koff), voffA); } } while (0)
; template <class Epi, class Sched, bool ALIGN_EPI, int DT>
; __device__ __forceinline__ void gemm_phase(LAS unsigned char* lds, const int KB, const Sched& S, const Epi& E) {
;     ...
;             PG8_WAIT_V(8); PG8_WAIT_L(0); PG8_BAR; PG8_MMA(1, 0, At, B0); PG8_MMA(1, 1, At, B1); PG8_BAR; PG8_SCHED;
;             PG8_LDB(B0, 1, 0); PG8_LDB(B1, 1, 1); PG8_SCHED; PG8_LDA(At, 1, 0); PG8_STA(PG8_SA(0, 1), last, 1, k2);
;             PG8_WAIT_V(8); PG8_WAIT_L(0); PG8_BAR; PG8_MMA(0, 0, At, B0); PG8_MMA(0, 1, At, B1); PG8_BAR; PG8_SCHED;
	s_setprio 1
	s_waitcnt lgkmcnt(0)
	v_mfma_i32_16x16x64_i8 v[62:65], v[152:155], v[196:199], v[62:65]
	v_mfma_i32_16x16x64_i8 v[58:61], v[160:163], v[196:199], v[58:61]
	v_mfma_i32_16x16x64_i8 v[46:49], v[152:155], v[204:207], v[46:49]
	v_mfma_i32_16x16x64_i8 v[42:45], v[160:163], v[204:207], v[42:45]
	v_mfma_i32_16x16x64_i8 v[30:33], v[152:155], v[212:215], v[30:33]
	v_mfma_i32_16x16x64_i8 v[26:29], v[160:163], v[212:215], v[26:29]
	v_mfma_i32_16x16x64_i8 v[6:9], v[152:155], v[220:223], v[6:9]
	v_mfma_i32_16x16x64_i8 v[2:5], v[160:163], v[220:223], v[2:5]
	v_mfma_i32_16x16x64_i8 v[62:65], v[156:159], v[200:203], v[62:65]
	v_mfma_i32_16x16x64_i8 v[58:61], v[164:167], v[200:203], v[58:61]
	v_mfma_i32_16x16x64_i8 v[46:49], v[156:159], v[208:211], v[46:49]
	v_mfma_i32_16x16x64_i8 v[42:45], v[164:167], v[208:211], v[42:45]
	v_mfma_i32_16x16x64_i8 v[30:33], v[156:159], v[216:219], v[30:33]
	v_mfma_i32_16x16x64_i8 v[26:29], v[164:167], v[216:219], v[26:29]
	v_mfma_i32_16x16x64_i8 v[6:9], v[156:159], v[224:227], v[6:9]
	v_mfma_i32_16x16x64_i8 v[2:5], v[164:167], v[224:227], v[2:5]
	s_setprio 0
	s_setprio 1
	v_mfma_i32_16x16x64_i8 v[54:57], v[168:171], v[196:199], v[54:57]
	v_mfma_i32_16x16x64_i8 v[50:53], v[186:189], v[196:199], v[50:53]
	v_mfma_i32_16x16x64_i8 v[38:41], v[168:171], v[204:207], v[38:41]
	v_mfma_i32_16x16x64_i8 v[34:37], v[186:189], v[204:207], v[34:37]
	v_mfma_i32_16x16x64_i8 v[14:17], v[168:171], v[212:215], v[14:17]
	v_mfma_i32_16x16x64_i8 v[10:13], v[186:189], v[212:215], v[10:13]
	v_mfma_i32_16x16x64_i8 v[22:25], v[168:171], v[220:223], v[22:25]
	v_mfma_i32_16x16x64_i8 v[18:21], v[186:189], v[220:223], v[18:21]
	v_mfma_i32_16x16x64_i8 v[54:57], v[182:185], v[200:203], v[54:57]
	v_mfma_i32_16x16x64_i8 v[50:53], v[190:193], v[200:203], v[50:53]
	v_mfma_i32_16x16x64_i8 v[38:41], v[182:185], v[208:211], v[38:41]
	v_mfma_i32_16x16x64_i8 v[34:37], v[190:193], v[208:211], v[34:37]
	v_mfma_i32_16x16x64_i8 v[14:17], v[182:185], v[216:219], v[14:17]
	v_mfma_i32_16x16x64_i8 v[10:13], v[190:193], v[216:219], v[10:13]
	v_mfma_i32_16x16x64_i8 v[22:25], v[182:185], v[224:227], v[22:25]
	v_mfma_i32_16x16x64_i8 v[18:21], v[190:193], v[224:227], v[18:21]
	s_setprio 0
	s_barrier
	s_add_i32 s42, 0, 0x18000
	v_add_u32_e32 v1, s42, v173
	s_add_i32 s43, 0, 0x1c000
	ds_read_b128 v[152:155], v1
	ds_read_b128 v[156:159], v1 offset:1024
	ds_read_b128 v[160:163], v1 offset:2048
	ds_read_b128 v[164:167], v1 offset:3072
	v_add_u32_e32 v1, s43, v173
	ds_read_b128 v[168:171], v1
	ds_read_b128 v[182:185], v1 offset:1024
	ds_read_b128 v[186:189], v1 offset:2048
	ds_read_b128 v[190:193], v1 offset:3072
	s_add_u32 s36, s36, 0x40000
	s_addc_u32 s37, s37, 0
	s_mov_b32 m0, s47
	v_lshl_add_u64 v[236:237], s[36:37], 0, v[136:137]
	ds_read_b128 v[196:199], v177 offset:32768
	ds_read_b128 v[200:203], v177 offset:33792
	ds_read_b128 v[204:207], v177 offset:34816
	ds_read_b128 v[208:211], v177 offset:35840
	ds_read_b128 v[212:215], v177 offset:36864
	ds_read_b128 v[216:219], v177 offset:37888
	ds_read_b128 v[220:223], v177 offset:38912
	ds_read_b128 v[224:227], v177 offset:39936
	global_load_lds_dwordx4 v[236:237], off
	v_lshl_add_u64 v[236:237], s[36:37], 0, v[138:139]
	s_mov_b32 m0, s49
	s_nop 0
	global_load_lds_dwordx4 v[236:237], off
	s_nop 0
	s_waitcnt vmcnt(8)
	s_waitcnt lgkmcnt(0)
	s_barrier
	s_setprio 1
	s_waitcnt lgkmcnt(0)
	v_mfma_i32_16x16x64_i8 v[126:129], v[152:155], v[196:199], v[126:129]
	v_mfma_i32_16x16x64_i8 v[122:125], v[160:163], v[196:199], v[122:125]
	v_mfma_i32_16x16x64_i8 v[110:113], v[152:155], v[204:207], v[110:113]
	v_mfma_i32_16x16x64_i8 v[106:109], v[160:163], v[204:207], v[106:109]
	v_mfma_i32_16x16x64_i8 v[94:97], v[152:155], v[212:215], v[94:97]
	v_mfma_i32_16x16x64_i8 v[90:93], v[160:163], v[212:215], v[90:93]
	v_mfma_i32_16x16x64_i8 v[78:81], v[152:155], v[220:223], v[78:81]
	v_mfma_i32_16x16x64_i8 v[74:77], v[160:163], v[220:223], v[74:77]
	v_mfma_i32_16x16x64_i8 v[126:129], v[156:159], v[200:203], v[126:129]
	v_mfma_i32_16x16x64_i8 v[122:125], v[164:167], v[200:203], v[122:125]
	v_mfma_i32_16x16x64_i8 v[110:113], v[156:159], v[208:211], v[110:113]
	v_mfma_i32_16x16x64_i8 v[106:109], v[164:167], v[208:211], v[106:109]
	v_mfma_i32_16x16x64_i8 v[94:97], v[156:159], v[216:219], v[94:97]
	v_mfma_i32_16x16x64_i8 v[90:93], v[164:167], v[216:219], v[90:93]
	v_mfma_i32_16x16x64_i8 v[78:81], v[156:159], v[224:227], v[78:81]
	v_mfma_i32_16x16x64_i8 v[74:77], v[164:167], v[224:227], v[74:77]
	s_setprio 0
	s_setprio 1
	v_mfma_i32_16x16x64_i8 v[118:121], v[168:171], v[196:199], v[118:121]
	v_mfma_i32_16x16x64_i8 v[114:117], v[186:189], v[196:199], v[114:117]
	v_mfma_i32_16x16x64_i8 v[102:105], v[168:171], v[204:207], v[102:105]
	v_mfma_i32_16x16x64_i8 v[98:101], v[186:189], v[204:207], v[98:101]
	v_mfma_i32_16x16x64_i8 v[86:89], v[168:171], v[212:215], v[86:89]
	v_mfma_i32_16x16x64_i8 v[82:85], v[186:189], v[212:215], v[82:85]
	v_mfma_i32_16x16x64_i8 v[70:73], v[168:171], v[220:223], v[70:73]
	v_mfma_i32_16x16x64_i8 v[66:69], v[186:189], v[220:223], v[66:69]
	v_mfma_i32_16x16x64_i8 v[118:121], v[182:185], v[200:203], v[118:121]
	v_mfma_i32_16x16x64_i8 v[114:117], v[190:193], v[200:203], v[114:117]
	v_mfma_i32_16x16x64_i8 v[102:105], v[182:185], v[208:211], v[102:105]
	v_mfma_i32_16x16x64_i8 v[98:101], v[190:193], v[208:211], v[98:101]
	v_mfma_i32_16x16x64_i8 v[86:89], v[182:185], v[216:219], v[86:89]
	v_mfma_i32_16x16x64_i8 v[82:85], v[190:193], v[216:219], v[82:85]
	v_mfma_i32_16x16x64_i8 v[70:73], v[182:185], v[224:227], v[70:73]
	v_mfma_i32_16x16x64_i8 v[66:69], v[190:193], v[224:227], v[66:69]
	s_setprio 0
	s_barrier
; #define PG8_STAGE(bufoff, gbase, voff) do { _Pragma("unroll") for (int _i = 0; _i < 2; ++_i) \
;         __builtin_amdgcn_global_load_lds((const unsigned*)((const char*)(gbase) + (voff)[_i]), (LAS unsigned*)(lds + (bufoff) + ldsw + _i * 8192), 16, 0, 0); } while (0)
; #define PG8_LDA(dst, b, h) do { _Pragma("unroll") for (int m = 0; m < 4; ++m) dst[m] = PG8_LD32(lds + PG8_SA(b, h) + aoff + m * 2048); } while (0)
; #define PG8_WAIT_V(n) asm volatile("s_waitcnt vmcnt(" #n ")" ::: "memory")
; #define PG8_WAIT_L(n) asm volatile("s_waitcnt lgkmcnt(" #n ")" ::: "memory")
; #define PG8_BAR __builtin_amdgcn_s_barrier()
; #define PG8_SCHED __builtin_amdgcn_sched_barrier(0)
; #define PG8_STA(bufoff, nextflag, h, koff) do { if constexpr (Sched::GATHER) { unsigned _o[2]; _o[0] = (nextflag) ? nxtA[h][0] : curA[h][0]; _o[1] = (nextflag) ? nxtA[h][1] : curA[h][1]; PG8_STAGE(bufoff, Ab + (koff), _o); } \
;         else { PG8_STAGE(bufoff, ((nextflag) ? nA : cA) + (size_t)(h) * hstep + (koff), voffA); } } while (0)
; template <class Epi, class Sched, bool ALIGN_EPI, int DT>
; __device__ __forceinline__ void gemm_phase(LAS unsigned char* lds, const int KB, const Sched& S, const Epi& E) {
;     ...
;             PG8_LDA(At, 1, 1); PG8_STAGE(PG8_SB(1, 0), b3, voffB); PG8_STAGE(PG8_SB(1, 1), b3 + hstep, voffB); PG8_STA(PG8_SA(1, 0), last, 0, k3);
;             PG8_WAIT_V(8); PG8_WAIT_L(0); PG8_BAR; PG8_MMA(1, 0, At, B0); PG8_MMA(1, 1, At, B1); PG8_BAR; PG8_SCHED;
;         }
;         if constexpr (ALIGN_EPI) { if (wr == 0) PG8_BAR; }
	s_add_i32 s36, s42, s5
	v_lshl_add_u64 v[228:229], v[228:229], 0, s[18:19]
	s_mov_b32 m0, s36
	ds_read_b128 v[196:199], v177 offset:49152
	ds_read_b128 v[200:203], v177 offset:50176
	ds_read_b128 v[204:207], v177 offset:51200
	ds_read_b128 v[208:211], v177 offset:52224
	ds_read_b128 v[212:215], v177 offset:53248
	ds_read_b128 v[216:219], v177 offset:54272
	ds_read_b128 v[220:223], v177 offset:55296
	ds_read_b128 v[224:227], v177 offset:56320
	global_load_lds_dwordx4 v[228:229], off
	s_add_i32 m0, s36, 0x2000
	s_add_u32 s36, s40, 0x40080
	v_lshl_add_u64 v[228:229], v[230:231], 0, s[18:19]
	s_addc_u32 s37, s41, 0
	s_add_i32 s40, s43, s5
	global_load_lds_dwordx4 v[228:229], off
	v_lshl_add_u64 v[228:229], s[36:37], 0, v[134:135]
	s_mov_b32 m0, s40
	s_nop 0
	global_load_lds_dwordx4 v[228:229], off
	v_lshl_add_u64 v[228:229], s[36:37], 0, v[132:133]
	s_add_i32 m0, s40, 0x2000
	s_nop 0
	global_load_lds_dwordx4 v[228:229], off
	v_lshl_add_u64 v[228:229], v[232:233], 0, s[18:19]
	s_mov_b32 m0, s55
	s_nop 0
	global_load_lds_dwordx4 v[228:229], off
	v_lshl_add_u64 v[228:229], v[234:235], 0, s[18:19]
	s_mov_b32 m0, s56
	s_nop 0
	global_load_lds_dwordx4 v[228:229], off
	s_waitcnt vmcnt(8)
	s_waitcnt lgkmcnt(0)
	s_barrier
	s_setprio 1
	s_waitcnt lgkmcnt(0)
	v_mfma_i32_16x16x64_i8 v[62:65], v[152:155], v[196:199], v[62:65]
	v_mfma_i32_16x16x64_i8 v[58:61], v[160:163], v[196:199], v[58:61]
	v_mfma_i32_16x16x64_i8 v[46:49], v[152:155], v[204:207], v[46:49]
	v_mfma_i32_16x16x64_i8 v[42:45], v[160:163], v[204:207], v[42:45]
	v_mfma_i32_16x16x64_i8 v[30:33], v[152:155], v[212:215], v[30:33]
	v_mfma_i32_16x16x64_i8 v[26:29], v[160:163], v[212:215], v[26:29]
	v_mfma_i32_16x16x64_i8 v[6:9], v[152:155], v[220:223], v[6:9]
	v_mfma_i32_16x16x64_i8 v[2:5], v[160:163], v[220:223], v[2:5]
	v_mfma_i32_16x16x64_i8 v[62:65], v[156:159], v[200:203], v[62:65]
	v_mfma_i32_16x16x64_i8 v[58:61], v[164:167], v[200:203], v[58:61]
	v_mfma_i32_16x16x64_i8 v[46:49], v[156:159], v[208:211], v[46:49]
	v_mfma_i32_16x16x64_i8 v[42:45], v[164:167], v[208:211], v[42:45]
	v_mfma_i32_16x16x64_i8 v[30:33], v[156:159], v[216:219], v[30:33]
	v_mfma_i32_16x16x64_i8 v[26:29], v[164:167], v[216:219], v[26:29]
	v_mfma_i32_16x16x64_i8 v[6:9], v[156:159], v[224:227], v[6:9]
	v_mfma_i32_16x16x64_i8 v[2:5], v[164:167], v[224:227], v[2:5]
	s_setprio 0
	s_setprio 1
	v_mfma_i32_16x16x64_i8 v[54:57], v[168:171], v[196:199], v[54:57]
	v_mfma_i32_16x16x64_i8 v[50:53], v[186:189], v[196:199], v[50:53]
	v_mfma_i32_16x16x64_i8 v[38:41], v[168:171], v[204:207], v[38:41]
	v_mfma_i32_16x16x64_i8 v[34:37], v[186:189], v[204:207], v[34:37]
	v_mfma_i32_16x16x64_i8 v[14:17], v[168:171], v[212:215], v[14:17]
	v_mfma_i32_16x16x64_i8 v[10:13], v[186:189], v[212:215], v[10:13]
	v_mfma_i32_16x16x64_i8 v[22:25], v[168:171], v[220:223], v[22:25]
	v_mfma_i32_16x16x64_i8 v[18:21], v[186:189], v[220:223], v[18:21]
	v_mfma_i32_16x16x64_i8 v[54:57], v[182:185], v[200:203], v[54:57]
	v_mfma_i32_16x16x64_i8 v[50:53], v[190:193], v[200:203], v[50:53]
	v_mfma_i32_16x16x64_i8 v[38:41], v[182:185], v[208:211], v[38:41]
	v_mfma_i32_16x16x64_i8 v[34:37], v[190:193], v[208:211], v[34:37]
	v_mfma_i32_16x16x64_i8 v[14:17], v[182:185], v[216:219], v[14:17]
	v_mfma_i32_16x16x64_i8 v[10:13], v[190:193], v[216:219], v[10:13]
	v_mfma_i32_16x16x64_i8 v[22:25], v[182:185], v[224:227], v[22:25]
	v_mfma_i32_16x16x64_i8 v[18:21], v[190:193], v[224:227], v[18:21]
	s_setprio 0
	s_barrier
	s_add_i32 s67, s67, 2
	s_cmp_gt_u32 s67, 13
	s_mov_b64 s[36:37], s[38:39]
	s_cbranch_scc0 .LBB0_193
	s_and_b64 vcc, exec, s[20:21]
	s_cbranch_vccz .LBB0_196
	s_barrier

; #define PG8_STAGE(bufoff, gbase, voff) do { _Pragma("unroll") for (int _i = 0; _i < 2; ++_i) \
;         __builtin_amdgcn_global_load_lds((const unsigned*)((const char*)(gbase) + (voff)[_i]), (LAS unsigned*)(lds + (bufoff) + ldsw + _i * 8192), 16, 0, 0); } while (0)
; #define PG8_LDA(dst, b, h) do { _Pragma("unroll") for (int m = 0; m < 4; ++m) dst[m] = PG8_LD32(lds + PG8_SA(b, h) + aoff + m * 2048); } while (0)
; #define PG8_LDB(dst, b, h) do { _Pragma("unroll") for (int n = 0; n < 2; ++n) dst[n] = PG8_LD32(lds + PG8_SB(b, h) + boff + n * 2048); } while (0)
; #define PG8_WAIT_V(n) asm volatile("s_waitcnt vmcnt(" #n ")" ::: "memory")
; #define PG8_WAIT_L(n) asm volatile("s_waitcnt lgkmcnt(" #n ")" ::: "memory")
; #define PG8_BAR __builtin_amdgcn_s_barrier()
; #define PG8_SCHED __builtin_amdgcn_sched_barrier(0)
; #define PG8_STA(bufoff, nextflag, h, koff) do { if constexpr (Sched::GATHER) { unsigned _o[2]; _o[0] = (nextflag) ? nxtA[h][0] : curA[h][0]; _o[1] = (nextflag) ? nxtA[h][1] : curA[h][1]; PG8_STAGE(bufoff, Ab + (koff), _o); } \
;         else { PG8_STAGE(bufoff, ((nextflag) ? nA : cA) + (size_t)(h) * hstep + (koff), voffA); } } while (0)
; template <class Epi, class Sched, bool ALIGN_EPI, int DT>
; __device__ __forceinline__ void gemm_phase(LAS unsigned char* lds, const int KB, const Sched& S, const Epi& E) {
;     ...
;         for (int t = 0; t < nt; t += 2) {
;             const bool last = (t == nt - 2);
;             const size_t k1 = (size_t)(t + 1) * kstep, k2 = last ? 0 : (size_t)(t + 2) * kstep, k3 = k2 + kstep;
;             const char* b2 = last ? nB : cB + (size_t)(t + 2) * kstep; const char* b3 = b2 + kstep;
;             PG8_LDB(B0, 0, 0); PG8_LDB(B1, 0, 1); PG8_SCHED; PG8_LDA(At, 0, 0); PG8_STA(PG8_SA(1, 1), false, 1, k1);
;             PG8_WAIT_V(8); PG8_WAIT_L(0); PG8_BAR; PG8_MMA(0, 0, At, B0); PG8_MMA(0, 1, At, B1); PG8_BAR; PG8_SCHED;
;             PG8_LDA(At, 0, 1); PG8_STAGE(PG8_SB(0, 0), b2, voffB); PG8_STAGE(PG8_SB(0, 1), b2 + hstep, voffB); PG8_STA(PG8_SA(0, 0), last, 0, k2);
;             PG8_WAIT_V(8); PG8_WAIT_L(0); PG8_BAR; PG8_MMA(1, 0, At, B0); PG8_MMA(1, 1, At, B1); PG8_BAR; PG8_SCHED;
.LBB0_1018:
	ds_read_b128 v[18:21], v193
	ds_read_b128 v[22:25], v193 offset:1024
	ds_read_b128 v[26:29], v193 offset:2048
	ds_read_b128 v[30:33], v193 offset:3072
	ds_read_b128 v[2:5], v195
	ds_read_b128 v[6:9], v195 offset:1024
	ds_read_b128 v[10:13], v195 offset:2048
	ds_read_b128 v[14:17], v195 offset:3072
	s_add_u32 s34, s38, 0x100
	s_addc_u32 s35, s39, 0
	s_add_u32 s68, s63, s38
	s_addc_u32 s69, s66, s39
	s_cmp_eq_u32 s67, 12
	s_cselect_b64 s[40:41], -1, 0
	s_and_b64 s[36:37], s[40:41], exec
	s_cselect_b32 s37, s21, s69
	s_cselect_b32 s36, s23, s68
	s_cselect_b32 s68, 0, s35
	s_cselect_b32 s69, 0, s34
	v_lshl_add_u64 v[222:223], v[178:179], 0, s[38:39]
	s_add_i32 m0, s29, 0xc000
	ds_read_b128 v[182:185], v196
	ds_read_b128 v[186:189], v196 offset:1024
	ds_read_b128 v[198:201], v196 offset:2048
	ds_read_b128 v[202:205], v196 offset:3072
	ds_read_b128 v[206:209], v196 offset:4096
	ds_read_b128 v[210:213], v196 offset:5120
	ds_read_b128 v[214:217], v196 offset:6144
	ds_read_b128 v[218:221], v196 offset:7168
	global_load_lds_dwordx4 v[222:223], off
	v_lshl_add_u64 v[222:223], v[180:181], 0, s[38:39]
	s_add_i32 m0, s29, 0xe000
	s_nop 0
	global_load_lds_dwordx4 v[222:223], off
	s_waitcnt vmcnt(8)
	s_waitcnt lgkmcnt(0)
	s_barrier
	s_setprio 1
	s_waitcnt lgkmcnt(0)
	v_mfma_scale_f32_16x16x128_f8f6f4 v[158:161], v[18:25], v[182:189], v[158:161], v190, v190 op_sel_hi:[0,0,0]
	v_mfma_scale_f32_16x16x128_f8f6f4 v[154:157], v[26:33], v[182:189], v[154:157], v190, v190 op_sel_hi:[0,0,0]
	v_mfma_scale_f32_16x16x128_f8f6f4 v[150:153], v[18:25], v[198:205], v[150:153], v190, v190 op_sel_hi:[0,0,0]
	v_mfma_scale_f32_16x16x128_f8f6f4 v[142:145], v[26:33], v[198:205], v[142:145], v190, v190 op_sel_hi:[0,0,0]
	v_mfma_scale_f32_16x16x128_f8f6f4 v[134:137], v[18:25], v[206:213], v[134:137], v190, v190 op_sel_hi:[0,0,0]
	v_mfma_scale_f32_16x16x128_f8f6f4 v[126:129], v[26:33], v[206:213], v[126:129], v190, v190 op_sel_hi:[0,0,0]
	v_mfma_scale_f32_16x16x128_f8f6f4 v[118:121], v[18:25], v[214:221], v[118:121], v190, v190 op_sel_hi:[0,0,0]
	v_mfma_scale_f32_16x16x128_f8f6f4 v[110:113], v[26:33], v[214:221], v[110:113], v190, v190 op_sel_hi:[0,0,0]
	s_setprio 0
	s_setprio 1
	v_mfma_scale_f32_16x16x128_f8f6f4 v[146:149], v[2:9], v[182:189], v[146:149], v190, v190 op_sel_hi:[0,0,0]
	v_mfma_scale_f32_16x16x128_f8f6f4 v[138:141], v[10:17], v[182:189], v[138:141], v190, v190 op_sel_hi:[0,0,0]
	v_mfma_scale_f32_16x16x128_f8f6f4 v[130:133], v[2:9], v[198:205], v[130:133], v190, v190 op_sel_hi:[0,0,0]
	v_mfma_scale_f32_16x16x128_f8f6f4 v[122:125], v[10:17], v[198:205], v[122:125], v190, v190 op_sel_hi:[0,0,0]
	v_mfma_scale_f32_16x16x128_f8f6f4 v[114:117], v[2:9], v[206:213], v[114:117], v190, v190 op_sel_hi:[0,0,0]
	v_mfma_scale_f32_16x16x128_f8f6f4 v[106:109], v[10:17], v[206:213], v[106:109], v190, v190 op_sel_hi:[0,0,0]
	v_mfma_scale_f32_16x16x128_f8f6f4 v[102:105], v[2:9], v[214:221], v[102:105], v190, v190 op_sel_hi:[0,0,0]
	v_mfma_scale_f32_16x16x128_f8f6f4 v[98:101], v[10:17], v[214:221], v[98:101], v190, v190 op_sel_hi:[0,0,0]
	s_setprio 0
	s_barrier
	s_add_i32 s38, s53, s42
	v_lshl_add_u64 v[182:183], s[36:37], 0, v[162:163]
	s_mov_b32 m0, s38
	ds_read_b128 v[198:201], v196 offset:16384
	ds_read_b128 v[202:205], v196 offset:17408
	ds_read_b128 v[206:209], v196 offset:18432
	ds_read_b128 v[210:213], v196 offset:19456
	ds_read_b128 v[214:217], v196 offset:20480
	ds_read_b128 v[218:221], v196 offset:21504
	ds_read_b128 v[222:225], v196 offset:22528
	ds_read_b128 v[226:229], v196 offset:23552
	global_load_lds_dwordx4 v[182:183], off
	s_add_i32 m0, s38, 0x2000
	s_add_u32 s38, s36, 0x40000
	v_lshl_add_u64 v[184:185], s[36:37], 0, v[164:165]
	s_addc_u32 s39, s37, 0
	s_add_i32 s70, s54, s42
	global_load_lds_dwordx4 v[184:185], off
	v_lshl_add_u64 v[186:187], s[38:39], 0, v[162:163]
	s_mov_b32 m0, s70
	s_nop 0
	global_load_lds_dwordx4 v[186:187], off
	v_lshl_add_u64 v[186:187], s[38:39], 0, v[164:165]
	s_add_i32 m0, s70, 0x2000
	s_and_b64 s[38:39], s[6:7], s[40:41]
	s_and_b64 s[38:39], s[38:39], exec
	s_cselect_b32 s38, s24, s30
	s_cselect_b32 s39, s25, s31
	s_add_u32 s38, s38, s69
	s_addc_u32 s39, s39, s68
	global_load_lds_dwordx4 v[186:187], off
	v_lshl_add_u64 v[186:187], s[38:39], 0, v[166:167]
	s_mov_b32 m0, s29
	v_lshl_add_u64 v[188:189], s[38:39], 0, v[168:169]
	global_load_lds_dwordx4 v[186:187], off
	s_mov_b32 m0, s43
	s_nop 0
	global_load_lds_dwordx4 v[188:189], off
	s_waitcnt vmcnt(8)
	s_waitcnt lgkmcnt(0)
	s_barrier
	s_setprio 1
	s_waitcnt lgkmcnt(0)
	v_mfma_scale_f32_16x16x128_f8f6f4 v[94:97], v[18:25], v[198:205], v[94:97], v190, v190 op_sel_hi:[0,0,0]
	v_mfma_scale_f32_16x16x128_f8f6f4 v[90:93], v[26:33], v[198:205], v[90:93], v190, v190 op_sel_hi:[0,0,0]
	v_mfma_scale_f32_16x16x128_f8f6f4 v[86:89], v[18:25], v[206:213], v[86:89], v190, v190 op_sel_hi:[0,0,0]
	v_mfma_scale_f32_16x16x128_f8f6f4 v[78:81], v[26:33], v[206:213], v[78:81], v190, v190 op_sel_hi:[0,0,0]
	v_mfma_scale_f32_16x16x128_f8f6f4 v[62:65], v[18:25], v[214:221], v[62:65], v190, v190 op_sel_hi:[0,0,0]
	v_mfma_scale_f32_16x16x128_f8f6f4 v[54:57], v[26:33], v[214:221], v[54:57], v190, v190 op_sel_hi:[0,0,0]
	v_mfma_scale_f32_16x16x128_f8f6f4 v[46:49], v[18:25], v[222:229], v[46:49], v190, v190 op_sel_hi:[0,0,0]
	v_mfma_scale_f32_16x16x128_f8f6f4 v[38:41], v[26:33], v[222:229], v[38:41], v190, v190 op_sel_hi:[0,0,0]
	s_setprio 0
	s_setprio 1
	v_mfma_scale_f32_16x16x128_f8f6f4 v[82:85], v[2:9], v[198:205], v[82:85], v190, v190 op_sel_hi:[0,0,0]
	v_mfma_scale_f32_16x16x128_f8f6f4 v[74:77], v[10:17], v[198:205], v[74:77], v190, v190 op_sel_hi:[0,0,0]
	v_mfma_scale_f32_16x16x128_f8f6f4 v[58:61], v[2:9], v[206:213], v[58:61], v190, v190 op_sel_hi:[0,0,0]
	v_mfma_scale_f32_16x16x128_f8f6f4 v[50:53], v[10:17], v[206:213], v[50:53], v190, v190 op_sel_hi:[0,0,0]
	v_mfma_scale_f32_16x16x128_f8f6f4 v[42:45], v[2:9], v[214:221], v[42:45], v190, v190 op_sel_hi:[0,0,0]
	v_mfma_scale_f32_16x16x128_f8f6f4 v[34:37], v[10:17], v[214:221], v[34:37], v190, v190 op_sel_hi:[0,0,0]
	v_mfma_scale_f32_16x16x128_f8f6f4 v[70:73], v[2:9], v[222:229], v[70:73], v190, v190 op_sel_hi:[0,0,0]
	v_mfma_scale_f32_16x16x128_f8f6f4 v[66:69], v[10:17], v[222:229], v[66:69], v190, v190 op_sel_hi:[0,0,0]
	s_setprio 0
	s_barrier
; #define PG8_STAGE(bufoff, gbase, voff) do { _Pragma("unroll") for (int _i = 0; _i < 2; ++_i) \
;         __builtin_amdgcn_global_load_lds((const unsigned*)((const char*)(gbase) + (voff)[_i]), (LAS unsigned*)(lds + (bufoff) + ldsw + _i * 8192), 16, 0, 0); } while (0)
; #define PG8_LDA(dst, b, h) do { _Pragma("unroll") for (int m = 0; m < 4; ++m) dst[m] = PG8_LD32(lds + PG8_SA(b, h) + aoff + m * 2048); } while (0)
; #define PG8_LDB(dst, b, h) do { _Pragma("unroll") for (int n = 0; n < 2; ++n) dst[n] = PG8_LD32(lds + PG8_SB(b, h) + boff + n * 2048); } while (0)
; #define PG8_WAIT_V(n) asm volatile("s_waitcnt vmcnt(" #n ")" ::: "memory")
; #define PG8_WAIT_L(n) asm volatile("s_waitcnt lgkmcnt(" #n ")" ::: "memory")
; #define PG8_BAR __builtin_amdgcn_s_barrier()
; #define PG8_SCHED __builtin_amdgcn_sched_barrier(0)
; #define PG8_STA(bufoff, nextflag, h, koff) do { if constexpr (Sched::GATHER) { unsigned _o[2]; _o[0] = (nextflag) ? nxtA[h][0] : curA[h][0]; _o[1] = (nextflag) ? nxtA[h][1] : curA[h][1]; PG8_STAGE(bufoff, Ab + (koff), _o); } \
;         else { PG8_STAGE(bufoff, ((nextflag) ? nA : cA) + (size_t)(h) * hstep + (koff), voffA); } } while (0)
; template <class Epi, class Sched, bool ALIGN_EPI, int DT>
; __device__ __forceinline__ void gemm_phase(LAS unsigned char* lds, const int KB, const Sched& S, const Epi& E) {
;     ...
;             PG8_WAIT_V(8); PG8_WAIT_L(0); PG8_BAR; PG8_MMA(1, 0, At, B0); PG8_MMA(1, 1, At, B1); PG8_BAR; PG8_SCHED;
;             PG8_LDB(B0, 1, 0); PG8_LDB(B1, 1, 1); PG8_SCHED; PG8_LDA(At, 1, 0); PG8_STA(PG8_SA(0, 1), last, 1, k2);
;             PG8_WAIT_V(8); PG8_WAIT_L(0); PG8_BAR; PG8_MMA(0, 0, At, B0); PG8_MMA(0, 1, At, B1); PG8_BAR; PG8_SCHED;
;             PG8_LDA(At, 1, 1); PG8_STAGE(PG8_SB(1, 0), b3, voffB); PG8_STAGE(PG8_SB(1, 1), b3 + hstep, voffB); PG8_STA(PG8_SA(1, 0), last, 0, k3);
;             PG8_WAIT_V(8); PG8_WAIT_L(0); PG8_BAR; PG8_MMA(1, 0, At, B0); PG8_MMA(1, 1, At, B1); PG8_BAR; PG8_SCHED;
;         }
	s_add_i32 s40, 0, 0x18000
	s_add_i32 s41, 0, 0x1c000
	v_add_u32_e32 v14, s40, v191
	v_add_u32_e32 v30, s41, v191
	ds_read_b128 v[2:5], v14
	ds_read_b128 v[6:9], v14 offset:1024
	ds_read_b128 v[10:13], v14 offset:2048
	ds_read_b128 v[14:17], v14 offset:3072
	ds_read_b128 v[18:21], v30
	ds_read_b128 v[22:25], v30 offset:1024
	ds_read_b128 v[26:29], v30 offset:2048
	ds_read_b128 v[30:33], v30 offset:3072
	s_add_u32 s38, s38, 0x40000
	s_addc_u32 s39, s39, 0
	s_mov_b32 m0, s44
	v_lshl_add_u64 v[230:231], s[38:39], 0, v[166:167]
	ds_read_b128 v[198:201], v196 offset:32768
	ds_read_b128 v[202:205], v196 offset:33792
	ds_read_b128 v[206:209], v196 offset:34816
	ds_read_b128 v[210:213], v196 offset:35840
	ds_read_b128 v[214:217], v196 offset:36864
	ds_read_b128 v[218:221], v196 offset:37888
	ds_read_b128 v[222:225], v196 offset:38912
	ds_read_b128 v[226:229], v196 offset:39936
	global_load_lds_dwordx4 v[230:231], off
	v_lshl_add_u64 v[230:231], s[38:39], 0, v[168:169]
	s_mov_b32 m0, s45
	s_nop 0
	global_load_lds_dwordx4 v[230:231], off
	s_nop 0
	s_waitcnt vmcnt(8)
	s_waitcnt lgkmcnt(0)
	s_barrier
	s_setprio 1
	s_waitcnt lgkmcnt(0)
	v_mfma_scale_f32_16x16x128_f8f6f4 v[158:161], v[2:9], v[198:205], v[158:161], v190, v190 op_sel_hi:[0,0,0]
	v_mfma_scale_f32_16x16x128_f8f6f4 v[154:157], v[10:17], v[198:205], v[154:157], v190, v190 op_sel_hi:[0,0,0]
	v_mfma_scale_f32_16x16x128_f8f6f4 v[150:153], v[2:9], v[206:213], v[150:153], v190, v190 op_sel_hi:[0,0,0]
	v_mfma_scale_f32_16x16x128_f8f6f4 v[142:145], v[10:17], v[206:213], v[142:145], v190, v190 op_sel_hi:[0,0,0]
	v_mfma_scale_f32_16x16x128_f8f6f4 v[134:137], v[2:9], v[214:221], v[134:137], v190, v190 op_sel_hi:[0,0,0]
	v_mfma_scale_f32_16x16x128_f8f6f4 v[126:129], v[10:17], v[214:221], v[126:129], v190, v190 op_sel_hi:[0,0,0]
	v_mfma_scale_f32_16x16x128_f8f6f4 v[118:121], v[2:9], v[222:229], v[118:121], v190, v190 op_sel_hi:[0,0,0]
	v_mfma_scale_f32_16x16x128_f8f6f4 v[110:113], v[10:17], v[222:229], v[110:113], v190, v190 op_sel_hi:[0,0,0]
	s_setprio 0
	s_setprio 1
	v_mfma_scale_f32_16x16x128_f8f6f4 v[146:149], v[18:25], v[198:205], v[146:149], v190, v190 op_sel_hi:[0,0,0]
	v_mfma_scale_f32_16x16x128_f8f6f4 v[138:141], v[26:33], v[198:205], v[138:141], v190, v190 op_sel_hi:[0,0,0]
	v_mfma_scale_f32_16x16x128_f8f6f4 v[130:133], v[18:25], v[206:213], v[130:133], v190, v190 op_sel_hi:[0,0,0]
	v_mfma_scale_f32_16x16x128_f8f6f4 v[122:125], v[26:33], v[206:213], v[122:125], v190, v190 op_sel_hi:[0,0,0]
	v_mfma_scale_f32_16x16x128_f8f6f4 v[114:117], v[18:25], v[214:221], v[114:117], v190, v190 op_sel_hi:[0,0,0]
	v_mfma_scale_f32_16x16x128_f8f6f4 v[106:109], v[26:33], v[214:221], v[106:109], v190, v190 op_sel_hi:[0,0,0]
	v_mfma_scale_f32_16x16x128_f8f6f4 v[102:105], v[18:25], v[222:229], v[102:105], v190, v190 op_sel_hi:[0,0,0]
	v_mfma_scale_f32_16x16x128_f8f6f4 v[98:101], v[26:33], v[222:229], v[98:101], v190, v190 op_sel_hi:[0,0,0]
	s_setprio 0
	s_barrier
	s_add_i32 s38, s40, s42
	v_lshl_add_u64 v[182:183], v[182:183], 0, s[10:11]
	s_mov_b32 m0, s38
	ds_read_b128 v[198:201], v196 offset:49152
	ds_read_b128 v[202:205], v196 offset:50176
	ds_read_b128 v[206:209], v196 offset:51200
	ds_read_b128 v[210:213], v196 offset:52224
	ds_read_b128 v[214:217], v196 offset:53248
	ds_read_b128 v[218:221], v196 offset:54272
	ds_read_b128 v[222:225], v196 offset:55296
	ds_read_b128 v[226:229], v196 offset:56320
	global_load_lds_dwordx4 v[182:183], off
	s_add_i32 m0, s38, 0x2000
	s_add_u32 s36, s36, 0x40080
	v_lshl_add_u64 v[182:183], v[184:185], 0, s[10:11]
	s_addc_u32 s37, s37, 0
	s_add_i32 s38, s41, s42
	global_load_lds_dwordx4 v[182:183], off
	v_lshl_add_u64 v[182:183], s[36:37], 0, v[162:163]
	s_mov_b32 m0, s38
	s_nop 0
	global_load_lds_dwordx4 v[182:183], off
	v_lshl_add_u64 v[182:183], s[36:37], 0, v[164:165]
	s_add_i32 m0, s38, 0x2000
	s_nop 0
	global_load_lds_dwordx4 v[182:183], off
	v_lshl_add_u64 v[182:183], v[186:187], 0, s[10:11]
	s_mov_b32 m0, s47
	s_nop 0
	global_load_lds_dwordx4 v[182:183], off
	v_lshl_add_u64 v[182:183], v[188:189], 0, s[10:11]
	s_mov_b32 m0, s49
	s_nop 0
	global_load_lds_dwordx4 v[182:183], off
	s_waitcnt vmcnt(8)
	s_waitcnt lgkmcnt(0)
	s_barrier
	s_setprio 1
	s_waitcnt lgkmcnt(0)
	v_mfma_scale_f32_16x16x128_f8f6f4 v[94:97], v[2:9], v[198:205], v[94:97], v190, v190 op_sel_hi:[0,0,0]
	v_mfma_scale_f32_16x16x128_f8f6f4 v[90:93], v[10:17], v[198:205], v[90:93], v190, v190 op_sel_hi:[0,0,0]
	v_mfma_scale_f32_16x16x128_f8f6f4 v[86:89], v[2:9], v[206:213], v[86:89], v190, v190 op_sel_hi:[0,0,0]
	v_mfma_scale_f32_16x16x128_f8f6f4 v[78:81], v[10:17], v[206:213], v[78:81], v190, v190 op_sel_hi:[0,0,0]
	v_mfma_scale_f32_16x16x128_f8f6f4 v[62:65], v[2:9], v[214:221], v[62:65], v190, v190 op_sel_hi:[0,0,0]
	v_mfma_scale_f32_16x16x128_f8f6f4 v[54:57], v[10:17], v[214:221], v[54:57], v190, v190 op_sel_hi:[0,0,0]
	v_mfma_scale_f32_16x16x128_f8f6f4 v[46:49], v[2:9], v[222:229], v[46:49], v190, v190 op_sel_hi:[0,0,0]
	v_mfma_scale_f32_16x16x128_f8f6f4 v[38:41], v[10:17], v[222:229], v[38:41], v190, v190 op_sel_hi:[0,0,0]
	s_setprio 0
	s_setprio 1
	v_mfma_scale_f32_16x16x128_f8f6f4 v[82:85], v[18:25], v[198:205], v[82:85], v190, v190 op_sel_hi:[0,0,0]
	v_mfma_scale_f32_16x16x128_f8f6f4 v[74:77], v[26:33], v[198:205], v[74:77], v190, v190 op_sel_hi:[0,0,0]
	v_mfma_scale_f32_16x16x128_f8f6f4 v[58:61], v[18:25], v[206:213], v[58:61], v190, v190 op_sel_hi:[0,0,0]
	v_mfma_scale_f32_16x16x128_f8f6f4 v[50:53], v[26:33], v[206:213], v[50:53], v190, v190 op_sel_hi:[0,0,0]
	v_mfma_scale_f32_16x16x128_f8f6f4 v[42:45], v[18:25], v[214:221], v[42:45], v190, v190 op_sel_hi:[0,0,0]
	v_mfma_scale_f32_16x16x128_f8f6f4 v[34:37], v[26:33], v[214:221], v[34:37], v190, v190 op_sel_hi:[0,0,0]
	v_mfma_scale_f32_16x16x128_f8f6f4 v[70:73], v[18:25], v[222:229], v[70:73], v190, v190 op_sel_hi:[0,0,0]
	v_mfma_scale_f32_16x16x128_f8f6f4 v[66:69], v[26:33], v[222:229], v[66:69], v190, v190 op_sel_hi:[0,0,0]
	s_setprio 0
	s_barrier
	s_add_i32 s67, s67, 2
	s_cmp_gt_u32 s67, 13
	s_mov_b64 s[38:39], s[34:35]
	s_cbranch_scc0 .LBB0_1018
	s_and_b64 vcc, exec, s[12:13]
	s_cbranch_vccz .LBB0_1021
	s_barrier

; #define PG8_STAGE(bufoff, gbase, voff) do { _Pragma("unroll") for (int _i = 0; _i < 2; ++_i) \
;         __builtin_amdgcn_global_load_lds((const unsigned*)((const char*)(gbase) + (voff)[_i]), (LAS unsigned*)(lds + (bufoff) + ldsw + _i * 8192), 16, 0, 0); } while (0)
; #define PG8_LDA(dst, b, h) do { _Pragma("unroll") for (int m = 0; m < 4; ++m) dst[m] = PG8_LD32(lds + PG8_SA(b, h) + aoff + m * 2048); } while (0)
; #define PG8_LDB(dst, b, h) do { _Pragma("unroll") for (int n = 0; n < 2; ++n) dst[n] = PG8_LD32(lds + PG8_SB(b, h) + boff + n * 2048); } while (0)
; #define PG8_WAIT_V(n) asm volatile("s_waitcnt vmcnt(" #n ")" ::: "memory")
; #define PG8_WAIT_L(n) asm volatile("s_waitcnt lgkmcnt(" #n ")" ::: "memory")
; #define PG8_BAR __builtin_amdgcn_s_barrier()
; #define PG8_SCHED __builtin_amdgcn_sched_barrier(0)
; #define PG8_STA(bufoff, nextflag, h, koff) do { if constexpr (Sched::GATHER) { unsigned _o[2]; _o[0] = (nextflag) ? nxtA[h][0] : curA[h][0]; _o[1] = (nextflag) ? nxtA[h][1] : curA[h][1]; PG8_STAGE(bufoff, Ab + (koff), _o); } \
;         else { PG8_STAGE(bufoff, ((nextflag) ? nA : cA) + (size_t)(h) * hstep + (koff), voffA); } } while (0)
; template <class Epi, class Sched, bool ALIGN_EPI, int DT>
; __device__ __forceinline__ void gemm_phase(LAS unsigned char* lds, const int KB, const Sched& S, const Epi& E) {
;     ...
;         for (int t = 0; t < nt; t += 2) {
;             const bool last = (t == nt - 2);
;             const size_t k1 = (size_t)(t + 1) * kstep, k2 = last ? 0 : (size_t)(t + 2) * kstep, k3 = k2 + kstep;
;             const char* b2 = last ? nB : cB + (size_t)(t + 2) * kstep; const char* b3 = b2 + kstep;
;             PG8_LDB(B0, 0, 0); PG8_LDB(B1, 0, 1); PG8_SCHED; PG8_LDA(At, 0, 0); PG8_STA(PG8_SA(1, 1), false, 1, k1);
;             PG8_WAIT_V(8); PG8_WAIT_L(0); PG8_BAR; PG8_MMA(0, 0, At, B0); PG8_MMA(0, 1, At, B1); PG8_BAR; PG8_SCHED;
;             PG8_LDA(At, 0, 1); PG8_STAGE(PG8_SB(0, 0), b2, voffB); PG8_STAGE(PG8_SB(0, 1), b2 + hstep, voffB); PG8_STA(PG8_SA(0, 0), last, 0, k2);
;             PG8_WAIT_V(8); PG8_WAIT_L(0); PG8_BAR; PG8_MMA(1, 0, At, B0); PG8_MMA(1, 1, At, B1); PG8_BAR; PG8_SCHED;
.LBB0_1154:
	ds_read_b128 v[70:73], v167
	ds_read_b128 v[156:159], v167 offset:1024
	ds_read_b128 v[160:163], v167 offset:2048
	ds_read_b128 v[172:175], v167 offset:3072
	ds_read_b128 v[176:179], v168
	ds_read_b128 v[180:183], v168 offset:1024
	ds_read_b128 v[184:187], v168 offset:2048
	ds_read_b128 v[188:191], v168 offset:3072
	s_add_u32 s30, s28, 0x100
	s_addc_u32 s31, s29, 0
	s_add_u32 s63, s56, s28
	s_addc_u32 s66, s57, s29
	s_cmp_eq_u32 s62, 12
	s_cselect_b64 s[36:37], -1, 0
	s_and_b64 s[34:35], s[36:37], exec
	s_cselect_b32 s67, 0, s30
	s_cselect_b32 s35, s17, s66
	s_cselect_b32 s34, s19, s63
	v_lshl_add_u64 v[192:193], v[66:67], 0, s[28:29]
	s_add_i32 m0, s25, 0xc000
	ds_read_b128 v[196:199], v169
	ds_read_b128 v[200:203], v169 offset:1024
	ds_read_b128 v[204:207], v169 offset:2048
	ds_read_b128 v[208:211], v169 offset:3072
	ds_read_b128 v[212:215], v169 offset:4096
	ds_read_b128 v[216:219], v169 offset:5120
	ds_read_b128 v[220:223], v169 offset:6144
	ds_read_b128 v[224:227], v169 offset:7168
	global_load_lds_dwordx4 v[192:193], off
	v_lshl_add_u64 v[192:193], v[68:69], 0, s[28:29]
	s_add_i32 m0, s25, 0xe000
	s_nop 0
	global_load_lds_dwordx4 v[192:193], off
	s_waitcnt vmcnt(8)
	s_waitcnt lgkmcnt(0)
	s_barrier
	s_setprio 1
	s_waitcnt lgkmcnt(0)
	v_mfma_i32_16x16x64_i8 v[134:137], v[70:73], v[196:199], v[134:137]
	v_mfma_i32_16x16x64_i8 v[126:129], v[160:163], v[196:199], v[126:129]
	v_mfma_i32_16x16x64_i8 v[118:121], v[70:73], v[204:207], v[118:121]
	v_mfma_i32_16x16x64_i8 v[110:113], v[160:163], v[204:207], v[110:113]
	v_mfma_i32_16x16x64_i8 v[102:105], v[70:73], v[212:215], v[102:105]
	v_mfma_i32_16x16x64_i8 v[94:97], v[160:163], v[212:215], v[94:97]
	v_mfma_i32_16x16x64_i8 v[86:89], v[70:73], v[220:223], v[86:89]
	v_mfma_i32_16x16x64_i8 v[78:81], v[160:163], v[220:223], v[78:81]
	v_mfma_i32_16x16x64_i8 v[134:137], v[156:159], v[200:203], v[134:137]
	v_mfma_i32_16x16x64_i8 v[126:129], v[172:175], v[200:203], v[126:129]
	v_mfma_i32_16x16x64_i8 v[118:121], v[156:159], v[208:211], v[118:121]
	v_mfma_i32_16x16x64_i8 v[110:113], v[172:175], v[208:211], v[110:113]
	v_mfma_i32_16x16x64_i8 v[102:105], v[156:159], v[216:219], v[102:105]
	v_mfma_i32_16x16x64_i8 v[94:97], v[172:175], v[216:219], v[94:97]
	v_mfma_i32_16x16x64_i8 v[86:89], v[156:159], v[224:227], v[86:89]
	v_mfma_i32_16x16x64_i8 v[78:81], v[172:175], v[224:227], v[78:81]
	s_setprio 0
	s_setprio 1
	v_mfma_i32_16x16x64_i8 v[130:133], v[176:179], v[196:199], v[130:133]
	v_mfma_i32_16x16x64_i8 v[122:125], v[184:187], v[196:199], v[122:125]
	v_mfma_i32_16x16x64_i8 v[114:117], v[176:179], v[204:207], v[114:117]
	v_mfma_i32_16x16x64_i8 v[106:109], v[184:187], v[204:207], v[106:109]
	v_mfma_i32_16x16x64_i8 v[98:101], v[176:179], v[212:215], v[98:101]
	v_mfma_i32_16x16x64_i8 v[90:93], v[184:187], v[212:215], v[90:93]
	v_mfma_i32_16x16x64_i8 v[82:85], v[176:179], v[220:223], v[82:85]
	v_mfma_i32_16x16x64_i8 v[74:77], v[184:187], v[220:223], v[74:77]
	v_mfma_i32_16x16x64_i8 v[130:133], v[180:183], v[200:203], v[130:133]
	v_mfma_i32_16x16x64_i8 v[122:125], v[188:191], v[200:203], v[122:125]
	v_mfma_i32_16x16x64_i8 v[114:117], v[180:183], v[208:211], v[114:117]
	v_mfma_i32_16x16x64_i8 v[106:109], v[188:191], v[208:211], v[106:109]
	v_mfma_i32_16x16x64_i8 v[98:101], v[180:183], v[216:219], v[98:101]
	v_mfma_i32_16x16x64_i8 v[90:93], v[188:191], v[216:219], v[90:93]
	v_mfma_i32_16x16x64_i8 v[82:85], v[180:183], v[224:227], v[82:85]
	v_mfma_i32_16x16x64_i8 v[74:77], v[188:191], v[224:227], v[74:77]
	s_setprio 0
	s_barrier
	s_add_i32 s28, s49, s38
	v_lshl_add_u64 v[192:193], s[34:35], 0, v[140:141]
	s_mov_b32 m0, s28
	ds_read_b128 v[196:199], v169 offset:16384
	ds_read_b128 v[200:203], v169 offset:17408
	ds_read_b128 v[204:207], v169 offset:18432
	ds_read_b128 v[208:211], v169 offset:19456
	ds_read_b128 v[212:215], v169 offset:20480
	ds_read_b128 v[216:219], v169 offset:21504
	ds_read_b128 v[220:223], v169 offset:22528
	ds_read_b128 v[224:227], v169 offset:23552
	global_load_lds_dwordx4 v[192:193], off
	s_add_i32 m0, s28, 0x2000
	s_add_u32 s28, s34, 0x40000
	v_lshl_add_u64 v[228:229], s[34:35], 0, v[138:139]
	s_addc_u32 s29, s35, 0
	s_add_i32 s63, s52, s38
	global_load_lds_dwordx4 v[228:229], off
	v_lshl_add_u64 v[230:231], s[28:29], 0, v[140:141]
	s_mov_b32 m0, s63
	s_nop 0
	global_load_lds_dwordx4 v[230:231], off
	v_lshl_add_u64 v[230:231], s[28:29], 0, v[138:139]
	s_add_i32 m0, s63, 0x2000
	s_and_b64 s[28:29], s[6:7], s[36:37]
	s_and_b64 s[28:29], s[28:29], exec
	s_cselect_b32 s28, s20, s26
	s_cselect_b32 s29, s21, s27
	s_add_u32 s28, s28, s67
	s_addc_u32 s29, s29, 0
	global_load_lds_dwordx4 v[230:231], off
	v_lshl_add_u64 v[230:231], s[28:29], 0, v[142:143]
	s_mov_b32 m0, s25
	v_lshl_add_u64 v[232:233], s[28:29], 0, v[144:145]
	global_load_lds_dwordx4 v[230:231], off
	s_mov_b32 m0, s41
	s_nop 0
	global_load_lds_dwordx4 v[232:233], off
	s_waitcnt vmcnt(8)
	s_waitcnt lgkmcnt(0)
	s_barrier
; #define PG8_LDA(dst, b, h) do { _Pragma("unroll") for (int m = 0; m < 4; ++m) dst[m] = PG8_LD32(lds + PG8_SA(b, h) + aoff + m * 2048); } while (0)
; #define PG8_LDB(dst, b, h) do { _Pragma("unroll") for (int n = 0; n < 2; ++n) dst[n] = PG8_LD32(lds + PG8_SB(b, h) + boff + n * 2048); } while (0)
; #define PG8_WAIT_V(n) asm volatile("s_waitcnt vmcnt(" #n ")" ::: "memory")
; #define PG8_WAIT_L(n) asm volatile("s_waitcnt lgkmcnt(" #n ")" ::: "memory")
; #define PG8_BAR __builtin_amdgcn_s_barrier()
; #define PG8_SCHED __builtin_amdgcn_sched_barrier(0)
; #define PG8_STA(bufoff, nextflag, h, koff) do { if constexpr (Sched::GATHER) { unsigned _o[2]; _o[0] = (nextflag) ? nxtA[h][0] : curA[h][0]; _o[1] = (nextflag) ? nxtA[h][1] : curA[h][1]; PG8_STAGE(bufoff, Ab + (koff), _o); } \
;         else { PG8_STAGE(bufoff, ((nextflag) ? nA : cA) + (size_t)(h) * hstep + (koff), voffA); } } while (0)
; template <class Epi, class Sched, bool ALIGN_EPI, int DT>
; __device__ __forceinline__ void gemm_phase(LAS unsigned char* lds, const int KB, const Sched& S, const Epi& E) {
;     ...
;             PG8_WAIT_V(8); PG8_WAIT_L(0); PG8_BAR; PG8_MMA(1, 0, At, B0); PG8_MMA(1, 1, At, B1); PG8_BAR; PG8_SCHED;
;             PG8_LDB(B0, 1, 0); PG8_LDB(B1, 1, 1); PG8_SCHED; PG8_LDA(At, 1, 0); PG8_STA(PG8_SA(0, 1), last, 1, k2);
;             PG8_WAIT_V(8); PG8_WAIT_L(0); PG8_BAR; PG8_MMA(0, 0, At, B0); PG8_MMA(0, 1, At, B1); PG8_BAR; PG8_SCHED;
	s_setprio 1
	s_waitcnt lgkmcnt(0)
	v_mfma_i32_16x16x64_i8 v[62:65], v[70:73], v[196:199], v[62:65]
	v_mfma_i32_16x16x64_i8 v[54:57], v[160:163], v[196:199], v[54:57]
	v_mfma_i32_16x16x64_i8 v[46:49], v[70:73], v[204:207], v[46:49]
	v_mfma_i32_16x16x64_i8 v[38:41], v[160:163], v[204:207], v[38:41]
	v_mfma_i32_16x16x64_i8 v[30:33], v[70:73], v[212:215], v[30:33]
	v_mfma_i32_16x16x64_i8 v[22:25], v[160:163], v[212:215], v[22:25]
	v_mfma_i32_16x16x64_i8 v[6:9], v[70:73], v[220:223], v[6:9]
	v_mfma_i32_16x16x64_i8 v[2:5], v[160:163], v[220:223], v[2:5]
	v_mfma_i32_16x16x64_i8 v[62:65], v[156:159], v[200:203], v[62:65]
	v_mfma_i32_16x16x64_i8 v[54:57], v[172:175], v[200:203], v[54:57]
	v_mfma_i32_16x16x64_i8 v[46:49], v[156:159], v[208:211], v[46:49]
	v_mfma_i32_16x16x64_i8 v[38:41], v[172:175], v[208:211], v[38:41]
	v_mfma_i32_16x16x64_i8 v[30:33], v[156:159], v[216:219], v[30:33]
	v_mfma_i32_16x16x64_i8 v[22:25], v[172:175], v[216:219], v[22:25]
	v_mfma_i32_16x16x64_i8 v[6:9], v[156:159], v[224:227], v[6:9]
	v_mfma_i32_16x16x64_i8 v[2:5], v[172:175], v[224:227], v[2:5]
	s_setprio 0
	s_setprio 1
	v_mfma_i32_16x16x64_i8 v[58:61], v[176:179], v[196:199], v[58:61]
	v_mfma_i32_16x16x64_i8 v[50:53], v[184:187], v[196:199], v[50:53]
	v_mfma_i32_16x16x64_i8 v[42:45], v[176:179], v[204:207], v[42:45]
	v_mfma_i32_16x16x64_i8 v[34:37], v[184:187], v[204:207], v[34:37]
	v_mfma_i32_16x16x64_i8 v[26:29], v[176:179], v[212:215], v[26:29]
	v_mfma_i32_16x16x64_i8 v[18:21], v[184:187], v[212:215], v[18:21]
	v_mfma_i32_16x16x64_i8 v[14:17], v[176:179], v[220:223], v[14:17]
	v_mfma_i32_16x16x64_i8 v[10:13], v[184:187], v[220:223], v[10:13]
	v_mfma_i32_16x16x64_i8 v[58:61], v[180:183], v[200:203], v[58:61]
	v_mfma_i32_16x16x64_i8 v[50:53], v[188:191], v[200:203], v[50:53]
	v_mfma_i32_16x16x64_i8 v[42:45], v[180:183], v[208:211], v[42:45]
	v_mfma_i32_16x16x64_i8 v[34:37], v[188:191], v[208:211], v[34:37]
	v_mfma_i32_16x16x64_i8 v[26:29], v[180:183], v[216:219], v[26:29]
	v_mfma_i32_16x16x64_i8 v[18:21], v[188:191], v[216:219], v[18:21]
	v_mfma_i32_16x16x64_i8 v[14:17], v[180:183], v[224:227], v[14:17]
	v_mfma_i32_16x16x64_i8 v[10:13], v[188:191], v[224:227], v[10:13]
	s_setprio 0
	s_barrier
	s_add_i32 s36, 0, 0x18000
	v_add_u32_e32 v1, s36, v165
	s_add_i32 s37, 0, 0x1c000
	ds_read_b128 v[70:73], v1
	ds_read_b128 v[156:159], v1 offset:1024
	ds_read_b128 v[160:163], v1 offset:2048
	ds_read_b128 v[172:175], v1 offset:3072
	v_add_u32_e32 v1, s37, v165
	ds_read_b128 v[176:179], v1
	ds_read_b128 v[180:183], v1 offset:1024
	ds_read_b128 v[184:187], v1 offset:2048
	ds_read_b128 v[188:191], v1 offset:3072
	s_add_u32 s28, s28, 0x40000
	s_addc_u32 s29, s29, 0
	s_mov_b32 m0, s42
	v_lshl_add_u64 v[234:235], s[28:29], 0, v[142:143]
	ds_read_b128 v[196:199], v169 offset:32768
	ds_read_b128 v[200:203], v169 offset:33792
	ds_read_b128 v[204:207], v169 offset:34816
	ds_read_b128 v[208:211], v169 offset:35840
	ds_read_b128 v[212:215], v169 offset:36864
	ds_read_b128 v[216:219], v169 offset:37888
	ds_read_b128 v[220:223], v169 offset:38912
	ds_read_b128 v[224:227], v169 offset:39936
	global_load_lds_dwordx4 v[234:235], off
	v_lshl_add_u64 v[234:235], s[28:29], 0, v[144:145]
	s_mov_b32 m0, s43
	s_nop 0
	global_load_lds_dwordx4 v[234:235], off
	s_nop 0
	s_waitcnt vmcnt(8)
	s_waitcnt lgkmcnt(0)
	s_barrier
	s_setprio 1
	s_waitcnt lgkmcnt(0)
	v_mfma_i32_16x16x64_i8 v[134:137], v[70:73], v[196:199], v[134:137]
	v_mfma_i32_16x16x64_i8 v[126:129], v[160:163], v[196:199], v[126:129]
	v_mfma_i32_16x16x64_i8 v[118:121], v[70:73], v[204:207], v[118:121]
	v_mfma_i32_16x16x64_i8 v[110:113], v[160:163], v[204:207], v[110:113]
	v_mfma_i32_16x16x64_i8 v[102:105], v[70:73], v[212:215], v[102:105]
	v_mfma_i32_16x16x64_i8 v[94:97], v[160:163], v[212:215], v[94:97]
	v_mfma_i32_16x16x64_i8 v[86:89], v[70:73], v[220:223], v[86:89]
	v_mfma_i32_16x16x64_i8 v[78:81], v[160:163], v[220:223], v[78:81]
	v_mfma_i32_16x16x64_i8 v[134:137], v[156:159], v[200:203], v[134:137]
	v_mfma_i32_16x16x64_i8 v[126:129], v[172:175], v[200:203], v[126:129]
	v_mfma_i32_16x16x64_i8 v[118:121], v[156:159], v[208:211], v[118:121]
	v_mfma_i32_16x16x64_i8 v[110:113], v[172:175], v[208:211], v[110:113]
	v_mfma_i32_16x16x64_i8 v[102:105], v[156:159], v[216:219], v[102:105]
	v_mfma_i32_16x16x64_i8 v[94:97], v[172:175], v[216:219], v[94:97]
	v_mfma_i32_16x16x64_i8 v[86:89], v[156:159], v[224:227], v[86:89]
	v_mfma_i32_16x16x64_i8 v[78:81], v[172:175], v[224:227], v[78:81]
	s_setprio 0
	s_setprio 1
	v_mfma_i32_16x16x64_i8 v[130:133], v[176:179], v[196:199], v[130:133]
	v_mfma_i32_16x16x64_i8 v[122:125], v[184:187], v[196:199], v[122:125]
	v_mfma_i32_16x16x64_i8 v[114:117], v[176:179], v[204:207], v[114:117]
	v_mfma_i32_16x16x64_i8 v[106:109], v[184:187], v[204:207], v[106:109]
	v_mfma_i32_16x16x64_i8 v[98:101], v[176:179], v[212:215], v[98:101]
	v_mfma_i32_16x16x64_i8 v[90:93], v[184:187], v[212:215], v[90:93]
	v_mfma_i32_16x16x64_i8 v[82:85], v[176:179], v[220:223], v[82:85]
	v_mfma_i32_16x16x64_i8 v[74:77], v[184:187], v[220:223], v[74:77]
	v_mfma_i32_16x16x64_i8 v[130:133], v[180:183], v[200:203], v[130:133]
	v_mfma_i32_16x16x64_i8 v[122:125], v[188:191], v[200:203], v[122:125]
	v_mfma_i32_16x16x64_i8 v[114:117], v[180:183], v[208:211], v[114:117]
	v_mfma_i32_16x16x64_i8 v[106:109], v[188:191], v[208:211], v[106:109]
	v_mfma_i32_16x16x64_i8 v[98:101], v[180:183], v[216:219], v[98:101]
	v_mfma_i32_16x16x64_i8 v[90:93], v[188:191], v[216:219], v[90:93]
	v_mfma_i32_16x16x64_i8 v[82:85], v[180:183], v[224:227], v[82:85]
	v_mfma_i32_16x16x64_i8 v[74:77], v[188:191], v[224:227], v[74:77]
	s_setprio 0
	s_barrier
; #define PG8_STAGE(bufoff, gbase, voff) do { _Pragma("unroll") for (int _i = 0; _i < 2; ++_i) \
;         __builtin_amdgcn_global_load_lds((const unsigned*)((const char*)(gbase) + (voff)[_i]), (LAS unsigned*)(lds + (bufoff) + ldsw + _i * 8192), 16, 0, 0); } while (0)
; #define PG8_LDA(dst, b, h) do { _Pragma("unroll") for (int m = 0; m < 4; ++m) dst[m] = PG8_LD32(lds + PG8_SA(b, h) + aoff + m * 2048); } while (0)
; #define PG8_WAIT_V(n) asm volatile("s_waitcnt vmcnt(" #n ")" ::: "memory")
; #define PG8_WAIT_L(n) asm volatile("s_waitcnt lgkmcnt(" #n ")" ::: "memory")
; #define PG8_BAR __builtin_amdgcn_s_barrier()
; #define PG8_SCHED __builtin_amdgcn_sched_barrier(0)
; #define PG8_STA(bufoff, nextflag, h, koff) do { if constexpr (Sched::GATHER) { unsigned _o[2]; _o[0] = (nextflag) ? nxtA[h][0] : curA[h][0]; _o[1] = (nextflag) ? nxtA[h][1] : curA[h][1]; PG8_STAGE(bufoff, Ab + (koff), _o); } \
;         else { PG8_STAGE(bufoff, ((nextflag) ? nA : cA) + (size_t)(h) * hstep + (koff), voffA); } } while (0)
; template <class Epi, class Sched, bool ALIGN_EPI, int DT>
; __device__ __forceinline__ void gemm_phase(LAS unsigned char* lds, const int KB, const Sched& S, const Epi& E) {
;     ...
;             PG8_LDA(At, 1, 1); PG8_STAGE(PG8_SB(1, 0), b3, voffB); PG8_STAGE(PG8_SB(1, 1), b3 + hstep, voffB); PG8_STA(PG8_SA(1, 0), last, 0, k3);
;             PG8_WAIT_V(8); PG8_WAIT_L(0); PG8_BAR; PG8_MMA(1, 0, At, B0); PG8_MMA(1, 1, At, B1); PG8_BAR; PG8_SCHED;
;         }
;         if constexpr (ALIGN_EPI) { if (wr == 0) PG8_BAR; }
	s_add_i32 s28, s36, s38
	v_lshl_add_u64 v[192:193], v[192:193], 0, s[12:13]
	s_mov_b32 m0, s28
	ds_read_b128 v[196:199], v169 offset:49152
	ds_read_b128 v[200:203], v169 offset:50176
	ds_read_b128 v[204:207], v169 offset:51200
	ds_read_b128 v[208:211], v169 offset:52224
	ds_read_b128 v[212:215], v169 offset:53248
	ds_read_b128 v[216:219], v169 offset:54272
	ds_read_b128 v[220:223], v169 offset:55296
	ds_read_b128 v[224:227], v169 offset:56320
	global_load_lds_dwordx4 v[192:193], off
	s_add_i32 m0, s28, 0x2000
	s_add_u32 s28, s34, 0x40080
	v_lshl_add_u64 v[192:193], v[228:229], 0, s[12:13]
	s_addc_u32 s29, s35, 0
	s_add_i32 s34, s37, s38
	global_load_lds_dwordx4 v[192:193], off
	v_lshl_add_u64 v[192:193], s[28:29], 0, v[140:141]
	s_mov_b32 m0, s34
	s_nop 0
	global_load_lds_dwordx4 v[192:193], off
	v_lshl_add_u64 v[192:193], s[28:29], 0, v[138:139]
	s_add_i32 m0, s34, 0x2000
	s_nop 0
	global_load_lds_dwordx4 v[192:193], off
	v_lshl_add_u64 v[192:193], v[230:231], 0, s[12:13]
	s_mov_b32 m0, s45
	s_nop 0
	global_load_lds_dwordx4 v[192:193], off
	v_lshl_add_u64 v[192:193], v[232:233], 0, s[12:13]
	s_mov_b32 m0, s46
	s_nop 0
	global_load_lds_dwordx4 v[192:193], off
	s_waitcnt vmcnt(8)
	s_waitcnt lgkmcnt(0)
	s_barrier
	s_setprio 1
	s_waitcnt lgkmcnt(0)
	v_mfma_i32_16x16x64_i8 v[62:65], v[70:73], v[196:199], v[62:65]
	v_mfma_i32_16x16x64_i8 v[54:57], v[160:163], v[196:199], v[54:57]
	v_mfma_i32_16x16x64_i8 v[46:49], v[70:73], v[204:207], v[46:49]
	v_mfma_i32_16x16x64_i8 v[38:41], v[160:163], v[204:207], v[38:41]
	v_mfma_i32_16x16x64_i8 v[30:33], v[70:73], v[212:215], v[30:33]
	v_mfma_i32_16x16x64_i8 v[22:25], v[160:163], v[212:215], v[22:25]
	v_mfma_i32_16x16x64_i8 v[6:9], v[70:73], v[220:223], v[6:9]
	v_mfma_i32_16x16x64_i8 v[2:5], v[160:163], v[220:223], v[2:5]
	v_mfma_i32_16x16x64_i8 v[62:65], v[156:159], v[200:203], v[62:65]
	v_mfma_i32_16x16x64_i8 v[54:57], v[172:175], v[200:203], v[54:57]
	v_mfma_i32_16x16x64_i8 v[46:49], v[156:159], v[208:211], v[46:49]
	v_mfma_i32_16x16x64_i8 v[38:41], v[172:175], v[208:211], v[38:41]
	v_mfma_i32_16x16x64_i8 v[30:33], v[156:159], v[216:219], v[30:33]
	v_mfma_i32_16x16x64_i8 v[22:25], v[172:175], v[216:219], v[22:25]
	v_mfma_i32_16x16x64_i8 v[6:9], v[156:159], v[224:227], v[6:9]
	v_mfma_i32_16x16x64_i8 v[2:5], v[172:175], v[224:227], v[2:5]
	s_setprio 0
	s_setprio 1
	v_mfma_i32_16x16x64_i8 v[58:61], v[176:179], v[196:199], v[58:61]
	v_mfma_i32_16x16x64_i8 v[50:53], v[184:187], v[196:199], v[50:53]
	v_mfma_i32_16x16x64_i8 v[42:45], v[176:179], v[204:207], v[42:45]
	v_mfma_i32_16x16x64_i8 v[34:37], v[184:187], v[204:207], v[34:37]
	v_mfma_i32_16x16x64_i8 v[26:29], v[176:179], v[212:215], v[26:29]
	v_mfma_i32_16x16x64_i8 v[18:21], v[184:187], v[212:215], v[18:21]
	v_mfma_i32_16x16x64_i8 v[14:17], v[176:179], v[220:223], v[14:17]
	v_mfma_i32_16x16x64_i8 v[10:13], v[184:187], v[220:223], v[10:13]
	v_mfma_i32_16x16x64_i8 v[58:61], v[180:183], v[200:203], v[58:61]
	v_mfma_i32_16x16x64_i8 v[50:53], v[188:191], v[200:203], v[50:53]
	v_mfma_i32_16x16x64_i8 v[42:45], v[180:183], v[208:211], v[42:45]
	v_mfma_i32_16x16x64_i8 v[34:37], v[188:191], v[208:211], v[34:37]
	v_mfma_i32_16x16x64_i8 v[26:29], v[180:183], v[216:219], v[26:29]
	v_mfma_i32_16x16x64_i8 v[18:21], v[188:191], v[216:219], v[18:21]
	v_mfma_i32_16x16x64_i8 v[14:17], v[180:183], v[224:227], v[14:17]
	v_mfma_i32_16x16x64_i8 v[10:13], v[188:191], v[224:227], v[10:13]
	s_setprio 0
	s_barrier
	s_add_i32 s62, s62, 2
	s_cmp_gt_u32 s62, 13
	s_mov_b64 s[28:29], s[30:31]
	s_cbranch_scc0 .LBB0_1154
	s_and_b64 vcc, exec, s[14:15]
	s_cbranch_vccz .LBB0_1157
	s_barrier

; #define PG8_STAGE(bufoff, gbase, voff) do { _Pragma("unroll") for (int _i = 0; _i < 2; ++_i) \
;         __builtin_amdgcn_global_load_lds((const unsigned*)((const char*)(gbase) + (voff)[_i]), (LAS unsigned*)(lds + (bufoff) + ldsw + _i * 8192), 16, 0, 0); } while (0)
; #define PG8_LDA(dst, b, h) do { _Pragma("unroll") for (int m = 0; m < 4; ++m) dst[m] = PG8_LD32(lds + PG8_SA(b, h) + aoff + m * 2048); } while (0)
; #define PG8_LDB(dst, b, h) do { _Pragma("unroll") for (int n = 0; n < 2; ++n) dst[n] = PG8_LD32(lds + PG8_SB(b, h) + boff + n * 2048); } while (0)
; #define PG8_WAIT_V(n) asm volatile("s_waitcnt vmcnt(" #n ")" ::: "memory")
; #define PG8_WAIT_L(n) asm volatile("s_waitcnt lgkmcnt(" #n ")" ::: "memory")
; #define PG8_BAR __builtin_amdgcn_s_barrier()
; #define PG8_SCHED __builtin_amdgcn_sched_barrier(0)
; #define PG8_STA(bufoff, nextflag, h, koff) do { if constexpr (Sched::GATHER) { unsigned _o[2]; _o[0] = (nextflag) ? nxtA[h][0] : curA[h][0]; _o[1] = (nextflag) ? nxtA[h][1] : curA[h][1]; PG8_STAGE(bufoff, Ab + (koff), _o); } \
;         else { PG8_STAGE(bufoff, ((nextflag) ? nA : cA) + (size_t)(h) * hstep + (koff), voffA); } } while (0)
; template <class Epi, class Sched, bool ALIGN_EPI, int DT>
; __device__ __forceinline__ void gemm_phase(LAS unsigned char* lds, const int KB, const Sched& S, const Epi& E) {
;     ...
;         for (int t = 0; t < nt; t += 2) {
;             const bool last = (t == nt - 2);
;             const size_t k1 = (size_t)(t + 1) * kstep, k2 = last ? 0 : (size_t)(t + 2) * kstep, k3 = k2 + kstep;
;             const char* b2 = last ? nB : cB + (size_t)(t + 2) * kstep; const char* b3 = b2 + kstep;
;             PG8_LDB(B0, 0, 0); PG8_LDB(B1, 0, 1); PG8_SCHED; PG8_LDA(At, 0, 0); PG8_STA(PG8_SA(1, 1), false, 1, k1);
;             PG8_WAIT_V(8); PG8_WAIT_L(0); PG8_BAR; PG8_MMA(0, 0, At, B0); PG8_MMA(0, 1, At, B1); PG8_BAR; PG8_SCHED;
;             PG8_LDA(At, 0, 1); PG8_STAGE(PG8_SB(0, 0), b2, voffB); PG8_STAGE(PG8_SB(0, 1), b2 + hstep, voffB); PG8_STA(PG8_SA(0, 0), last, 0, k2);
;             PG8_WAIT_V(8); PG8_WAIT_L(0); PG8_BAR; PG8_MMA(1, 0, At, B0); PG8_MMA(1, 1, At, B1); PG8_BAR; PG8_SCHED;
;             PG8_LDB(B0, 1, 0); PG8_LDB(B1, 1, 1); PG8_SCHED; PG8_LDA(At, 1, 0); PG8_STA(PG8_SA(0, 1), last, 1, k2);
;             PG8_WAIT_V(8); PG8_WAIT_L(0); PG8_BAR; PG8_MMA(0, 0, At, B0); PG8_MMA(0, 1, At, B1); PG8_BAR; PG8_SCHED;
.LBB0_1237:
	ds_read_b128 v[18:21], v193
	ds_read_b128 v[22:25], v193 offset:1024
	ds_read_b128 v[26:29], v193 offset:2048
	ds_read_b128 v[30:33], v193 offset:3072
	ds_read_b128 v[2:5], v195
	ds_read_b128 v[6:9], v195 offset:1024
	ds_read_b128 v[10:13], v195 offset:2048
	ds_read_b128 v[14:17], v195 offset:3072
	s_add_u32 s26, s30, 0x100
	s_addc_u32 s27, s31, 0
	s_add_u32 s28, s56, s30
	s_addc_u32 s29, s57, s31
	s_add_i32 s68, s43, s34
	s_add_i32 m0, s35, 0xc000
	s_add_i32 s69, s35, 0xe000
	s_add_i32 s63, s68, 0x2000
	s_cmp_eq_u32 s62, 40
	s_cselect_b32 s29, s23, s29
	s_cselect_b32 s28, s22, s28
	s_cselect_b32 s66, 0, s27
	s_cselect_b32 s67, 0, s26
	v_lshl_add_u64 v[222:223], v[178:179], 0, s[30:31]
	ds_read_b128 v[182:185], v196
	ds_read_b128 v[186:189], v196 offset:1024
	ds_read_b128 v[198:201], v196 offset:2048
	ds_read_b128 v[202:205], v196 offset:3072
	ds_read_b128 v[206:209], v196 offset:4096
	ds_read_b128 v[210:213], v196 offset:5120
	ds_read_b128 v[214:217], v196 offset:6144
	ds_read_b128 v[218:221], v196 offset:7168
	global_load_lds_dwordx4 v[222:223], off
	v_lshl_add_u64 v[222:223], v[180:181], 0, s[30:31]
	s_mov_b32 m0, s69
	s_nop 0
	global_load_lds_dwordx4 v[222:223], off
	s_waitcnt vmcnt(8)
	s_waitcnt lgkmcnt(0)
	s_barrier
	s_setprio 1
	s_waitcnt lgkmcnt(0)
	v_mfma_scale_f32_16x16x128_f8f6f4 v[158:161], v[18:25], v[182:189], v[158:161], v190, v190 op_sel_hi:[0,0,0]
	v_mfma_scale_f32_16x16x128_f8f6f4 v[154:157], v[26:33], v[182:189], v[154:157], v190, v190 op_sel_hi:[0,0,0]
	v_mfma_scale_f32_16x16x128_f8f6f4 v[150:153], v[18:25], v[198:205], v[150:153], v190, v190 op_sel_hi:[0,0,0]
	v_mfma_scale_f32_16x16x128_f8f6f4 v[142:145], v[26:33], v[198:205], v[142:145], v190, v190 op_sel_hi:[0,0,0]
	v_mfma_scale_f32_16x16x128_f8f6f4 v[134:137], v[18:25], v[206:213], v[134:137], v190, v190 op_sel_hi:[0,0,0]
	v_mfma_scale_f32_16x16x128_f8f6f4 v[126:129], v[26:33], v[206:213], v[126:129], v190, v190 op_sel_hi:[0,0,0]
	v_mfma_scale_f32_16x16x128_f8f6f4 v[118:121], v[18:25], v[214:221], v[118:121], v190, v190 op_sel_hi:[0,0,0]
	v_mfma_scale_f32_16x16x128_f8f6f4 v[110:113], v[26:33], v[214:221], v[110:113], v190, v190 op_sel_hi:[0,0,0]
	s_setprio 0
	s_setprio 1
	v_mfma_scale_f32_16x16x128_f8f6f4 v[146:149], v[2:9], v[182:189], v[146:149], v190, v190 op_sel_hi:[0,0,0]
	v_mfma_scale_f32_16x16x128_f8f6f4 v[138:141], v[10:17], v[182:189], v[138:141], v190, v190 op_sel_hi:[0,0,0]
	v_mfma_scale_f32_16x16x128_f8f6f4 v[130:133], v[2:9], v[198:205], v[130:133], v190, v190 op_sel_hi:[0,0,0]
	v_mfma_scale_f32_16x16x128_f8f6f4 v[122:125], v[10:17], v[198:205], v[122:125], v190, v190 op_sel_hi:[0,0,0]
	v_mfma_scale_f32_16x16x128_f8f6f4 v[114:117], v[2:9], v[206:213], v[114:117], v190, v190 op_sel_hi:[0,0,0]
	v_mfma_scale_f32_16x16x128_f8f6f4 v[106:109], v[10:17], v[206:213], v[106:109], v190, v190 op_sel_hi:[0,0,0]
	v_mfma_scale_f32_16x16x128_f8f6f4 v[102:105], v[2:9], v[214:221], v[102:105], v190, v190 op_sel_hi:[0,0,0]
	v_mfma_scale_f32_16x16x128_f8f6f4 v[98:101], v[10:17], v[214:221], v[98:101], v190, v190 op_sel_hi:[0,0,0]
	s_setprio 0
	s_barrier
	s_mov_b32 m0, s68
	v_lshl_add_u64 v[184:185], s[28:29], 0, v[162:163]
	ds_read_b128 v[198:201], v196 offset:16384
	ds_read_b128 v[202:205], v196 offset:17408
	ds_read_b128 v[206:209], v196 offset:18432
	ds_read_b128 v[210:213], v196 offset:19456
	ds_read_b128 v[214:217], v196 offset:20480
	ds_read_b128 v[218:221], v196 offset:21504
	ds_read_b128 v[222:225], v196 offset:22528
	ds_read_b128 v[226:229], v196 offset:23552
	global_load_lds_dwordx4 v[184:185], off
	s_mov_b32 m0, s63
	s_cselect_b32 s63, s9, s25
	s_cselect_b32 s68, s8, s24
	s_add_u32 s30, s28, 0xb0000
	v_lshl_add_u64 v[182:183], s[28:29], 0, v[164:165]
	s_addc_u32 s31, s29, 0
	s_add_i32 s69, s44, s34
	global_load_lds_dwordx4 v[182:183], off
	v_lshl_add_u64 v[186:187], s[30:31], 0, v[162:163]
	s_mov_b32 m0, s69
	s_nop 0
	global_load_lds_dwordx4 v[186:187], off
	s_add_i32 m0, s69, 0x2000
	v_lshl_add_u64 v[186:187], s[30:31], 0, v[164:165]
	s_add_u32 s30, s68, s67
	s_addc_u32 s31, s63, s66
	global_load_lds_dwordx4 v[186:187], off
	v_lshl_add_u64 v[186:187], s[30:31], 0, v[166:167]
	s_mov_b32 m0, s35
	v_lshl_add_u64 v[188:189], s[30:31], 0, v[168:169]
	global_load_lds_dwordx4 v[186:187], off
	s_mov_b32 m0, s36
	s_nop 0
	global_load_lds_dwordx4 v[188:189], off
	s_waitcnt vmcnt(8)
	s_waitcnt lgkmcnt(0)
	s_barrier
	s_setprio 1
	s_waitcnt lgkmcnt(0)
	v_mfma_scale_f32_16x16x128_f8f6f4 v[94:97], v[18:25], v[198:205], v[94:97], v190, v190 op_sel_hi:[0,0,0]
	v_mfma_scale_f32_16x16x128_f8f6f4 v[90:93], v[26:33], v[198:205], v[90:93], v190, v190 op_sel_hi:[0,0,0]
	v_mfma_scale_f32_16x16x128_f8f6f4 v[86:89], v[18:25], v[206:213], v[86:89], v190, v190 op_sel_hi:[0,0,0]
	v_mfma_scale_f32_16x16x128_f8f6f4 v[78:81], v[26:33], v[206:213], v[78:81], v190, v190 op_sel_hi:[0,0,0]
	v_mfma_scale_f32_16x16x128_f8f6f4 v[62:65], v[18:25], v[214:221], v[62:65], v190, v190 op_sel_hi:[0,0,0]
	v_mfma_scale_f32_16x16x128_f8f6f4 v[54:57], v[26:33], v[214:221], v[54:57], v190, v190 op_sel_hi:[0,0,0]
	v_mfma_scale_f32_16x16x128_f8f6f4 v[46:49], v[18:25], v[222:229], v[46:49], v190, v190 op_sel_hi:[0,0,0]
	v_mfma_scale_f32_16x16x128_f8f6f4 v[38:41], v[26:33], v[222:229], v[38:41], v190, v190 op_sel_hi:[0,0,0]
	s_setprio 0
	s_setprio 1
	v_mfma_scale_f32_16x16x128_f8f6f4 v[82:85], v[2:9], v[198:205], v[82:85], v190, v190 op_sel_hi:[0,0,0]
	v_mfma_scale_f32_16x16x128_f8f6f4 v[74:77], v[10:17], v[198:205], v[74:77], v190, v190 op_sel_hi:[0,0,0]
	v_mfma_scale_f32_16x16x128_f8f6f4 v[58:61], v[2:9], v[206:213], v[58:61], v190, v190 op_sel_hi:[0,0,0]
	v_mfma_scale_f32_16x16x128_f8f6f4 v[50:53], v[10:17], v[206:213], v[50:53], v190, v190 op_sel_hi:[0,0,0]
	v_mfma_scale_f32_16x16x128_f8f6f4 v[42:45], v[2:9], v[214:221], v[42:45], v190, v190 op_sel_hi:[0,0,0]
	v_mfma_scale_f32_16x16x128_f8f6f4 v[34:37], v[10:17], v[214:221], v[34:37], v190, v190 op_sel_hi:[0,0,0]
	v_mfma_scale_f32_16x16x128_f8f6f4 v[70:73], v[2:9], v[222:229], v[70:73], v190, v190 op_sel_hi:[0,0,0]
	v_mfma_scale_f32_16x16x128_f8f6f4 v[66:69], v[10:17], v[222:229], v[66:69], v190, v190 op_sel_hi:[0,0,0]
	s_setprio 0
	s_barrier
; #define PG8_STAGE(bufoff, gbase, voff) do { _Pragma("unroll") for (int _i = 0; _i < 2; ++_i) \
;         __builtin_amdgcn_global_load_lds((const unsigned*)((const char*)(gbase) + (voff)[_i]), (LAS unsigned*)(lds + (bufoff) + ldsw + _i * 8192), 16, 0, 0); } while (0)
; #define PG8_LDA(dst, b, h) do { _Pragma("unroll") for (int m = 0; m < 4; ++m) dst[m] = PG8_LD32(lds + PG8_SA(b, h) + aoff + m * 2048); } while (0)
; #define PG8_LDB(dst, b, h) do { _Pragma("unroll") for (int n = 0; n < 2; ++n) dst[n] = PG8_LD32(lds + PG8_SB(b, h) + boff + n * 2048); } while (0)
; #define PG8_WAIT_V(n) asm volatile("s_waitcnt vmcnt(" #n ")" ::: "memory")
; #define PG8_WAIT_L(n) asm volatile("s_waitcnt lgkmcnt(" #n ")" ::: "memory")
; #define PG8_BAR __builtin_amdgcn_s_barrier()
; #define PG8_SCHED __builtin_amdgcn_sched_barrier(0)
; #define PG8_STA(bufoff, nextflag, h, koff) do { if constexpr (Sched::GATHER) { unsigned _o[2]; _o[0] = (nextflag) ? nxtA[h][0] : curA[h][0]; _o[1] = (nextflag) ? nxtA[h][1] : curA[h][1]; PG8_STAGE(bufoff, Ab + (koff), _o); } \
;         else { PG8_STAGE(bufoff, ((nextflag) ? nA : cA) + (size_t)(h) * hstep + (koff), voffA); } } while (0)
; template <class Epi, class Sched, bool ALIGN_EPI, int DT>
; __device__ __forceinline__ void gemm_phase(LAS unsigned char* lds, const int KB, const Sched& S, const Epi& E) {
;     ...
;             PG8_LDB(B0, 1, 0); PG8_LDB(B1, 1, 1); PG8_SCHED; PG8_LDA(At, 1, 0); PG8_STA(PG8_SA(0, 1), last, 1, k2);
;             PG8_WAIT_V(8); PG8_WAIT_L(0); PG8_BAR; PG8_MMA(0, 0, At, B0); PG8_MMA(0, 1, At, B1); PG8_BAR; PG8_SCHED;
;             PG8_LDA(At, 1, 1); PG8_STAGE(PG8_SB(1, 0), b3, voffB); PG8_STAGE(PG8_SB(1, 1), b3 + hstep, voffB); PG8_STA(PG8_SA(1, 0), last, 0, k3);
;             PG8_WAIT_V(8); PG8_WAIT_L(0); PG8_BAR; PG8_MMA(1, 0, At, B0); PG8_MMA(1, 1, At, B1); PG8_BAR; PG8_SCHED;
;         }
;         if constexpr (ALIGN_EPI) { if (wr == 0) PG8_BAR; }
	s_add_i32 s63, 0, 0x18000
	s_add_i32 s66, 0, 0x1c000
	v_add_u32_e32 v14, s63, v191
	v_add_u32_e32 v30, s66, v191
	ds_read_b128 v[2:5], v14
	ds_read_b128 v[6:9], v14 offset:1024
	ds_read_b128 v[10:13], v14 offset:2048
	ds_read_b128 v[14:17], v14 offset:3072
	ds_read_b128 v[18:21], v30
	ds_read_b128 v[22:25], v30 offset:1024
	ds_read_b128 v[26:29], v30 offset:2048
	ds_read_b128 v[30:33], v30 offset:3072
	s_add_u32 s30, s30, 0xb0000
	s_addc_u32 s31, s31, 0
	s_mov_b32 m0, s37
	v_lshl_add_u64 v[230:231], s[30:31], 0, v[166:167]
	ds_read_b128 v[198:201], v196 offset:32768
	ds_read_b128 v[202:205], v196 offset:33792
	ds_read_b128 v[206:209], v196 offset:34816
	ds_read_b128 v[210:213], v196 offset:35840
	ds_read_b128 v[214:217], v196 offset:36864
	ds_read_b128 v[218:221], v196 offset:37888
	ds_read_b128 v[222:225], v196 offset:38912
	ds_read_b128 v[226:229], v196 offset:39936
	global_load_lds_dwordx4 v[230:231], off
	v_lshl_add_u64 v[230:231], s[30:31], 0, v[168:169]
	s_mov_b32 m0, s38
	s_nop 0
	global_load_lds_dwordx4 v[230:231], off
	s_nop 0
	s_waitcnt vmcnt(8)
	s_waitcnt lgkmcnt(0)
	s_barrier
	s_setprio 1
	s_waitcnt lgkmcnt(0)
	v_mfma_scale_f32_16x16x128_f8f6f4 v[158:161], v[2:9], v[198:205], v[158:161], v190, v190 op_sel_hi:[0,0,0]
	v_mfma_scale_f32_16x16x128_f8f6f4 v[154:157], v[10:17], v[198:205], v[154:157], v190, v190 op_sel_hi:[0,0,0]
	v_mfma_scale_f32_16x16x128_f8f6f4 v[150:153], v[2:9], v[206:213], v[150:153], v190, v190 op_sel_hi:[0,0,0]
	v_mfma_scale_f32_16x16x128_f8f6f4 v[142:145], v[10:17], v[206:213], v[142:145], v190, v190 op_sel_hi:[0,0,0]
	v_mfma_scale_f32_16x16x128_f8f6f4 v[134:137], v[2:9], v[214:221], v[134:137], v190, v190 op_sel_hi:[0,0,0]
	v_mfma_scale_f32_16x16x128_f8f6f4 v[126:129], v[10:17], v[214:221], v[126:129], v190, v190 op_sel_hi:[0,0,0]
	v_mfma_scale_f32_16x16x128_f8f6f4 v[118:121], v[2:9], v[222:229], v[118:121], v190, v190 op_sel_hi:[0,0,0]
	v_mfma_scale_f32_16x16x128_f8f6f4 v[110:113], v[10:17], v[222:229], v[110:113], v190, v190 op_sel_hi:[0,0,0]
	s_setprio 0
	s_setprio 1
	v_mfma_scale_f32_16x16x128_f8f6f4 v[146:149], v[18:25], v[198:205], v[146:149], v190, v190 op_sel_hi:[0,0,0]
	v_mfma_scale_f32_16x16x128_f8f6f4 v[138:141], v[26:33], v[198:205], v[138:141], v190, v190 op_sel_hi:[0,0,0]
	v_mfma_scale_f32_16x16x128_f8f6f4 v[130:133], v[18:25], v[206:213], v[130:133], v190, v190 op_sel_hi:[0,0,0]
	v_mfma_scale_f32_16x16x128_f8f6f4 v[122:125], v[26:33], v[206:213], v[122:125], v190, v190 op_sel_hi:[0,0,0]
	v_mfma_scale_f32_16x16x128_f8f6f4 v[114:117], v[18:25], v[214:221], v[114:117], v190, v190 op_sel_hi:[0,0,0]
	v_mfma_scale_f32_16x16x128_f8f6f4 v[106:109], v[26:33], v[214:221], v[106:109], v190, v190 op_sel_hi:[0,0,0]
	v_mfma_scale_f32_16x16x128_f8f6f4 v[102:105], v[18:25], v[222:229], v[102:105], v190, v190 op_sel_hi:[0,0,0]
	v_mfma_scale_f32_16x16x128_f8f6f4 v[98:101], v[26:33], v[222:229], v[98:101], v190, v190 op_sel_hi:[0,0,0]
	s_setprio 0
	s_barrier
	s_add_i32 s30, s63, s34
	v_lshl_add_u64 v[184:185], v[184:185], 0, s[12:13]
	s_mov_b32 m0, s30
	ds_read_b128 v[198:201], v196 offset:49152
	ds_read_b128 v[202:205], v196 offset:50176
	ds_read_b128 v[206:209], v196 offset:51200
	ds_read_b128 v[210:213], v196 offset:52224
	ds_read_b128 v[214:217], v196 offset:53248
	ds_read_b128 v[218:221], v196 offset:54272
	ds_read_b128 v[222:225], v196 offset:55296
	ds_read_b128 v[226:229], v196 offset:56320
	global_load_lds_dwordx4 v[184:185], off
	s_add_i32 m0, s30, 0x2000
	s_add_u32 s28, s28, 0xb0080
	v_lshl_add_u64 v[182:183], v[182:183], 0, s[12:13]
	s_addc_u32 s29, s29, 0
	s_add_i32 s30, s66, s34
	global_load_lds_dwordx4 v[182:183], off
	v_lshl_add_u64 v[182:183], s[28:29], 0, v[162:163]
	s_mov_b32 m0, s30
	s_nop 0
	global_load_lds_dwordx4 v[182:183], off
	v_lshl_add_u64 v[182:183], s[28:29], 0, v[164:165]
	s_add_i32 m0, s30, 0x2000
	s_nop 0
	global_load_lds_dwordx4 v[182:183], off
	v_lshl_add_u64 v[182:183], v[186:187], 0, s[12:13]
	s_mov_b32 m0, s40
	s_nop 0
	global_load_lds_dwordx4 v[182:183], off
	v_lshl_add_u64 v[182:183], v[188:189], 0, s[12:13]
	s_mov_b32 m0, s41
	s_nop 0
	global_load_lds_dwordx4 v[182:183], off
	s_waitcnt vmcnt(8)
	s_waitcnt lgkmcnt(0)
	s_barrier
	s_setprio 1
	s_waitcnt lgkmcnt(0)
	v_mfma_scale_f32_16x16x128_f8f6f4 v[94:97], v[2:9], v[198:205], v[94:97], v190, v190 op_sel_hi:[0,0,0]
	v_mfma_scale_f32_16x16x128_f8f6f4 v[90:93], v[10:17], v[198:205], v[90:93], v190, v190 op_sel_hi:[0,0,0]
	v_mfma_scale_f32_16x16x128_f8f6f4 v[86:89], v[2:9], v[206:213], v[86:89], v190, v190 op_sel_hi:[0,0,0]
	v_mfma_scale_f32_16x16x128_f8f6f4 v[78:81], v[10:17], v[206:213], v[78:81], v190, v190 op_sel_hi:[0,0,0]
	v_mfma_scale_f32_16x16x128_f8f6f4 v[62:65], v[2:9], v[214:221], v[62:65], v190, v190 op_sel_hi:[0,0,0]
	v_mfma_scale_f32_16x16x128_f8f6f4 v[54:57], v[10:17], v[214:221], v[54:57], v190, v190 op_sel_hi:[0,0,0]
	v_mfma_scale_f32_16x16x128_f8f6f4 v[46:49], v[2:9], v[222:229], v[46:49], v190, v190 op_sel_hi:[0,0,0]
	v_mfma_scale_f32_16x16x128_f8f6f4 v[38:41], v[10:17], v[222:229], v[38:41], v190, v190 op_sel_hi:[0,0,0]
	s_setprio 0
	s_setprio 1
	v_mfma_scale_f32_16x16x128_f8f6f4 v[82:85], v[18:25], v[198:205], v[82:85], v190, v190 op_sel_hi:[0,0,0]
	v_mfma_scale_f32_16x16x128_f8f6f4 v[74:77], v[26:33], v[198:205], v[74:77], v190, v190 op_sel_hi:[0,0,0]
	v_mfma_scale_f32_16x16x128_f8f6f4 v[58:61], v[18:25], v[206:213], v[58:61], v190, v190 op_sel_hi:[0,0,0]
	v_mfma_scale_f32_16x16x128_f8f6f4 v[50:53], v[26:33], v[206:213], v[50:53], v190, v190 op_sel_hi:[0,0,0]
	v_mfma_scale_f32_16x16x128_f8f6f4 v[42:45], v[18:25], v[214:221], v[42:45], v190, v190 op_sel_hi:[0,0,0]
	v_mfma_scale_f32_16x16x128_f8f6f4 v[34:37], v[26:33], v[214:221], v[34:37], v190, v190 op_sel_hi:[0,0,0]
	v_mfma_scale_f32_16x16x128_f8f6f4 v[70:73], v[18:25], v[222:229], v[70:73], v190, v190 op_sel_hi:[0,0,0]
	v_mfma_scale_f32_16x16x128_f8f6f4 v[66:69], v[26:33], v[222:229], v[66:69], v190, v190 op_sel_hi:[0,0,0]
	s_setprio 0
	s_barrier
	s_add_i32 s62, s62, 2
	s_cmp_gt_u32 s62, 41
	s_mov_b64 s[30:31], s[26:27]
	s_cbranch_scc0 .LBB0_1237
	s_and_b64 vcc, exec, s[14:15]
	s_cbranch_vccz .LBB0_1240
	s_barrier

; #define PG8_STAGE(bufoff, gbase, voff) do { _Pragma("unroll") for (int _i = 0; _i < 2; ++_i) \
;         __builtin_amdgcn_global_load_lds((const unsigned*)((const char*)(gbase) + (voff)[_i]), (LAS unsigned*)(lds + (bufoff) + ldsw + _i * 8192), 16, 0, 0); } while (0)
; #define PG8_LDA(dst, b, h) do { _Pragma("unroll") for (int m = 0; m < 4; ++m) dst[m] = PG8_LD32(lds + PG8_SA(b, h) + aoff + m * 2048); } while (0)
; #define PG8_LDB(dst, b, h) do { _Pragma("unroll") for (int n = 0; n < 2; ++n) dst[n] = PG8_LD32(lds + PG8_SB(b, h) + boff + n * 2048); } while (0)
; #define PG8_WAIT_V(n) asm volatile("s_waitcnt vmcnt(" #n ")" ::: "memory")
; #define PG8_WAIT_L(n) asm volatile("s_waitcnt lgkmcnt(" #n ")" ::: "memory")
; #define PG8_BAR __builtin_amdgcn_s_barrier()
; #define PG8_SCHED __builtin_amdgcn_sched_barrier(0)
; #define PG8_STA(bufoff, nextflag, h, koff) do { if constexpr (Sched::GATHER) { unsigned _o[2]; _o[0] = (nextflag) ? nxtA[h][0] : curA[h][0]; _o[1] = (nextflag) ? nxtA[h][1] : curA[h][1]; PG8_STAGE(bufoff, Ab + (koff), _o); } \
;         else { PG8_STAGE(bufoff, ((nextflag) ? nA : cA) + (size_t)(h) * hstep + (koff), voffA); } } while (0)
; template <class Epi, class Sched, bool ALIGN_EPI, int DT>
; __device__ __forceinline__ void gemm_phase(LAS unsigned char* lds, const int KB, const Sched& S, const Epi& E) {
;     ...
;             PG8_LDB(B0, 0, 0); PG8_LDB(B1, 0, 1); PG8_SCHED; PG8_LDA(At, 0, 0); PG8_STA(PG8_SA(1, 1), false, 1, k1);
;             PG8_WAIT_V(8); PG8_WAIT_L(0); PG8_BAR; PG8_MMA(0, 0, At, B0); PG8_MMA(0, 1, At, B1); PG8_BAR; PG8_SCHED;
;             PG8_LDA(At, 0, 1); PG8_STAGE(PG8_SB(0, 0), b2, voffB); PG8_STAGE(PG8_SB(0, 1), b2 + hstep, voffB); PG8_STA(PG8_SA(0, 0), last, 0, k2);
;             PG8_WAIT_V(8); PG8_WAIT_L(0); PG8_BAR; PG8_MMA(1, 0, At, B0); PG8_MMA(1, 1, At, B1); PG8_BAR; PG8_SCHED;
.LBB0_1385:
	ds_read_b128 v[152:155], v174
	ds_read_b128 v[156:159], v174 offset:1024
	ds_read_b128 v[160:163], v174 offset:2048
	ds_read_b128 v[164:167], v174 offset:3072
	ds_read_b128 v[168:171], v175
	ds_read_b128 v[180:183], v175 offset:1024
	ds_read_b128 v[184:187], v175 offset:2048
	ds_read_b128 v[188:191], v175 offset:3072
	s_add_u32 s38, s36, 0x100
	s_addc_u32 s39, s37, 0
	s_add_u32 s74, s25, s36
	s_addc_u32 s75, s70, s37
	s_cmp_eq_u32 s71, 12
	s_cselect_b64 s[42:43], -1, 0
	s_and_b64 s[40:41], s[42:43], exec
	s_cselect_b32 s76, 0, s38
	s_cselect_b32 s41, s0, s75
	s_cselect_b32 s40, s23, s74
	v_lshl_add_u64 v[192:193], v[148:149], 0, s[36:37]
	s_add_i32 m0, s47, 0xc000
	ds_read_b128 v[196:199], v176
	ds_read_b128 v[200:203], v176 offset:1024
	ds_read_b128 v[204:207], v176 offset:2048
	ds_read_b128 v[208:211], v176 offset:3072
	ds_read_b128 v[212:215], v176 offset:4096
	ds_read_b128 v[216:219], v176 offset:5120
	ds_read_b128 v[220:223], v176 offset:6144
	ds_read_b128 v[224:227], v176 offset:7168
	global_load_lds_dwordx4 v[192:193], off
	v_lshl_add_u64 v[192:193], v[150:151], 0, s[36:37]
	s_add_i32 m0, s47, 0xe000
	s_nop 0
	global_load_lds_dwordx4 v[192:193], off
	s_nop 0
	s_waitcnt vmcnt(8)
	s_waitcnt lgkmcnt(0)
	s_barrier
	s_setprio 1
	s_waitcnt lgkmcnt(0)
	v_mfma_i32_16x16x64_i8 v[126:129], v[152:155], v[196:199], v[126:129]
	v_mfma_i32_16x16x64_i8 v[122:125], v[160:163], v[196:199], v[122:125]
	v_mfma_i32_16x16x64_i8 v[110:113], v[152:155], v[204:207], v[110:113]
	v_mfma_i32_16x16x64_i8 v[106:109], v[160:163], v[204:207], v[106:109]
	v_mfma_i32_16x16x64_i8 v[94:97], v[152:155], v[212:215], v[94:97]
	v_mfma_i32_16x16x64_i8 v[90:93], v[160:163], v[212:215], v[90:93]
	v_mfma_i32_16x16x64_i8 v[78:81], v[152:155], v[220:223], v[78:81]
	v_mfma_i32_16x16x64_i8 v[74:77], v[160:163], v[220:223], v[74:77]
	v_mfma_i32_16x16x64_i8 v[126:129], v[156:159], v[200:203], v[126:129]
	v_mfma_i32_16x16x64_i8 v[122:125], v[164:167], v[200:203], v[122:125]
	v_mfma_i32_16x16x64_i8 v[110:113], v[156:159], v[208:211], v[110:113]
	v_mfma_i32_16x16x64_i8 v[106:109], v[164:167], v[208:211], v[106:109]
	v_mfma_i32_16x16x64_i8 v[94:97], v[156:159], v[216:219], v[94:97]
	v_mfma_i32_16x16x64_i8 v[90:93], v[164:167], v[216:219], v[90:93]
	v_mfma_i32_16x16x64_i8 v[78:81], v[156:159], v[224:227], v[78:81]
	v_mfma_i32_16x16x64_i8 v[74:77], v[164:167], v[224:227], v[74:77]
	s_setprio 0
	s_setprio 1
	v_mfma_i32_16x16x64_i8 v[118:121], v[168:171], v[196:199], v[118:121]
	v_mfma_i32_16x16x64_i8 v[114:117], v[184:187], v[196:199], v[114:117]
	v_mfma_i32_16x16x64_i8 v[102:105], v[168:171], v[204:207], v[102:105]
	v_mfma_i32_16x16x64_i8 v[98:101], v[184:187], v[204:207], v[98:101]
	v_mfma_i32_16x16x64_i8 v[86:89], v[168:171], v[212:215], v[86:89]
	v_mfma_i32_16x16x64_i8 v[82:85], v[184:187], v[212:215], v[82:85]
	v_mfma_i32_16x16x64_i8 v[70:73], v[168:171], v[220:223], v[70:73]
	v_mfma_i32_16x16x64_i8 v[66:69], v[184:187], v[220:223], v[66:69]
	v_mfma_i32_16x16x64_i8 v[118:121], v[180:183], v[200:203], v[118:121]
	v_mfma_i32_16x16x64_i8 v[114:117], v[188:191], v[200:203], v[114:117]
	v_mfma_i32_16x16x64_i8 v[102:105], v[180:183], v[208:211], v[102:105]
	v_mfma_i32_16x16x64_i8 v[98:101], v[188:191], v[208:211], v[98:101]
	v_mfma_i32_16x16x64_i8 v[86:89], v[180:183], v[216:219], v[86:89]
	v_mfma_i32_16x16x64_i8 v[82:85], v[188:191], v[216:219], v[82:85]
	v_mfma_i32_16x16x64_i8 v[70:73], v[180:183], v[224:227], v[70:73]
	v_mfma_i32_16x16x64_i8 v[66:69], v[188:191], v[224:227], v[66:69]
	s_setprio 0
	s_barrier
	s_add_i32 s36, s66, s44
	v_lshl_add_u64 v[192:193], s[40:41], 0, v[134:135]
	s_mov_b32 m0, s36
	ds_read_b128 v[196:199], v176 offset:16384
	ds_read_b128 v[200:203], v176 offset:17408
	ds_read_b128 v[204:207], v176 offset:18432
	ds_read_b128 v[208:211], v176 offset:19456
	ds_read_b128 v[212:215], v176 offset:20480
	ds_read_b128 v[216:219], v176 offset:21504
	ds_read_b128 v[220:223], v176 offset:22528
	ds_read_b128 v[224:227], v176 offset:23552
	global_load_lds_dwordx4 v[192:193], off
	s_add_i32 m0, s36, 0x2000
	s_add_u32 s36, s40, 0x40000
	v_lshl_add_u64 v[228:229], s[40:41], 0, v[132:133]
	s_addc_u32 s37, s41, 0
	s_add_i32 s74, s67, s44
	global_load_lds_dwordx4 v[228:229], off
	v_lshl_add_u64 v[230:231], s[36:37], 0, v[134:135]
	s_mov_b32 m0, s74
	s_nop 0
	global_load_lds_dwordx4 v[230:231], off
	v_lshl_add_u64 v[230:231], s[36:37], 0, v[132:133]
	s_add_i32 m0, s74, 0x2000
	s_and_b64 s[36:37], s[8:9], s[42:43]
	s_and_b64 s[36:37], s[36:37], exec
	s_cselect_b32 s36, s26, s34
	s_cselect_b32 s37, s27, s35
	s_add_u32 s36, s36, s76
	s_addc_u32 s37, s37, 0
	global_load_lds_dwordx4 v[230:231], off
	v_lshl_add_u64 v[230:231], s[36:37], 0, v[136:137]
	s_mov_b32 m0, s47
	v_lshl_add_u64 v[232:233], s[36:37], 0, v[138:139]
	global_load_lds_dwordx4 v[230:231], off
	s_mov_b32 m0, s49
	s_nop 0
	global_load_lds_dwordx4 v[232:233], off
	s_waitcnt vmcnt(8)
	s_waitcnt lgkmcnt(0)
	s_barrier
; #define PG8_LDA(dst, b, h) do { _Pragma("unroll") for (int m = 0; m < 4; ++m) dst[m] = PG8_LD32(lds + PG8_SA(b, h) + aoff + m * 2048); } while (0)
; #define PG8_LDB(dst, b, h) do { _Pragma("unroll") for (int n = 0; n < 2; ++n) dst[n] = PG8_LD32(lds + PG8_SB(b, h) + boff + n * 2048); } while (0)
; #define PG8_WAIT_V(n) asm volatile("s_waitcnt vmcnt(" #n ")" ::: "memory")
; #define PG8_WAIT_L(n) asm volatile("s_waitcnt lgkmcnt(" #n ")" ::: "memory")
; #define PG8_BAR __builtin_amdgcn_s_barrier()
; #define PG8_SCHED __builtin_amdgcn_sched_barrier(0)
; #define PG8_STA(bufoff, nextflag, h, koff) do { if constexpr (Sched::GATHER) { unsigned _o[2]; _o[0] = (nextflag) ? nxtA[h][0] : curA[h][0]; _o[1] = (nextflag) ? nxtA[h][1] : curA[h][1]; PG8_STAGE(bufoff, Ab + (koff), _o); } \
;         else { PG8_STAGE(bufoff, ((nextflag) ? nA : cA) + (size_t)(h) * hstep + (koff), voffA); } } while (0)
; template <class Epi, class Sched, bool ALIGN_EPI, int DT>
; __device__ __forceinline__ void gemm_phase(LAS unsigned char* lds, const int KB, const Sched& S, const Epi& E) {
;     ...
;             PG8_WAIT_V(8); PG8_WAIT_L(0); PG8_BAR; PG8_MMA(1, 0, At, B0); PG8_MMA(1, 1, At, B1); PG8_BAR; PG8_SCHED;
;             PG8_LDB(B0, 1, 0); PG8_LDB(B1, 1, 1); PG8_SCHED; PG8_LDA(At, 1, 0); PG8_STA(PG8_SA(0, 1), last, 1, k2);
;             PG8_WAIT_V(8); PG8_WAIT_L(0); PG8_BAR; PG8_MMA(0, 0, At, B0); PG8_MMA(0, 1, At, B1); PG8_BAR; PG8_SCHED;
	s_setprio 1
	s_waitcnt lgkmcnt(0)
	v_mfma_i32_16x16x64_i8 v[62:65], v[152:155], v[196:199], v[62:65]
	v_mfma_i32_16x16x64_i8 v[58:61], v[160:163], v[196:199], v[58:61]
	v_mfma_i32_16x16x64_i8 v[46:49], v[152:155], v[204:207], v[46:49]
	v_mfma_i32_16x16x64_i8 v[42:45], v[160:163], v[204:207], v[42:45]
	v_mfma_i32_16x16x64_i8 v[30:33], v[152:155], v[212:215], v[30:33]
	v_mfma_i32_16x16x64_i8 v[26:29], v[160:163], v[212:215], v[26:29]
	v_mfma_i32_16x16x64_i8 v[6:9], v[152:155], v[220:223], v[6:9]
	v_mfma_i32_16x16x64_i8 v[2:5], v[160:163], v[220:223], v[2:5]
	v_mfma_i32_16x16x64_i8 v[62:65], v[156:159], v[200:203], v[62:65]
	v_mfma_i32_16x16x64_i8 v[58:61], v[164:167], v[200:203], v[58:61]
	v_mfma_i32_16x16x64_i8 v[46:49], v[156:159], v[208:211], v[46:49]
	v_mfma_i32_16x16x64_i8 v[42:45], v[164:167], v[208:211], v[42:45]
	v_mfma_i32_16x16x64_i8 v[30:33], v[156:159], v[216:219], v[30:33]
	v_mfma_i32_16x16x64_i8 v[26:29], v[164:167], v[216:219], v[26:29]
	v_mfma_i32_16x16x64_i8 v[6:9], v[156:159], v[224:227], v[6:9]
	v_mfma_i32_16x16x64_i8 v[2:5], v[164:167], v[224:227], v[2:5]
	s_setprio 0
	s_setprio 1
	v_mfma_i32_16x16x64_i8 v[54:57], v[168:171], v[196:199], v[54:57]
	v_mfma_i32_16x16x64_i8 v[50:53], v[184:187], v[196:199], v[50:53]
	v_mfma_i32_16x16x64_i8 v[38:41], v[168:171], v[204:207], v[38:41]
	v_mfma_i32_16x16x64_i8 v[34:37], v[184:187], v[204:207], v[34:37]
	v_mfma_i32_16x16x64_i8 v[14:17], v[168:171], v[212:215], v[14:17]
	v_mfma_i32_16x16x64_i8 v[10:13], v[184:187], v[212:215], v[10:13]
	v_mfma_i32_16x16x64_i8 v[22:25], v[168:171], v[220:223], v[22:25]
	v_mfma_i32_16x16x64_i8 v[18:21], v[184:187], v[220:223], v[18:21]
	v_mfma_i32_16x16x64_i8 v[54:57], v[180:183], v[200:203], v[54:57]
	v_mfma_i32_16x16x64_i8 v[50:53], v[188:191], v[200:203], v[50:53]
	v_mfma_i32_16x16x64_i8 v[38:41], v[180:183], v[208:211], v[38:41]
	v_mfma_i32_16x16x64_i8 v[34:37], v[188:191], v[208:211], v[34:37]
	v_mfma_i32_16x16x64_i8 v[14:17], v[180:183], v[216:219], v[14:17]
	v_mfma_i32_16x16x64_i8 v[10:13], v[188:191], v[216:219], v[10:13]
	v_mfma_i32_16x16x64_i8 v[22:25], v[180:183], v[224:227], v[22:25]
	v_mfma_i32_16x16x64_i8 v[18:21], v[188:191], v[224:227], v[18:21]
	s_setprio 0
	s_barrier
	s_add_i32 s42, 0, 0x18000
	v_add_u32_e32 v1, s42, v172
	s_add_i32 s43, 0, 0x1c000
	ds_read_b128 v[152:155], v1
	ds_read_b128 v[156:159], v1 offset:1024
	ds_read_b128 v[160:163], v1 offset:2048
	ds_read_b128 v[164:167], v1 offset:3072
	v_add_u32_e32 v1, s43, v172
	ds_read_b128 v[168:171], v1
	ds_read_b128 v[180:183], v1 offset:1024
	ds_read_b128 v[184:187], v1 offset:2048
	ds_read_b128 v[188:191], v1 offset:3072
	s_add_u32 s36, s36, 0x40000
	s_addc_u32 s37, s37, 0
	s_mov_b32 m0, s52
	v_lshl_add_u64 v[234:235], s[36:37], 0, v[136:137]
	ds_read_b128 v[196:199], v176 offset:32768
	ds_read_b128 v[200:203], v176 offset:33792
	ds_read_b128 v[204:207], v176 offset:34816
	ds_read_b128 v[208:211], v176 offset:35840
	ds_read_b128 v[212:215], v176 offset:36864
	ds_read_b128 v[216:219], v176 offset:37888
	ds_read_b128 v[220:223], v176 offset:38912
	ds_read_b128 v[224:227], v176 offset:39936
	global_load_lds_dwordx4 v[234:235], off
	v_lshl_add_u64 v[234:235], s[36:37], 0, v[138:139]
	s_mov_b32 m0, s53
	s_nop 0
	global_load_lds_dwordx4 v[234:235], off
	s_nop 0
	s_waitcnt vmcnt(8)
	s_waitcnt lgkmcnt(0)
	s_barrier
	s_setprio 1
	s_waitcnt lgkmcnt(0)
	v_mfma_i32_16x16x64_i8 v[126:129], v[152:155], v[196:199], v[126:129]
	v_mfma_i32_16x16x64_i8 v[122:125], v[160:163], v[196:199], v[122:125]
	v_mfma_i32_16x16x64_i8 v[110:113], v[152:155], v[204:207], v[110:113]
	v_mfma_i32_16x16x64_i8 v[106:109], v[160:163], v[204:207], v[106:109]
	v_mfma_i32_16x16x64_i8 v[94:97], v[152:155], v[212:215], v[94:97]
	v_mfma_i32_16x16x64_i8 v[90:93], v[160:163], v[212:215], v[90:93]
	v_mfma_i32_16x16x64_i8 v[78:81], v[152:155], v[220:223], v[78:81]
	v_mfma_i32_16x16x64_i8 v[74:77], v[160:163], v[220:223], v[74:77]
	v_mfma_i32_16x16x64_i8 v[126:129], v[156:159], v[200:203], v[126:129]
	v_mfma_i32_16x16x64_i8 v[122:125], v[164:167], v[200:203], v[122:125]
	v_mfma_i32_16x16x64_i8 v[110:113], v[156:159], v[208:211], v[110:113]
	v_mfma_i32_16x16x64_i8 v[106:109], v[164:167], v[208:211], v[106:109]
	v_mfma_i32_16x16x64_i8 v[94:97], v[156:159], v[216:219], v[94:97]
	v_mfma_i32_16x16x64_i8 v[90:93], v[164:167], v[216:219], v[90:93]
	v_mfma_i32_16x16x64_i8 v[78:81], v[156:159], v[224:227], v[78:81]
	v_mfma_i32_16x16x64_i8 v[74:77], v[164:167], v[224:227], v[74:77]
	s_setprio 0
	s_setprio 1
	v_mfma_i32_16x16x64_i8 v[118:121], v[168:171], v[196:199], v[118:121]
	v_mfma_i32_16x16x64_i8 v[114:117], v[184:187], v[196:199], v[114:117]
	v_mfma_i32_16x16x64_i8 v[102:105], v[168:171], v[204:207], v[102:105]
	v_mfma_i32_16x16x64_i8 v[98:101], v[184:187], v[204:207], v[98:101]
	v_mfma_i32_16x16x64_i8 v[86:89], v[168:171], v[212:215], v[86:89]
	v_mfma_i32_16x16x64_i8 v[82:85], v[184:187], v[212:215], v[82:85]
	v_mfma_i32_16x16x64_i8 v[70:73], v[168:171], v[220:223], v[70:73]
	v_mfma_i32_16x16x64_i8 v[66:69], v[184:187], v[220:223], v[66:69]
	v_mfma_i32_16x16x64_i8 v[118:121], v[180:183], v[200:203], v[118:121]
	v_mfma_i32_16x16x64_i8 v[114:117], v[188:191], v[200:203], v[114:117]
	v_mfma_i32_16x16x64_i8 v[102:105], v[180:183], v[208:211], v[102:105]
	v_mfma_i32_16x16x64_i8 v[98:101], v[188:191], v[208:211], v[98:101]
	v_mfma_i32_16x16x64_i8 v[86:89], v[180:183], v[216:219], v[86:89]
	v_mfma_i32_16x16x64_i8 v[82:85], v[188:191], v[216:219], v[82:85]
	v_mfma_i32_16x16x64_i8 v[70:73], v[180:183], v[224:227], v[70:73]
	v_mfma_i32_16x16x64_i8 v[66:69], v[188:191], v[224:227], v[66:69]
	s_setprio 0
	s_barrier
; #define PG8_STAGE(bufoff, gbase, voff) do { _Pragma("unroll") for (int _i = 0; _i < 2; ++_i) \
;         __builtin_amdgcn_global_load_lds((const unsigned*)((const char*)(gbase) + (voff)[_i]), (LAS unsigned*)(lds + (bufoff) + ldsw + _i * 8192), 16, 0, 0); } while (0)
; #define PG8_LDA(dst, b, h) do { _Pragma("unroll") for (int m = 0; m < 4; ++m) dst[m] = PG8_LD32(lds + PG8_SA(b, h) + aoff + m * 2048); } while (0)
; #define PG8_WAIT_V(n) asm volatile("s_waitcnt vmcnt(" #n ")" ::: "memory")
; #define PG8_WAIT_L(n) asm volatile("s_waitcnt lgkmcnt(" #n ")" ::: "memory")
; #define PG8_BAR __builtin_amdgcn_s_barrier()
; #define PG8_SCHED __builtin_amdgcn_sched_barrier(0)
; #define PG8_STA(bufoff, nextflag, h, koff) do { if constexpr (Sched::GATHER) { unsigned _o[2]; _o[0] = (nextflag) ? nxtA[h][0] : curA[h][0]; _o[1] = (nextflag) ? nxtA[h][1] : curA[h][1]; PG8_STAGE(bufoff, Ab + (koff), _o); } \
;         else { PG8_STAGE(bufoff, ((nextflag) ? nA : cA) + (size_t)(h) * hstep + (koff), voffA); } } while (0)
; template <class Epi, class Sched, bool ALIGN_EPI, int DT>
; __device__ __forceinline__ void gemm_phase(LAS unsigned char* lds, const int KB, const Sched& S, const Epi& E) {
;     ...
;             PG8_LDA(At, 1, 1); PG8_STAGE(PG8_SB(1, 0), b3, voffB); PG8_STAGE(PG8_SB(1, 1), b3 + hstep, voffB); PG8_STA(PG8_SA(1, 0), last, 0, k3);
;             PG8_WAIT_V(8); PG8_WAIT_L(0); PG8_BAR; PG8_MMA(1, 0, At, B0); PG8_MMA(1, 1, At, B1); PG8_BAR; PG8_SCHED;
;         }
;         if constexpr (ALIGN_EPI) { if (wr == 0) PG8_BAR; }
	s_add_i32 s36, s42, s44
	v_lshl_add_u64 v[192:193], v[192:193], 0, s[18:19]
	s_mov_b32 m0, s36
	ds_read_b128 v[196:199], v176 offset:49152
	ds_read_b128 v[200:203], v176 offset:50176
	ds_read_b128 v[204:207], v176 offset:51200
	ds_read_b128 v[208:211], v176 offset:52224
	ds_read_b128 v[212:215], v176 offset:53248
	ds_read_b128 v[216:219], v176 offset:54272
	ds_read_b128 v[220:223], v176 offset:55296
	ds_read_b128 v[224:227], v176 offset:56320
	global_load_lds_dwordx4 v[192:193], off
	s_add_i32 m0, s36, 0x2000
	s_add_u32 s36, s40, 0x40080
	v_lshl_add_u64 v[192:193], v[228:229], 0, s[18:19]
	s_addc_u32 s37, s41, 0
	s_add_i32 s40, s43, s44
	global_load_lds_dwordx4 v[192:193], off
	v_lshl_add_u64 v[192:193], s[36:37], 0, v[134:135]
	s_mov_b32 m0, s40
	s_nop 0
	global_load_lds_dwordx4 v[192:193], off
	v_lshl_add_u64 v[192:193], s[36:37], 0, v[132:133]
	s_add_i32 m0, s40, 0x2000
	s_nop 0
	global_load_lds_dwordx4 v[192:193], off
	v_lshl_add_u64 v[192:193], v[230:231], 0, s[18:19]
	s_mov_b32 m0, s57
	s_nop 0
	global_load_lds_dwordx4 v[192:193], off
	v_lshl_add_u64 v[192:193], v[232:233], 0, s[18:19]
	s_mov_b32 m0, s62
	s_nop 0
	global_load_lds_dwordx4 v[192:193], off
	s_waitcnt vmcnt(8)
	s_waitcnt lgkmcnt(0)
	s_barrier
	s_setprio 1
	s_waitcnt lgkmcnt(0)
	v_mfma_i32_16x16x64_i8 v[62:65], v[152:155], v[196:199], v[62:65]
	v_mfma_i32_16x16x64_i8 v[58:61], v[160:163], v[196:199], v[58:61]
	v_mfma_i32_16x16x64_i8 v[46:49], v[152:155], v[204:207], v[46:49]
	v_mfma_i32_16x16x64_i8 v[42:45], v[160:163], v[204:207], v[42:45]
	v_mfma_i32_16x16x64_i8 v[30:33], v[152:155], v[212:215], v[30:33]
	v_mfma_i32_16x16x64_i8 v[26:29], v[160:163], v[212:215], v[26:29]
	v_mfma_i32_16x16x64_i8 v[6:9], v[152:155], v[220:223], v[6:9]
	v_mfma_i32_16x16x64_i8 v[2:5], v[160:163], v[220:223], v[2:5]
	v_mfma_i32_16x16x64_i8 v[62:65], v[156:159], v[200:203], v[62:65]
	v_mfma_i32_16x16x64_i8 v[58:61], v[164:167], v[200:203], v[58:61]
	v_mfma_i32_16x16x64_i8 v[46:49], v[156:159], v[208:211], v[46:49]
	v_mfma_i32_16x16x64_i8 v[42:45], v[164:167], v[208:211], v[42:45]
	v_mfma_i32_16x16x64_i8 v[30:33], v[156:159], v[216:219], v[30:33]
	v_mfma_i32_16x16x64_i8 v[26:29], v[164:167], v[216:219], v[26:29]
	v_mfma_i32_16x16x64_i8 v[6:9], v[156:159], v[224:227], v[6:9]
	v_mfma_i32_16x16x64_i8 v[2:5], v[164:167], v[224:227], v[2:5]
	s_setprio 0
	s_setprio 1
	v_mfma_i32_16x16x64_i8 v[54:57], v[168:171], v[196:199], v[54:57]
	v_mfma_i32_16x16x64_i8 v[50:53], v[184:187], v[196:199], v[50:53]
	v_mfma_i32_16x16x64_i8 v[38:41], v[168:171], v[204:207], v[38:41]
	v_mfma_i32_16x16x64_i8 v[34:37], v[184:187], v[204:207], v[34:37]
	v_mfma_i32_16x16x64_i8 v[14:17], v[168:171], v[212:215], v[14:17]
	v_mfma_i32_16x16x64_i8 v[10:13], v[184:187], v[212:215], v[10:13]
	v_mfma_i32_16x16x64_i8 v[22:25], v[168:171], v[220:223], v[22:25]
	v_mfma_i32_16x16x64_i8 v[18:21], v[184:187], v[220:223], v[18:21]
	v_mfma_i32_16x16x64_i8 v[54:57], v[180:183], v[200:203], v[54:57]
	v_mfma_i32_16x16x64_i8 v[50:53], v[188:191], v[200:203], v[50:53]
	v_mfma_i32_16x16x64_i8 v[38:41], v[180:183], v[208:211], v[38:41]
	v_mfma_i32_16x16x64_i8 v[34:37], v[188:191], v[208:211], v[34:37]
	v_mfma_i32_16x16x64_i8 v[14:17], v[180:183], v[216:219], v[14:17]
	v_mfma_i32_16x16x64_i8 v[10:13], v[188:191], v[216:219], v[10:13]
	v_mfma_i32_16x16x64_i8 v[22:25], v[180:183], v[224:227], v[22:25]
	v_mfma_i32_16x16x64_i8 v[18:21], v[188:191], v[224:227], v[18:21]
	s_setprio 0
	s_barrier
	s_add_i32 s71, s71, 2
	s_cmp_gt_u32 s71, 13
	s_mov_b64 s[36:37], s[38:39]
	s_cbranch_scc0 .LBB0_1385
	s_and_b64 vcc, exec, s[20:21]
	s_cbranch_vccz .LBB0_1388
	s_barrier

; #define PG8_STAGE(bufoff, gbase, voff) do { _Pragma("unroll") for (int _i = 0; _i < 2; ++_i) \
;         __builtin_amdgcn_global_load_lds((const unsigned*)((const char*)(gbase) + (voff)[_i]), (LAS unsigned*)(lds + (bufoff) + ldsw + _i * 8192), 16, 0, 0); } while (0)
; #define PG8_LDA(dst, b, h) do { _Pragma("unroll") for (int m = 0; m < 4; ++m) dst[m] = PG8_LD32(lds + PG8_SA(b, h) + aoff + m * 2048); } while (0)
; #define PG8_LDB(dst, b, h) do { _Pragma("unroll") for (int n = 0; n < 2; ++n) dst[n] = PG8_LD32(lds + PG8_SB(b, h) + boff + n * 2048); } while (0)
; #define PG8_WAIT_V(n) asm volatile("s_waitcnt vmcnt(" #n ")" ::: "memory")
; #define PG8_WAIT_L(n) asm volatile("s_waitcnt lgkmcnt(" #n ")" ::: "memory")
; #define PG8_BAR __builtin_amdgcn_s_barrier()
; #define PG8_SCHED __builtin_amdgcn_sched_barrier(0)
; #define PG8_STA(bufoff, nextflag, h, koff) do { if constexpr (Sched::GATHER) { unsigned _o[2]; _o[0] = (nextflag) ? nxtA[h][0] : curA[h][0]; _o[1] = (nextflag) ? nxtA[h][1] : curA[h][1]; PG8_STAGE(bufoff, Ab + (koff), _o); } \
;         else { PG8_STAGE(bufoff, ((nextflag) ? nA : cA) + (size_t)(h) * hstep + (koff), voffA); } } while (0)
; template <class Epi, class Sched, bool ALIGN_EPI, int DT>
; __device__ __forceinline__ void gemm_phase(LAS unsigned char* lds, const int KB, const Sched& S, const Epi& E) {
;     ...
;             PG8_LDB(B0, 0, 0); PG8_LDB(B1, 0, 1); PG8_SCHED; PG8_LDA(At, 0, 0); PG8_STA(PG8_SA(1, 1), false, 1, k1);
;             PG8_WAIT_V(8); PG8_WAIT_L(0); PG8_BAR; PG8_MMA(0, 0, At, B0); PG8_MMA(0, 1, At, B1); PG8_BAR; PG8_SCHED;
;             PG8_LDA(At, 0, 1); PG8_STAGE(PG8_SB(0, 0), b2, voffB); PG8_STAGE(PG8_SB(0, 1), b2 + hstep, voffB); PG8_STA(PG8_SA(0, 0), last, 0, k2);
;             PG8_WAIT_V(8); PG8_WAIT_L(0); PG8_BAR; PG8_MMA(1, 0, At, B0); PG8_MMA(1, 1, At, B1); PG8_BAR; PG8_SCHED;
.LBB0_2108:
	ds_read_b128 v[18:21], v193
	ds_read_b128 v[22:25], v193 offset:1024
	ds_read_b128 v[26:29], v193 offset:2048
	ds_read_b128 v[30:33], v193 offset:3072
	ds_read_b128 v[2:5], v195
	ds_read_b128 v[6:9], v195 offset:1024
	ds_read_b128 v[10:13], v195 offset:2048
	ds_read_b128 v[14:17], v195 offset:3072
	s_add_u32 s38, s42, 0x100
	s_addc_u32 s39, s43, 0
	s_add_u32 s71, s68, s42
	s_addc_u32 s74, s69, s43
	s_cmp_eq_u32 s70, 12
	s_cselect_b64 s[44:45], -1, 0
	s_and_b64 s[40:41], s[44:45], exec
	s_cselect_b32 s41, s25, s74
	s_cselect_b32 s40, s27, s71
	s_cselect_b32 s71, 0, s39
	s_cselect_b32 s74, 0, s38
	v_lshl_add_u64 v[222:223], v[178:179], 0, s[42:43]
	s_add_i32 m0, s35, 0xc000
	ds_read_b128 v[182:185], v196
	ds_read_b128 v[186:189], v196 offset:1024
	ds_read_b128 v[198:201], v196 offset:2048
	ds_read_b128 v[202:205], v196 offset:3072
	ds_read_b128 v[206:209], v196 offset:4096
	ds_read_b128 v[210:213], v196 offset:5120
	ds_read_b128 v[214:217], v196 offset:6144
	ds_read_b128 v[218:221], v196 offset:7168
	global_load_lds_dwordx4 v[222:223], off
	v_lshl_add_u64 v[222:223], v[180:181], 0, s[42:43]
	s_add_i32 m0, s35, 0xe000
	s_nop 0
	global_load_lds_dwordx4 v[222:223], off
	s_nop 0
	s_waitcnt vmcnt(8)
	s_waitcnt lgkmcnt(0)
	s_barrier
	s_setprio 1
	s_waitcnt lgkmcnt(0)
	v_mfma_scale_f32_16x16x128_f8f6f4 v[158:161], v[18:25], v[182:189], v[158:161], v1, v1 op_sel_hi:[0,0,0]
	v_mfma_scale_f32_16x16x128_f8f6f4 v[154:157], v[26:33], v[182:189], v[154:157], v1, v1 op_sel_hi:[0,0,0]
	v_mfma_scale_f32_16x16x128_f8f6f4 v[150:153], v[18:25], v[198:205], v[150:153], v1, v1 op_sel_hi:[0,0,0]
	v_mfma_scale_f32_16x16x128_f8f6f4 v[142:145], v[26:33], v[198:205], v[142:145], v1, v1 op_sel_hi:[0,0,0]
	v_mfma_scale_f32_16x16x128_f8f6f4 v[134:137], v[18:25], v[206:213], v[134:137], v1, v1 op_sel_hi:[0,0,0]
	v_mfma_scale_f32_16x16x128_f8f6f4 v[126:129], v[26:33], v[206:213], v[126:129], v1, v1 op_sel_hi:[0,0,0]
	v_mfma_scale_f32_16x16x128_f8f6f4 v[118:121], v[18:25], v[214:221], v[118:121], v1, v1 op_sel_hi:[0,0,0]
	v_mfma_scale_f32_16x16x128_f8f6f4 v[110:113], v[26:33], v[214:221], v[110:113], v1, v1 op_sel_hi:[0,0,0]
	s_setprio 0
	s_setprio 1
	v_mfma_scale_f32_16x16x128_f8f6f4 v[146:149], v[2:9], v[182:189], v[146:149], v1, v1 op_sel_hi:[0,0,0]
	v_mfma_scale_f32_16x16x128_f8f6f4 v[138:141], v[10:17], v[182:189], v[138:141], v1, v1 op_sel_hi:[0,0,0]
	v_mfma_scale_f32_16x16x128_f8f6f4 v[130:133], v[2:9], v[198:205], v[130:133], v1, v1 op_sel_hi:[0,0,0]
	v_mfma_scale_f32_16x16x128_f8f6f4 v[122:125], v[10:17], v[198:205], v[122:125], v1, v1 op_sel_hi:[0,0,0]
	v_mfma_scale_f32_16x16x128_f8f6f4 v[114:117], v[2:9], v[206:213], v[114:117], v1, v1 op_sel_hi:[0,0,0]
	v_mfma_scale_f32_16x16x128_f8f6f4 v[106:109], v[10:17], v[206:213], v[106:109], v1, v1 op_sel_hi:[0,0,0]
	v_mfma_scale_f32_16x16x128_f8f6f4 v[102:105], v[2:9], v[214:221], v[102:105], v1, v1 op_sel_hi:[0,0,0]
	v_mfma_scale_f32_16x16x128_f8f6f4 v[98:101], v[10:17], v[214:221], v[98:101], v1, v1 op_sel_hi:[0,0,0]
	s_setprio 0
	s_barrier
	s_add_i32 s42, s57, s46
	v_lshl_add_u64 v[182:183], s[40:41], 0, v[162:163]
	s_mov_b32 m0, s42
	ds_read_b128 v[198:201], v196 offset:16384
	ds_read_b128 v[202:205], v196 offset:17408
	ds_read_b128 v[206:209], v196 offset:18432
	ds_read_b128 v[210:213], v196 offset:19456
	ds_read_b128 v[214:217], v196 offset:20480
	ds_read_b128 v[218:221], v196 offset:21504
	ds_read_b128 v[222:225], v196 offset:22528
	ds_read_b128 v[226:229], v196 offset:23552
	global_load_lds_dwordx4 v[182:183], off
	s_add_i32 m0, s42, 0x2000
	s_add_u32 s42, s40, 0x40000
	v_lshl_add_u64 v[184:185], s[40:41], 0, v[164:165]
	s_addc_u32 s43, s41, 0
	s_add_i32 s75, s62, s46
	global_load_lds_dwordx4 v[184:185], off
	v_lshl_add_u64 v[186:187], s[42:43], 0, v[162:163]
	s_mov_b32 m0, s75
	s_nop 0
	global_load_lds_dwordx4 v[186:187], off
	v_lshl_add_u64 v[186:187], s[42:43], 0, v[164:165]
	s_add_i32 m0, s75, 0x2000
	s_and_b64 s[42:43], s[6:7], s[44:45]
	s_and_b64 s[42:43], s[42:43], exec
	s_cselect_b32 s42, s28, s36
	s_cselect_b32 s43, s29, s37
	s_add_u32 s42, s42, s74
	s_addc_u32 s43, s43, s71
	global_load_lds_dwordx4 v[186:187], off
	v_lshl_add_u64 v[186:187], s[42:43], 0, v[166:167]
	s_mov_b32 m0, s35
	v_lshl_add_u64 v[188:189], s[42:43], 0, v[168:169]
	global_load_lds_dwordx4 v[186:187], off
	s_mov_b32 m0, s47
	s_nop 0
	global_load_lds_dwordx4 v[188:189], off
	s_waitcnt vmcnt(8)
	s_waitcnt lgkmcnt(0)
	s_barrier
	s_setprio 1
	s_waitcnt lgkmcnt(0)
	v_mfma_scale_f32_16x16x128_f8f6f4 v[94:97], v[18:25], v[198:205], v[94:97], v1, v1 op_sel_hi:[0,0,0]
	v_mfma_scale_f32_16x16x128_f8f6f4 v[90:93], v[26:33], v[198:205], v[90:93], v1, v1 op_sel_hi:[0,0,0]
	v_mfma_scale_f32_16x16x128_f8f6f4 v[86:89], v[18:25], v[206:213], v[86:89], v1, v1 op_sel_hi:[0,0,0]
	v_mfma_scale_f32_16x16x128_f8f6f4 v[78:81], v[26:33], v[206:213], v[78:81], v1, v1 op_sel_hi:[0,0,0]
	v_mfma_scale_f32_16x16x128_f8f6f4 v[62:65], v[18:25], v[214:221], v[62:65], v1, v1 op_sel_hi:[0,0,0]
	v_mfma_scale_f32_16x16x128_f8f6f4 v[54:57], v[26:33], v[214:221], v[54:57], v1, v1 op_sel_hi:[0,0,0]
	v_mfma_scale_f32_16x16x128_f8f6f4 v[46:49], v[18:25], v[222:229], v[46:49], v1, v1 op_sel_hi:[0,0,0]
	v_mfma_scale_f32_16x16x128_f8f6f4 v[38:41], v[26:33], v[222:229], v[38:41], v1, v1 op_sel_hi:[0,0,0]
	s_setprio 0
	s_setprio 1
	v_mfma_scale_f32_16x16x128_f8f6f4 v[82:85], v[2:9], v[198:205], v[82:85], v1, v1 op_sel_hi:[0,0,0]
	v_mfma_scale_f32_16x16x128_f8f6f4 v[74:77], v[10:17], v[198:205], v[74:77], v1, v1 op_sel_hi:[0,0,0]
	v_mfma_scale_f32_16x16x128_f8f6f4 v[58:61], v[2:9], v[206:213], v[58:61], v1, v1 op_sel_hi:[0,0,0]
	v_mfma_scale_f32_16x16x128_f8f6f4 v[50:53], v[10:17], v[206:213], v[50:53], v1, v1 op_sel_hi:[0,0,0]
	v_mfma_scale_f32_16x16x128_f8f6f4 v[42:45], v[2:9], v[214:221], v[42:45], v1, v1 op_sel_hi:[0,0,0]
	v_mfma_scale_f32_16x16x128_f8f6f4 v[34:37], v[10:17], v[214:221], v[34:37], v1, v1 op_sel_hi:[0,0,0]
	v_mfma_scale_f32_16x16x128_f8f6f4 v[70:73], v[2:9], v[222:229], v[70:73], v1, v1 op_sel_hi:[0,0,0]
	v_mfma_scale_f32_16x16x128_f8f6f4 v[66:69], v[10:17], v[222:229], v[66:69], v1, v1 op_sel_hi:[0,0,0]
	s_setprio 0
	s_barrier
; #define PG8_STAGE(bufoff, gbase, voff) do { _Pragma("unroll") for (int _i = 0; _i < 2; ++_i) \
;         __builtin_amdgcn_global_load_lds((const unsigned*)((const char*)(gbase) + (voff)[_i]), (LAS unsigned*)(lds + (bufoff) + ldsw + _i * 8192), 16, 0, 0); } while (0)
; #define PG8_LDA(dst, b, h) do { _Pragma("unroll") for (int m = 0; m < 4; ++m) dst[m] = PG8_LD32(lds + PG8_SA(b, h) + aoff + m * 2048); } while (0)
; #define PG8_LDB(dst, b, h) do { _Pragma("unroll") for (int n = 0; n < 2; ++n) dst[n] = PG8_LD32(lds + PG8_SB(b, h) + boff + n * 2048); } while (0)
; #define PG8_WAIT_V(n) asm volatile("s_waitcnt vmcnt(" #n ")" ::: "memory")
; #define PG8_WAIT_L(n) asm volatile("s_waitcnt lgkmcnt(" #n ")" ::: "memory")
; #define PG8_BAR __builtin_amdgcn_s_barrier()
; #define PG8_SCHED __builtin_amdgcn_sched_barrier(0)
; #define PG8_STA(bufoff, nextflag, h, koff) do { if constexpr (Sched::GATHER) { unsigned _o[2]; _o[0] = (nextflag) ? nxtA[h][0] : curA[h][0]; _o[1] = (nextflag) ? nxtA[h][1] : curA[h][1]; PG8_STAGE(bufoff, Ab + (koff), _o); } \
;         else { PG8_STAGE(bufoff, ((nextflag) ? nA : cA) + (size_t)(h) * hstep + (koff), voffA); } } while (0)
; template <class Epi, class Sched, bool ALIGN_EPI, int DT>
; __device__ __forceinline__ void gemm_phase(LAS unsigned char* lds, const int KB, const Sched& S, const Epi& E) {
;     ...
;             PG8_LDB(B0, 1, 0); PG8_LDB(B1, 1, 1); PG8_SCHED; PG8_LDA(At, 1, 0); PG8_STA(PG8_SA(0, 1), last, 1, k2);
;             PG8_WAIT_V(8); PG8_WAIT_L(0); PG8_BAR; PG8_MMA(0, 0, At, B0); PG8_MMA(0, 1, At, B1); PG8_BAR; PG8_SCHED;
;             PG8_LDA(At, 1, 1); PG8_STAGE(PG8_SB(1, 0), b3, voffB); PG8_STAGE(PG8_SB(1, 1), b3 + hstep, voffB); PG8_STA(PG8_SA(1, 0), last, 0, k3);
;             PG8_WAIT_V(8); PG8_WAIT_L(0); PG8_BAR; PG8_MMA(1, 0, At, B0); PG8_MMA(1, 1, At, B1); PG8_BAR; PG8_SCHED;
;         }
;         if constexpr (ALIGN_EPI) { if (wr == 0) PG8_BAR; }
	s_add_i32 s44, 0, 0x18000
	s_add_i32 s45, 0, 0x1c000
	v_add_u32_e32 v14, s44, v191
	v_add_u32_e32 v30, s45, v191
	ds_read_b128 v[2:5], v14
	ds_read_b128 v[6:9], v14 offset:1024
	ds_read_b128 v[10:13], v14 offset:2048
	ds_read_b128 v[14:17], v14 offset:3072
	ds_read_b128 v[18:21], v30
	ds_read_b128 v[22:25], v30 offset:1024
	ds_read_b128 v[26:29], v30 offset:2048
	ds_read_b128 v[30:33], v30 offset:3072
	s_add_u32 s42, s42, 0x40000
	s_addc_u32 s43, s43, 0
	s_mov_b32 m0, s49
	v_lshl_add_u64 v[230:231], s[42:43], 0, v[166:167]
	ds_read_b128 v[198:201], v196 offset:32768
	ds_read_b128 v[202:205], v196 offset:33792
	ds_read_b128 v[206:209], v196 offset:34816
	ds_read_b128 v[210:213], v196 offset:35840
	ds_read_b128 v[214:217], v196 offset:36864
	ds_read_b128 v[218:221], v196 offset:37888
	ds_read_b128 v[222:225], v196 offset:38912
	ds_read_b128 v[226:229], v196 offset:39936
	global_load_lds_dwordx4 v[230:231], off
	v_lshl_add_u64 v[230:231], s[42:43], 0, v[168:169]
	s_mov_b32 m0, s52
	s_nop 0
	global_load_lds_dwordx4 v[230:231], off
	s_nop 0
	s_waitcnt vmcnt(8)
	s_waitcnt lgkmcnt(0)
	s_barrier
	s_setprio 1
	s_waitcnt lgkmcnt(0)
	v_mfma_scale_f32_16x16x128_f8f6f4 v[158:161], v[2:9], v[198:205], v[158:161], v1, v1 op_sel_hi:[0,0,0]
	v_mfma_scale_f32_16x16x128_f8f6f4 v[154:157], v[10:17], v[198:205], v[154:157], v1, v1 op_sel_hi:[0,0,0]
	v_mfma_scale_f32_16x16x128_f8f6f4 v[150:153], v[2:9], v[206:213], v[150:153], v1, v1 op_sel_hi:[0,0,0]
	v_mfma_scale_f32_16x16x128_f8f6f4 v[142:145], v[10:17], v[206:213], v[142:145], v1, v1 op_sel_hi:[0,0,0]
	v_mfma_scale_f32_16x16x128_f8f6f4 v[134:137], v[2:9], v[214:221], v[134:137], v1, v1 op_sel_hi:[0,0,0]
	v_mfma_scale_f32_16x16x128_f8f6f4 v[126:129], v[10:17], v[214:221], v[126:129], v1, v1 op_sel_hi:[0,0,0]
	v_mfma_scale_f32_16x16x128_f8f6f4 v[118:121], v[2:9], v[222:229], v[118:121], v1, v1 op_sel_hi:[0,0,0]
	v_mfma_scale_f32_16x16x128_f8f6f4 v[110:113], v[10:17], v[222:229], v[110:113], v1, v1 op_sel_hi:[0,0,0]
	s_setprio 0
	s_setprio 1
	v_mfma_scale_f32_16x16x128_f8f6f4 v[146:149], v[18:25], v[198:205], v[146:149], v1, v1 op_sel_hi:[0,0,0]
	v_mfma_scale_f32_16x16x128_f8f6f4 v[138:141], v[26:33], v[198:205], v[138:141], v1, v1 op_sel_hi:[0,0,0]
	v_mfma_scale_f32_16x16x128_f8f6f4 v[130:133], v[18:25], v[206:213], v[130:133], v1, v1 op_sel_hi:[0,0,0]
	v_mfma_scale_f32_16x16x128_f8f6f4 v[122:125], v[26:33], v[206:213], v[122:125], v1, v1 op_sel_hi:[0,0,0]
	v_mfma_scale_f32_16x16x128_f8f6f4 v[114:117], v[18:25], v[214:221], v[114:117], v1, v1 op_sel_hi:[0,0,0]
	v_mfma_scale_f32_16x16x128_f8f6f4 v[106:109], v[26:33], v[214:221], v[106:109], v1, v1 op_sel_hi:[0,0,0]
	v_mfma_scale_f32_16x16x128_f8f6f4 v[102:105], v[18:25], v[222:229], v[102:105], v1, v1 op_sel_hi:[0,0,0]
	v_mfma_scale_f32_16x16x128_f8f6f4 v[98:101], v[26:33], v[222:229], v[98:101], v1, v1 op_sel_hi:[0,0,0]
	s_setprio 0
	s_barrier
	s_add_i32 s42, s44, s46
	v_lshl_add_u64 v[182:183], v[182:183], 0, s[10:11]
	s_mov_b32 m0, s42
	ds_read_b128 v[198:201], v196 offset:49152
	ds_read_b128 v[202:205], v196 offset:50176
	ds_read_b128 v[206:209], v196 offset:51200
	ds_read_b128 v[210:213], v196 offset:52224
	ds_read_b128 v[214:217], v196 offset:53248
	ds_read_b128 v[218:221], v196 offset:54272
	ds_read_b128 v[222:225], v196 offset:55296
	ds_read_b128 v[226:229], v196 offset:56320
	global_load_lds_dwordx4 v[182:183], off
	s_add_i32 m0, s42, 0x2000
	s_add_u32 s40, s40, 0x40080
	v_lshl_add_u64 v[182:183], v[184:185], 0, s[10:11]
	s_addc_u32 s41, s41, 0
	s_add_i32 s42, s45, s46
	global_load_lds_dwordx4 v[182:183], off
	v_lshl_add_u64 v[182:183], s[40:41], 0, v[162:163]
	s_mov_b32 m0, s42
	s_nop 0
	global_load_lds_dwordx4 v[182:183], off
	v_lshl_add_u64 v[182:183], s[40:41], 0, v[164:165]
	s_add_i32 m0, s42, 0x2000
	s_nop 0
	global_load_lds_dwordx4 v[182:183], off
	v_lshl_add_u64 v[182:183], v[186:187], 0, s[10:11]
	s_mov_b32 m0, s54
	s_nop 0
	global_load_lds_dwordx4 v[182:183], off
	v_lshl_add_u64 v[182:183], v[188:189], 0, s[10:11]
	s_mov_b32 m0, s55
	s_nop 0
	global_load_lds_dwordx4 v[182:183], off
	s_waitcnt vmcnt(8)
	s_waitcnt lgkmcnt(0)
	s_barrier
	s_setprio 1
	s_waitcnt lgkmcnt(0)
	v_mfma_scale_f32_16x16x128_f8f6f4 v[94:97], v[2:9], v[198:205], v[94:97], v1, v1 op_sel_hi:[0,0,0]
	v_mfma_scale_f32_16x16x128_f8f6f4 v[90:93], v[10:17], v[198:205], v[90:93], v1, v1 op_sel_hi:[0,0,0]
	v_mfma_scale_f32_16x16x128_f8f6f4 v[86:89], v[2:9], v[206:213], v[86:89], v1, v1 op_sel_hi:[0,0,0]
	v_mfma_scale_f32_16x16x128_f8f6f4 v[78:81], v[10:17], v[206:213], v[78:81], v1, v1 op_sel_hi:[0,0,0]
	v_mfma_scale_f32_16x16x128_f8f6f4 v[62:65], v[2:9], v[214:221], v[62:65], v1, v1 op_sel_hi:[0,0,0]
	v_mfma_scale_f32_16x16x128_f8f6f4 v[54:57], v[10:17], v[214:221], v[54:57], v1, v1 op_sel_hi:[0,0,0]
	v_mfma_scale_f32_16x16x128_f8f6f4 v[46:49], v[2:9], v[222:229], v[46:49], v1, v1 op_sel_hi:[0,0,0]
	v_mfma_scale_f32_16x16x128_f8f6f4 v[38:41], v[10:17], v[222:229], v[38:41], v1, v1 op_sel_hi:[0,0,0]
	s_setprio 0
	s_setprio 1
	v_mfma_scale_f32_16x16x128_f8f6f4 v[82:85], v[18:25], v[198:205], v[82:85], v1, v1 op_sel_hi:[0,0,0]
	v_mfma_scale_f32_16x16x128_f8f6f4 v[74:77], v[26:33], v[198:205], v[74:77], v1, v1 op_sel_hi:[0,0,0]
	v_mfma_scale_f32_16x16x128_f8f6f4 v[58:61], v[18:25], v[206:213], v[58:61], v1, v1 op_sel_hi:[0,0,0]
	v_mfma_scale_f32_16x16x128_f8f6f4 v[50:53], v[26:33], v[206:213], v[50:53], v1, v1 op_sel_hi:[0,0,0]
	v_mfma_scale_f32_16x16x128_f8f6f4 v[42:45], v[18:25], v[214:221], v[42:45], v1, v1 op_sel_hi:[0,0,0]
	v_mfma_scale_f32_16x16x128_f8f6f4 v[34:37], v[26:33], v[214:221], v[34:37], v1, v1 op_sel_hi:[0,0,0]
	v_mfma_scale_f32_16x16x128_f8f6f4 v[70:73], v[18:25], v[222:229], v[70:73], v1, v1 op_sel_hi:[0,0,0]
	v_mfma_scale_f32_16x16x128_f8f6f4 v[66:69], v[26:33], v[222:229], v[66:69], v1, v1 op_sel_hi:[0,0,0]
	s_setprio 0
	s_barrier
	s_add_i32 s70, s70, 2
	s_cmp_gt_u32 s70, 13
	s_mov_b64 s[42:43], s[38:39]
	s_cbranch_scc0 .LBB0_2108
	s_and_b64 vcc, exec, s[12:13]
	s_cbranch_vccz .LBB0_2111
	s_barrier

; #define PG8_STAGE(bufoff, gbase, voff) do { _Pragma("unroll") for (int _i = 0; _i < 2; ++_i) \
;         __builtin_amdgcn_global_load_lds((const unsigned*)((const char*)(gbase) + (voff)[_i]), (LAS unsigned*)(lds + (bufoff) + ldsw + _i * 8192), 16, 0, 0); } while (0)
; #define PG8_LDA(dst, b, h) do { _Pragma("unroll") for (int m = 0; m < 4; ++m) dst[m] = PG8_LD32(lds + PG8_SA(b, h) + aoff + m * 2048); } while (0)
; #define PG8_LDB(dst, b, h) do { _Pragma("unroll") for (int n = 0; n < 2; ++n) dst[n] = PG8_LD32(lds + PG8_SB(b, h) + boff + n * 2048); } while (0)
; #define PG8_WAIT_V(n) asm volatile("s_waitcnt vmcnt(" #n ")" ::: "memory")
; #define PG8_WAIT_L(n) asm volatile("s_waitcnt lgkmcnt(" #n ")" ::: "memory")
; #define PG8_BAR __builtin_amdgcn_s_barrier()
; #define PG8_SCHED __builtin_amdgcn_sched_barrier(0)
; #define PG8_STA(bufoff, nextflag, h, koff) do { if constexpr (Sched::GATHER) { unsigned _o[2]; _o[0] = (nextflag) ? nxtA[h][0] : curA[h][0]; _o[1] = (nextflag) ? nxtA[h][1] : curA[h][1]; PG8_STAGE(bufoff, Ab + (koff), _o); } \
;         else { PG8_STAGE(bufoff, ((nextflag) ? nA : cA) + (size_t)(h) * hstep + (koff), voffA); } } while (0)
; template <class Epi, class Sched, bool ALIGN_EPI, int DT>
; __device__ __forceinline__ void gemm_phase(LAS unsigned char* lds, const int KB, const Sched& S, const Epi& E) {
;     ...
;             PG8_LDB(B0, 0, 0); PG8_LDB(B1, 0, 1); PG8_SCHED; PG8_LDA(At, 0, 0); PG8_STA(PG8_SA(1, 1), false, 1, k1);
;             PG8_WAIT_V(8); PG8_WAIT_L(0); PG8_BAR; PG8_MMA(0, 0, At, B0); PG8_MMA(0, 1, At, B1); PG8_BAR; PG8_SCHED;
;             PG8_LDA(At, 0, 1); PG8_STAGE(PG8_SB(0, 0), b2, voffB); PG8_STAGE(PG8_SB(0, 1), b2 + hstep, voffB); PG8_STA(PG8_SA(0, 0), last, 0, k2);
;             PG8_WAIT_V(8); PG8_WAIT_L(0); PG8_BAR; PG8_MMA(1, 0, At, B0); PG8_MMA(1, 1, At, B1); PG8_BAR; PG8_SCHED;
.LBB0_2294:
	v_add_u32_e32 v79, s65, v167
	ds_read_b128 v[142:145], v79
	ds_read_b128 v[156:159], v79 offset:1024
	ds_read_b128 v[178:181], v79 offset:2048
	ds_read_b128 v[182:185], v79 offset:3072
	v_add_u32_e32 v79, s66, v167
	ds_read_b128 v[186:189], v79
	ds_read_b128 v[190:193], v79 offset:1024
	ds_read_b128 v[196:199], v79 offset:2048
	ds_read_b128 v[200:203], v79 offset:3072
	s_add_u32 s40, s8, 0x100
	s_addc_u32 s41, s9, 0
	s_cmpk_eq_i32 s8, 0x700
	s_cselect_b64 vcc, -1, 0
	v_lshl_add_u64 v[160:161], v[88:89], 0, s[8:9]
	s_and_b64 s[76:77], vcc, exec
	v_cndmask_b32_e32 v161, v161, v155, vcc
	s_cselect_b32 s75, 0, s40
	v_cndmask_b32_e32 v160, v160, v154, vcc
	v_lshl_add_u64 v[236:237], v[140:141], 0, s[8:9]
	s_add_i32 m0, s42, 0xc000
	ds_read_b128 v[204:207], v169
	ds_read_b128 v[208:211], v169 offset:1024
	ds_read_b128 v[212:215], v169 offset:2048
	ds_read_b128 v[216:219], v169 offset:3072
	ds_read_b128 v[220:223], v169 offset:4096
	ds_read_b128 v[224:227], v169 offset:5120
	ds_read_b128 v[228:231], v169 offset:6144
	ds_read_b128 v[232:235], v169 offset:7168
	global_load_lds_dwordx4 v[236:237], off
	v_lshl_add_u64 v[236:237], v[138:139], 0, s[8:9]
	s_add_i32 m0, s42, 0xe000
	s_nop 0
	global_load_lds_dwordx4 v[236:237], off
	s_nop 0
	s_waitcnt vmcnt(8)
	s_waitcnt lgkmcnt(0)
	s_barrier
	s_setprio 1
	s_waitcnt lgkmcnt(0)
	v_mfma_i32_16x16x64_i8 v[134:137], v[142:145], v[204:207], v[134:137]
	v_mfma_i32_16x16x64_i8 v[126:129], v[178:181], v[204:207], v[126:129]
	v_mfma_i32_16x16x64_i8 v[118:121], v[142:145], v[212:215], v[118:121]
	v_mfma_i32_16x16x64_i8 v[110:113], v[178:181], v[212:215], v[110:113]
	v_mfma_i32_16x16x64_i8 v[102:105], v[142:145], v[220:223], v[102:105]
	v_mfma_i32_16x16x64_i8 v[94:97], v[178:181], v[220:223], v[94:97]
	v_mfma_i32_16x16x64_i8 v[82:85], v[142:145], v[228:231], v[82:85]
	v_mfma_i32_16x16x64_i8 v[70:73], v[178:181], v[228:231], v[70:73]
	v_mfma_i32_16x16x64_i8 v[134:137], v[156:159], v[208:211], v[134:137]
	v_mfma_i32_16x16x64_i8 v[126:129], v[182:185], v[208:211], v[126:129]
	v_mfma_i32_16x16x64_i8 v[118:121], v[156:159], v[216:219], v[118:121]
	v_mfma_i32_16x16x64_i8 v[110:113], v[182:185], v[216:219], v[110:113]
	v_mfma_i32_16x16x64_i8 v[102:105], v[156:159], v[224:227], v[102:105]
	v_mfma_i32_16x16x64_i8 v[94:97], v[182:185], v[224:227], v[94:97]
	v_mfma_i32_16x16x64_i8 v[82:85], v[156:159], v[232:235], v[82:85]
	v_mfma_i32_16x16x64_i8 v[70:73], v[182:185], v[232:235], v[70:73]
	s_setprio 0
	s_setprio 1
	v_mfma_i32_16x16x64_i8 v[130:133], v[186:189], v[204:207], v[130:133]
	v_mfma_i32_16x16x64_i8 v[122:125], v[196:199], v[204:207], v[122:125]
	v_mfma_i32_16x16x64_i8 v[114:117], v[186:189], v[212:215], v[114:117]
	v_mfma_i32_16x16x64_i8 v[106:109], v[196:199], v[212:215], v[106:109]
	v_mfma_i32_16x16x64_i8 v[98:101], v[186:189], v[220:223], v[98:101]
	v_mfma_i32_16x16x64_i8 v[90:93], v[196:199], v[220:223], v[90:93]
	v_mfma_i32_16x16x64_i8 v[74:77], v[186:189], v[228:231], v[74:77]
	v_mfma_i32_16x16x64_i8 v[66:69], v[196:199], v[228:231], v[66:69]
	v_mfma_i32_16x16x64_i8 v[130:133], v[190:193], v[208:211], v[130:133]
	v_mfma_i32_16x16x64_i8 v[122:125], v[200:203], v[208:211], v[122:125]
	v_mfma_i32_16x16x64_i8 v[114:117], v[190:193], v[216:219], v[114:117]
	v_mfma_i32_16x16x64_i8 v[106:109], v[200:203], v[216:219], v[106:109]
	v_mfma_i32_16x16x64_i8 v[98:101], v[190:193], v[224:227], v[98:101]
	v_mfma_i32_16x16x64_i8 v[90:93], v[200:203], v[224:227], v[90:93]
	v_mfma_i32_16x16x64_i8 v[74:77], v[190:193], v[232:235], v[74:77]
	v_mfma_i32_16x16x64_i8 v[66:69], v[200:203], v[232:235], v[66:69]
	s_setprio 0
	s_barrier
	s_add_i32 s8, s65, s33
	v_lshl_add_u64 v[236:237], v[160:161], 0, v[148:149]
	s_mov_b32 m0, s8
	ds_read_b128 v[204:207], v169 offset:16384
	ds_read_b128 v[208:211], v169 offset:17408
	ds_read_b128 v[212:215], v169 offset:18432
	ds_read_b128 v[216:219], v169 offset:19456
	ds_read_b128 v[220:223], v169 offset:20480
	ds_read_b128 v[224:227], v169 offset:21504
	ds_read_b128 v[228:231], v169 offset:22528
	ds_read_b128 v[232:235], v169 offset:23552
	global_load_lds_dwordx4 v[236:237], off
	v_lshl_add_u64 v[238:239], v[160:161], 0, v[150:151]
	s_add_i32 m0, s8, 0x2000
	v_lshl_add_u64 v[240:241], v[160:161], 0, s[10:11]
	s_add_i32 s8, s66, s33
	global_load_lds_dwordx4 v[238:239], off
	v_lshl_add_u64 v[242:243], v[240:241], 0, v[148:149]
	s_mov_b32 m0, s8
	v_lshl_add_u64 v[240:241], v[240:241], 0, v[150:151]
	global_load_lds_dwordx4 v[242:243], off
	s_add_i32 m0, s8, 0x2000
	s_add_u32 s8, s60, s75
	global_load_lds_dwordx4 v[240:241], off
	v_cndmask_b32_e32 v146, v81, v173, vcc
	s_addc_u32 s9, s61, 0
	s_mov_b32 m0, s42
	v_cndmask_b32_e32 v240, v80, v174, vcc
	global_load_lds_dwordx4 v146, s[8:9]
	s_mov_b32 m0, s43
	v_mov_b32_e32 v241, v147
	global_load_lds_dwordx4 v240, s[8:9]
	s_waitcnt vmcnt(8)
	s_waitcnt lgkmcnt(0)
	v_lshl_add_u64 v[242:243], s[8:9], 0, v[146:147]
	v_lshl_add_u64 v[240:241], s[8:9], 0, v[240:241]
	s_barrier
; #define PG8_LDA(dst, b, h) do { _Pragma("unroll") for (int m = 0; m < 4; ++m) dst[m] = PG8_LD32(lds + PG8_SA(b, h) + aoff + m * 2048); } while (0)
; #define PG8_LDB(dst, b, h) do { _Pragma("unroll") for (int n = 0; n < 2; ++n) dst[n] = PG8_LD32(lds + PG8_SB(b, h) + boff + n * 2048); } while (0)
; #define PG8_WAIT_V(n) asm volatile("s_waitcnt vmcnt(" #n ")" ::: "memory")
; #define PG8_WAIT_L(n) asm volatile("s_waitcnt lgkmcnt(" #n ")" ::: "memory")
; #define PG8_BAR __builtin_amdgcn_s_barrier()
; #define PG8_SCHED __builtin_amdgcn_sched_barrier(0)
; #define PG8_STA(bufoff, nextflag, h, koff) do { if constexpr (Sched::GATHER) { unsigned _o[2]; _o[0] = (nextflag) ? nxtA[h][0] : curA[h][0]; _o[1] = (nextflag) ? nxtA[h][1] : curA[h][1]; PG8_STAGE(bufoff, Ab + (koff), _o); } \
;         else { PG8_STAGE(bufoff, ((nextflag) ? nA : cA) + (size_t)(h) * hstep + (koff), voffA); } } while (0)
; template <class Epi, class Sched, bool ALIGN_EPI, int DT>
; __device__ __forceinline__ void gemm_phase(LAS unsigned char* lds, const int KB, const Sched& S, const Epi& E) {
;     ...
;             PG8_WAIT_V(8); PG8_WAIT_L(0); PG8_BAR; PG8_MMA(1, 0, At, B0); PG8_MMA(1, 1, At, B1); PG8_BAR; PG8_SCHED;
;             PG8_LDB(B0, 1, 0); PG8_LDB(B1, 1, 1); PG8_SCHED; PG8_LDA(At, 1, 0); PG8_STA(PG8_SA(0, 1), last, 1, k2);
;             PG8_WAIT_V(8); PG8_WAIT_L(0); PG8_BAR; PG8_MMA(0, 0, At, B0); PG8_MMA(0, 1, At, B1); PG8_BAR; PG8_SCHED;
	s_setprio 1
	s_waitcnt lgkmcnt(0)
	v_mfma_i32_16x16x64_i8 v[54:57], v[142:145], v[204:207], v[54:57]
	v_mfma_i32_16x16x64_i8 v[50:53], v[178:181], v[204:207], v[50:53]
	v_mfma_i32_16x16x64_i8 v[42:45], v[142:145], v[212:215], v[42:45]
	v_mfma_i32_16x16x64_i8 v[34:37], v[178:181], v[212:215], v[34:37]
	v_mfma_i32_16x16x64_i8 v[26:29], v[142:145], v[220:223], v[26:29]
	v_mfma_i32_16x16x64_i8 v[18:21], v[178:181], v[220:223], v[18:21]
	v_mfma_i32_16x16x64_i8 v[10:13], v[142:145], v[228:231], v[10:13]
	v_mfma_i32_16x16x64_i8 v[2:5], v[178:181], v[228:231], v[2:5]
	v_mfma_i32_16x16x64_i8 v[54:57], v[156:159], v[208:211], v[54:57]
	v_mfma_i32_16x16x64_i8 v[50:53], v[182:185], v[208:211], v[50:53]
	v_mfma_i32_16x16x64_i8 v[42:45], v[156:159], v[216:219], v[42:45]
	v_mfma_i32_16x16x64_i8 v[34:37], v[182:185], v[216:219], v[34:37]
	v_mfma_i32_16x16x64_i8 v[26:29], v[156:159], v[224:227], v[26:29]
	v_mfma_i32_16x16x64_i8 v[18:21], v[182:185], v[224:227], v[18:21]
	v_mfma_i32_16x16x64_i8 v[10:13], v[156:159], v[232:235], v[10:13]
	v_mfma_i32_16x16x64_i8 v[2:5], v[182:185], v[232:235], v[2:5]
	s_setprio 0
	s_setprio 1
	v_mfma_i32_16x16x64_i8 v[62:65], v[186:189], v[204:207], v[62:65]
	v_mfma_i32_16x16x64_i8 v[58:61], v[196:199], v[204:207], v[58:61]
	v_mfma_i32_16x16x64_i8 v[46:49], v[186:189], v[212:215], v[46:49]
	v_mfma_i32_16x16x64_i8 v[38:41], v[196:199], v[212:215], v[38:41]
	v_mfma_i32_16x16x64_i8 v[30:33], v[186:189], v[220:223], v[30:33]
	v_mfma_i32_16x16x64_i8 v[22:25], v[196:199], v[220:223], v[22:25]
	v_mfma_i32_16x16x64_i8 v[14:17], v[186:189], v[228:231], v[14:17]
	v_mfma_i32_16x16x64_i8 v[6:9], v[196:199], v[228:231], v[6:9]
	v_mfma_i32_16x16x64_i8 v[62:65], v[190:193], v[208:211], v[62:65]
	v_mfma_i32_16x16x64_i8 v[58:61], v[200:203], v[208:211], v[58:61]
	v_mfma_i32_16x16x64_i8 v[46:49], v[190:193], v[216:219], v[46:49]
	v_mfma_i32_16x16x64_i8 v[38:41], v[200:203], v[216:219], v[38:41]
	v_mfma_i32_16x16x64_i8 v[30:33], v[190:193], v[224:227], v[30:33]
	v_mfma_i32_16x16x64_i8 v[22:25], v[200:203], v[224:227], v[22:25]
	v_mfma_i32_16x16x64_i8 v[14:17], v[190:193], v[232:235], v[14:17]
	v_mfma_i32_16x16x64_i8 v[6:9], v[200:203], v[232:235], v[6:9]
	s_setprio 0
	s_barrier
	s_add_i32 s75, 0, 0x18000
	v_add_u32_e32 v79, s75, v167
	s_add_i32 s76, 0, 0x1c000
	ds_read_b128 v[142:145], v79
	ds_read_b128 v[156:159], v79 offset:1024
	ds_read_b128 v[178:181], v79 offset:2048
	ds_read_b128 v[182:185], v79 offset:3072
	v_add_u32_e32 v79, s76, v167
	ds_read_b128 v[186:189], v79
	ds_read_b128 v[190:193], v79 offset:1024
	ds_read_b128 v[196:199], v79 offset:2048
	ds_read_b128 v[200:203], v79 offset:3072
	s_mov_b32 m0, s44
	v_cndmask_b32_e32 v79, v78, v175, vcc
	ds_read_b128 v[204:207], v169 offset:32768
	ds_read_b128 v[208:211], v169 offset:33792
	ds_read_b128 v[212:215], v169 offset:34816
	ds_read_b128 v[216:219], v169 offset:35840
	ds_read_b128 v[220:223], v169 offset:36864
	ds_read_b128 v[224:227], v169 offset:37888
	ds_read_b128 v[228:231], v169 offset:38912
	ds_read_b128 v[232:235], v169 offset:39936
	v_cndmask_b32_e32 v87, v86, v176, vcc
	global_load_lds_dwordx4 v79, s[8:9]
	s_mov_b32 m0, s45
	s_nop 0
	global_load_lds_dwordx4 v87, s[8:9]
	s_waitcnt vmcnt(8)
	s_waitcnt lgkmcnt(0)
	s_barrier
	s_setprio 1
	s_waitcnt lgkmcnt(0)
	v_mfma_i32_16x16x64_i8 v[134:137], v[142:145], v[204:207], v[134:137]
	v_mfma_i32_16x16x64_i8 v[126:129], v[178:181], v[204:207], v[126:129]
	v_mfma_i32_16x16x64_i8 v[118:121], v[142:145], v[212:215], v[118:121]
	v_mfma_i32_16x16x64_i8 v[110:113], v[178:181], v[212:215], v[110:113]
	v_mfma_i32_16x16x64_i8 v[102:105], v[142:145], v[220:223], v[102:105]
	v_mfma_i32_16x16x64_i8 v[94:97], v[178:181], v[220:223], v[94:97]
	v_mfma_i32_16x16x64_i8 v[82:85], v[142:145], v[228:231], v[82:85]
	v_mfma_i32_16x16x64_i8 v[70:73], v[178:181], v[228:231], v[70:73]
	v_mfma_i32_16x16x64_i8 v[134:137], v[156:159], v[208:211], v[134:137]
	v_mfma_i32_16x16x64_i8 v[126:129], v[182:185], v[208:211], v[126:129]
	v_mfma_i32_16x16x64_i8 v[118:121], v[156:159], v[216:219], v[118:121]
	v_mfma_i32_16x16x64_i8 v[110:113], v[182:185], v[216:219], v[110:113]
	v_mfma_i32_16x16x64_i8 v[102:105], v[156:159], v[224:227], v[102:105]
	v_mfma_i32_16x16x64_i8 v[94:97], v[182:185], v[224:227], v[94:97]
	v_mfma_i32_16x16x64_i8 v[82:85], v[156:159], v[232:235], v[82:85]
	v_mfma_i32_16x16x64_i8 v[70:73], v[182:185], v[232:235], v[70:73]
	s_setprio 0
	s_setprio 1
	v_mfma_i32_16x16x64_i8 v[130:133], v[186:189], v[204:207], v[130:133]
	v_mfma_i32_16x16x64_i8 v[122:125], v[196:199], v[204:207], v[122:125]
	v_mfma_i32_16x16x64_i8 v[114:117], v[186:189], v[212:215], v[114:117]
	v_mfma_i32_16x16x64_i8 v[106:109], v[196:199], v[212:215], v[106:109]
	v_mfma_i32_16x16x64_i8 v[98:101], v[186:189], v[220:223], v[98:101]
	v_mfma_i32_16x16x64_i8 v[90:93], v[196:199], v[220:223], v[90:93]
	v_mfma_i32_16x16x64_i8 v[74:77], v[186:189], v[228:231], v[74:77]
	v_mfma_i32_16x16x64_i8 v[66:69], v[196:199], v[228:231], v[66:69]
	v_mfma_i32_16x16x64_i8 v[130:133], v[190:193], v[208:211], v[130:133]
	v_mfma_i32_16x16x64_i8 v[122:125], v[200:203], v[208:211], v[122:125]
	v_mfma_i32_16x16x64_i8 v[114:117], v[190:193], v[216:219], v[114:117]
	v_mfma_i32_16x16x64_i8 v[106:109], v[200:203], v[216:219], v[106:109]
	v_mfma_i32_16x16x64_i8 v[98:101], v[190:193], v[224:227], v[98:101]
	v_mfma_i32_16x16x64_i8 v[90:93], v[200:203], v[224:227], v[90:93]
	v_mfma_i32_16x16x64_i8 v[74:77], v[190:193], v[232:235], v[74:77]
	v_mfma_i32_16x16x64_i8 v[66:69], v[200:203], v[232:235], v[66:69]
	s_setprio 0
	s_barrier
; #define PG8_STAGE(bufoff, gbase, voff) do { _Pragma("unroll") for (int _i = 0; _i < 2; ++_i) \
;         __builtin_amdgcn_global_load_lds((const unsigned*)((const char*)(gbase) + (voff)[_i]), (LAS unsigned*)(lds + (bufoff) + ldsw + _i * 8192), 16, 0, 0); } while (0)
; #define PG8_LDA(dst, b, h) do { _Pragma("unroll") for (int m = 0; m < 4; ++m) dst[m] = PG8_LD32(lds + PG8_SA(b, h) + aoff + m * 2048); } while (0)
; #define PG8_WAIT_V(n) asm volatile("s_waitcnt vmcnt(" #n ")" ::: "memory")
; #define PG8_WAIT_L(n) asm volatile("s_waitcnt lgkmcnt(" #n ")" ::: "memory")
; #define PG8_BAR __builtin_amdgcn_s_barrier()
; #define PG8_SCHED __builtin_amdgcn_sched_barrier(0)
; #define PG8_STA(bufoff, nextflag, h, koff) do { if constexpr (Sched::GATHER) { unsigned _o[2]; _o[0] = (nextflag) ? nxtA[h][0] : curA[h][0]; _o[1] = (nextflag) ? nxtA[h][1] : curA[h][1]; PG8_STAGE(bufoff, Ab + (koff), _o); } \
;         else { PG8_STAGE(bufoff, ((nextflag) ? nA : cA) + (size_t)(h) * hstep + (koff), voffA); } } while (0)
; template <class Epi, class Sched, bool ALIGN_EPI, int DT>
; __device__ __forceinline__ void gemm_phase(LAS unsigned char* lds, const int KB, const Sched& S, const Epi& E) {
;     ...
;             PG8_LDA(At, 1, 1); PG8_STAGE(PG8_SB(1, 0), b3, voffB); PG8_STAGE(PG8_SB(1, 1), b3 + hstep, voffB); PG8_STA(PG8_SA(1, 0), last, 0, k3);
;             PG8_WAIT_V(8); PG8_WAIT_L(0); PG8_BAR; PG8_MMA(1, 0, At, B0); PG8_MMA(1, 1, At, B1); PG8_BAR; PG8_SCHED;
;         }
;         if constexpr (ALIGN_EPI) { if (wr == 0) PG8_BAR; }
	s_add_i32 s8, s75, s33
	v_lshl_add_u64 v[236:237], v[236:237], 0, s[20:21]
	s_mov_b32 m0, s8
	ds_read_b128 v[204:207], v169 offset:49152
	ds_read_b128 v[208:211], v169 offset:50176
	ds_read_b128 v[212:215], v169 offset:51200
	ds_read_b128 v[216:219], v169 offset:52224
	ds_read_b128 v[220:223], v169 offset:53248
	ds_read_b128 v[224:227], v169 offset:54272
	ds_read_b128 v[228:231], v169 offset:55296
	ds_read_b128 v[232:235], v169 offset:56320
	global_load_lds_dwordx4 v[236:237], off
	v_lshl_add_u64 v[236:237], v[238:239], 0, s[20:21]
	s_add_i32 m0, s8, 0x2000
	v_lshl_add_u64 v[160:161], v[160:161], 0, s[24:25]
	s_add_i32 s8, s76, s33
	global_load_lds_dwordx4 v[236:237], off
	v_lshl_add_u64 v[236:237], v[160:161], 0, v[148:149]
	s_mov_b32 m0, s8
	v_lshl_add_u64 v[160:161], v[160:161], 0, v[150:151]
	global_load_lds_dwordx4 v[236:237], off
	s_add_i32 m0, s8, 0x2000
	s_nop 0
	global_load_lds_dwordx4 v[160:161], off
	v_lshl_add_u64 v[160:161], v[242:243], 0, s[20:21]
	s_mov_b32 m0, s46
	s_nop 0
	global_load_lds_dwordx4 v[160:161], off
	v_lshl_add_u64 v[160:161], v[240:241], 0, s[20:21]
	s_mov_b32 m0, s47
	s_nop 0
	global_load_lds_dwordx4 v[160:161], off
	s_waitcnt vmcnt(8)
	s_waitcnt lgkmcnt(0)
	s_barrier
	s_setprio 1
	s_waitcnt lgkmcnt(0)
	v_mfma_i32_16x16x64_i8 v[54:57], v[142:145], v[204:207], v[54:57]
	v_mfma_i32_16x16x64_i8 v[50:53], v[178:181], v[204:207], v[50:53]
	v_mfma_i32_16x16x64_i8 v[42:45], v[142:145], v[212:215], v[42:45]
	v_mfma_i32_16x16x64_i8 v[34:37], v[178:181], v[212:215], v[34:37]
	v_mfma_i32_16x16x64_i8 v[26:29], v[142:145], v[220:223], v[26:29]
	v_mfma_i32_16x16x64_i8 v[18:21], v[178:181], v[220:223], v[18:21]
	v_mfma_i32_16x16x64_i8 v[10:13], v[142:145], v[228:231], v[10:13]
	v_mfma_i32_16x16x64_i8 v[2:5], v[178:181], v[228:231], v[2:5]
	v_mfma_i32_16x16x64_i8 v[54:57], v[156:159], v[208:211], v[54:57]
	v_mfma_i32_16x16x64_i8 v[50:53], v[182:185], v[208:211], v[50:53]
	v_mfma_i32_16x16x64_i8 v[42:45], v[156:159], v[216:219], v[42:45]
	v_mfma_i32_16x16x64_i8 v[34:37], v[182:185], v[216:219], v[34:37]
	v_mfma_i32_16x16x64_i8 v[26:29], v[156:159], v[224:227], v[26:29]
	v_mfma_i32_16x16x64_i8 v[18:21], v[182:185], v[224:227], v[18:21]
	v_mfma_i32_16x16x64_i8 v[10:13], v[156:159], v[232:235], v[10:13]
	v_mfma_i32_16x16x64_i8 v[2:5], v[182:185], v[232:235], v[2:5]
	s_setprio 0
	s_setprio 1
	v_mfma_i32_16x16x64_i8 v[62:65], v[186:189], v[204:207], v[62:65]
	v_mfma_i32_16x16x64_i8 v[58:61], v[196:199], v[204:207], v[58:61]
	v_mfma_i32_16x16x64_i8 v[46:49], v[186:189], v[212:215], v[46:49]
	v_mfma_i32_16x16x64_i8 v[38:41], v[196:199], v[212:215], v[38:41]
	v_mfma_i32_16x16x64_i8 v[30:33], v[186:189], v[220:223], v[30:33]
	v_mfma_i32_16x16x64_i8 v[22:25], v[196:199], v[220:223], v[22:25]
	v_mfma_i32_16x16x64_i8 v[14:17], v[186:189], v[228:231], v[14:17]
	v_mfma_i32_16x16x64_i8 v[6:9], v[196:199], v[228:231], v[6:9]
	v_mfma_i32_16x16x64_i8 v[62:65], v[190:193], v[208:211], v[62:65]
	v_mfma_i32_16x16x64_i8 v[58:61], v[200:203], v[208:211], v[58:61]
	v_mfma_i32_16x16x64_i8 v[46:49], v[190:193], v[216:219], v[46:49]
	v_mfma_i32_16x16x64_i8 v[38:41], v[200:203], v[216:219], v[38:41]
	v_mfma_i32_16x16x64_i8 v[30:33], v[190:193], v[224:227], v[30:33]
	v_mfma_i32_16x16x64_i8 v[22:25], v[200:203], v[224:227], v[22:25]
	v_mfma_i32_16x16x64_i8 v[14:17], v[190:193], v[232:235], v[14:17]
	v_mfma_i32_16x16x64_i8 v[6:9], v[200:203], v[232:235], v[6:9]
	s_setprio 0
	s_barrier
	s_add_i32 s37, s37, 2
	s_cmp_gt_u32 s37, 13
	s_mov_b64 s[8:9], s[40:41]
	s_cbranch_scc0 .LBB0_2294
	s_and_b64 vcc, exec, s[26:27]
	s_cbranch_vccz .LBB0_2297
	s_barrier

; #define PG8_STAGE(bufoff, gbase, voff) do { _Pragma("unroll") for (int _i = 0; _i < 2; ++_i) \
;         __builtin_amdgcn_global_load_lds((const unsigned*)((const char*)(gbase) + (voff)[_i]), (LAS unsigned*)(lds + (bufoff) + ldsw + _i * 8192), 16, 0, 0); } while (0)
; #define PG8_LDA(dst, b, h) do { _Pragma("unroll") for (int m = 0; m < 4; ++m) dst[m] = PG8_LD32(lds + PG8_SA(b, h) + aoff + m * 2048); } while (0)
; #define PG8_LDB(dst, b, h) do { _Pragma("unroll") for (int n = 0; n < 2; ++n) dst[n] = PG8_LD32(lds + PG8_SB(b, h) + boff + n * 2048); } while (0)
; #define PG8_WAIT_V(n) asm volatile("s_waitcnt vmcnt(" #n ")" ::: "memory")
; #define PG8_WAIT_L(n) asm volatile("s_waitcnt lgkmcnt(" #n ")" ::: "memory")
; #define PG8_BAR __builtin_amdgcn_s_barrier()
; #define PG8_SCHED __builtin_amdgcn_sched_barrier(0)
; #define PG8_STA(bufoff, nextflag, h, koff) do { if constexpr (Sched::GATHER) { unsigned _o[2]; _o[0] = (nextflag) ? nxtA[h][0] : curA[h][0]; _o[1] = (nextflag) ? nxtA[h][1] : curA[h][1]; PG8_STAGE(bufoff, Ab + (koff), _o); } \
;         else { PG8_STAGE(bufoff, ((nextflag) ? nA : cA) + (size_t)(h) * hstep + (koff), voffA); } } while (0)
; template <class Epi, class Sched, bool ALIGN_EPI, int DT>
; __device__ __forceinline__ void gemm_phase(LAS unsigned char* lds, const int KB, const Sched& S, const Epi& E) {
;     ...
;             PG8_LDB(B0, 0, 0); PG8_LDB(B1, 0, 1); PG8_SCHED; PG8_LDA(At, 0, 0); PG8_STA(PG8_SA(1, 1), false, 1, k1);
;             PG8_WAIT_V(8); PG8_WAIT_L(0); PG8_BAR; PG8_MMA(0, 0, At, B0); PG8_MMA(0, 1, At, B1); PG8_BAR; PG8_SCHED;
;             PG8_LDA(At, 0, 1); PG8_STAGE(PG8_SB(0, 0), b2, voffB); PG8_STAGE(PG8_SB(0, 1), b2 + hstep, voffB); PG8_STA(PG8_SA(0, 0), last, 0, k2);
;             PG8_WAIT_V(8); PG8_WAIT_L(0); PG8_BAR; PG8_MMA(1, 0, At, B0); PG8_MMA(1, 1, At, B1); PG8_BAR; PG8_SCHED;
.LBB0_2387:
	ds_read_b128 v[18:21], v198
	ds_read_b128 v[22:25], v198 offset:1024
	ds_read_b128 v[26:29], v198 offset:2048
	ds_read_b128 v[30:33], v198 offset:3072
	ds_read_b128 v[2:5], v199
	ds_read_b128 v[6:9], v199 offset:1024
	ds_read_b128 v[10:13], v199 offset:2048
	ds_read_b128 v[14:17], v199 offset:3072
	s_add_u32 s42, s44, 0x100
	s_addc_u32 s43, s45, 0
	s_add_i32 s76, s63, s4
	s_add_i32 m0, s33, 0xc000
	s_add_i32 s77, s33, 0xe000
	s_add_i32 s74, s76, 0x2000
	s_cmp_eq_u32 s71, 18
	v_lshl_add_u64 v[184:185], v[178:179], 0, s[44:45]
	s_cselect_b64 vcc, -1, 0
	s_cselect_b32 s75, 0, s42
	v_cndmask_b32_e32 v185, v185, v177, vcc
	v_cndmask_b32_e32 v184, v184, v176, vcc
	v_lshl_add_u64 v[226:227], v[180:181], 0, s[44:45]
	ds_read_b128 v[186:189], v200
	ds_read_b128 v[190:193], v200 offset:1024
	ds_read_b128 v[202:205], v200 offset:2048
	ds_read_b128 v[206:209], v200 offset:3072
	ds_read_b128 v[210:213], v200 offset:4096
	ds_read_b128 v[214:217], v200 offset:5120
	ds_read_b128 v[218:221], v200 offset:6144
	ds_read_b128 v[222:225], v200 offset:7168
	global_load_lds_dwordx4 v[226:227], off
	v_lshl_add_u64 v[226:227], v[182:183], 0, s[44:45]
	s_mov_b32 m0, s77
	s_nop 0
	global_load_lds_dwordx4 v[226:227], off
	s_nop 0
	s_waitcnt vmcnt(8)
	s_waitcnt lgkmcnt(0)
	s_barrier
	s_setprio 1
	s_waitcnt lgkmcnt(0)
	v_mfma_scale_f32_16x16x128_f8f6f4 v[158:161], v[18:25], v[186:193], v[158:161], v1, v1 op_sel_hi:[0,0,0]
	v_mfma_scale_f32_16x16x128_f8f6f4 v[154:157], v[26:33], v[186:193], v[154:157], v1, v1 op_sel_hi:[0,0,0]
	v_mfma_scale_f32_16x16x128_f8f6f4 v[150:153], v[18:25], v[202:209], v[150:153], v1, v1 op_sel_hi:[0,0,0]
	v_mfma_scale_f32_16x16x128_f8f6f4 v[142:145], v[26:33], v[202:209], v[142:145], v1, v1 op_sel_hi:[0,0,0]
	v_mfma_scale_f32_16x16x128_f8f6f4 v[134:137], v[18:25], v[210:217], v[134:137], v1, v1 op_sel_hi:[0,0,0]
	v_mfma_scale_f32_16x16x128_f8f6f4 v[126:129], v[26:33], v[210:217], v[126:129], v1, v1 op_sel_hi:[0,0,0]
	v_mfma_scale_f32_16x16x128_f8f6f4 v[118:121], v[18:25], v[218:225], v[118:121], v1, v1 op_sel_hi:[0,0,0]
	v_mfma_scale_f32_16x16x128_f8f6f4 v[110:113], v[26:33], v[218:225], v[110:113], v1, v1 op_sel_hi:[0,0,0]
	s_setprio 0
	s_setprio 1
	v_mfma_scale_f32_16x16x128_f8f6f4 v[146:149], v[2:9], v[186:193], v[146:149], v1, v1 op_sel_hi:[0,0,0]
	v_mfma_scale_f32_16x16x128_f8f6f4 v[138:141], v[10:17], v[186:193], v[138:141], v1, v1 op_sel_hi:[0,0,0]
	v_mfma_scale_f32_16x16x128_f8f6f4 v[130:133], v[2:9], v[202:209], v[130:133], v1, v1 op_sel_hi:[0,0,0]
	v_mfma_scale_f32_16x16x128_f8f6f4 v[122:125], v[10:17], v[202:209], v[122:125], v1, v1 op_sel_hi:[0,0,0]
	v_mfma_scale_f32_16x16x128_f8f6f4 v[114:117], v[2:9], v[210:217], v[114:117], v1, v1 op_sel_hi:[0,0,0]
	v_mfma_scale_f32_16x16x128_f8f6f4 v[106:109], v[10:17], v[210:217], v[106:109], v1, v1 op_sel_hi:[0,0,0]
	v_mfma_scale_f32_16x16x128_f8f6f4 v[102:105], v[2:9], v[218:225], v[102:105], v1, v1 op_sel_hi:[0,0,0]
	v_mfma_scale_f32_16x16x128_f8f6f4 v[98:101], v[10:17], v[218:225], v[98:101], v1, v1 op_sel_hi:[0,0,0]
	s_setprio 0
	s_barrier
	s_mov_b32 m0, s76
	v_lshl_add_u64 v[188:189], v[184:185], 0, v[170:171]
	ds_read_b128 v[202:205], v200 offset:16384
	ds_read_b128 v[206:209], v200 offset:17408
	ds_read_b128 v[210:213], v200 offset:18432
	ds_read_b128 v[214:217], v200 offset:19456
	ds_read_b128 v[218:221], v200 offset:20480
	ds_read_b128 v[222:225], v200 offset:21504
	ds_read_b128 v[226:229], v200 offset:22528
	ds_read_b128 v[230:233], v200 offset:23552
	global_load_lds_dwordx4 v[188:189], off
	v_lshl_add_u64 v[186:187], v[184:185], 0, v[164:165]
	s_mov_b32 m0, s74
	s_cselect_b32 s45, s9, s41
	s_cselect_b32 s44, s8, s40
	v_lshl_add_u64 v[190:191], v[184:185], 0, s[12:13]
	s_add_i32 s74, s64, s4
	global_load_lds_dwordx4 v[186:187], off
	v_lshl_add_u64 v[192:193], v[190:191], 0, v[170:171]
	s_mov_b32 m0, s74
	v_lshl_add_u64 v[190:191], v[190:191], 0, v[164:165]
	global_load_lds_dwordx4 v[192:193], off
	s_add_i32 m0, s74, 0x2000
	s_add_u32 s44, s44, s75
	s_addc_u32 s45, s45, 0
	global_load_lds_dwordx4 v[190:191], off
	v_lshl_add_u64 v[190:191], s[44:45], 0, v[166:167]
	s_mov_b32 m0, s33
	v_lshl_add_u64 v[192:193], s[44:45], 0, v[168:169]
	global_load_lds_dwordx4 v[190:191], off
	s_mov_b32 m0, s39
	s_nop 0
	global_load_lds_dwordx4 v[192:193], off
	s_waitcnt vmcnt(8)
	s_waitcnt lgkmcnt(0)
	s_barrier
	s_setprio 1
	s_waitcnt lgkmcnt(0)
	v_mfma_scale_f32_16x16x128_f8f6f4 v[94:97], v[18:25], v[202:209], v[94:97], v1, v1 op_sel_hi:[0,0,0]
	v_mfma_scale_f32_16x16x128_f8f6f4 v[90:93], v[26:33], v[202:209], v[90:93], v1, v1 op_sel_hi:[0,0,0]
	v_mfma_scale_f32_16x16x128_f8f6f4 v[86:89], v[18:25], v[210:217], v[86:89], v1, v1 op_sel_hi:[0,0,0]
	v_mfma_scale_f32_16x16x128_f8f6f4 v[78:81], v[26:33], v[210:217], v[78:81], v1, v1 op_sel_hi:[0,0,0]
	v_mfma_scale_f32_16x16x128_f8f6f4 v[62:65], v[18:25], v[218:225], v[62:65], v1, v1 op_sel_hi:[0,0,0]
	v_mfma_scale_f32_16x16x128_f8f6f4 v[54:57], v[26:33], v[218:225], v[54:57], v1, v1 op_sel_hi:[0,0,0]
	v_mfma_scale_f32_16x16x128_f8f6f4 v[46:49], v[18:25], v[226:233], v[46:49], v1, v1 op_sel_hi:[0,0,0]
	v_mfma_scale_f32_16x16x128_f8f6f4 v[38:41], v[26:33], v[226:233], v[38:41], v1, v1 op_sel_hi:[0,0,0]
	s_setprio 0
	s_setprio 1
	v_mfma_scale_f32_16x16x128_f8f6f4 v[82:85], v[2:9], v[202:209], v[82:85], v1, v1 op_sel_hi:[0,0,0]
	v_mfma_scale_f32_16x16x128_f8f6f4 v[74:77], v[10:17], v[202:209], v[74:77], v1, v1 op_sel_hi:[0,0,0]
	v_mfma_scale_f32_16x16x128_f8f6f4 v[58:61], v[2:9], v[210:217], v[58:61], v1, v1 op_sel_hi:[0,0,0]
	v_mfma_scale_f32_16x16x128_f8f6f4 v[50:53], v[10:17], v[210:217], v[50:53], v1, v1 op_sel_hi:[0,0,0]
	v_mfma_scale_f32_16x16x128_f8f6f4 v[42:45], v[2:9], v[218:225], v[42:45], v1, v1 op_sel_hi:[0,0,0]
	v_mfma_scale_f32_16x16x128_f8f6f4 v[34:37], v[10:17], v[218:225], v[34:37], v1, v1 op_sel_hi:[0,0,0]
	v_mfma_scale_f32_16x16x128_f8f6f4 v[70:73], v[2:9], v[226:233], v[70:73], v1, v1 op_sel_hi:[0,0,0]
	v_mfma_scale_f32_16x16x128_f8f6f4 v[66:69], v[10:17], v[226:233], v[66:69], v1, v1 op_sel_hi:[0,0,0]
	s_setprio 0
	s_barrier
; #define PG8_STAGE(bufoff, gbase, voff) do { _Pragma("unroll") for (int _i = 0; _i < 2; ++_i) \
;         __builtin_amdgcn_global_load_lds((const unsigned*)((const char*)(gbase) + (voff)[_i]), (LAS unsigned*)(lds + (bufoff) + ldsw + _i * 8192), 16, 0, 0); } while (0)
; #define PG8_LDA(dst, b, h) do { _Pragma("unroll") for (int m = 0; m < 4; ++m) dst[m] = PG8_LD32(lds + PG8_SA(b, h) + aoff + m * 2048); } while (0)
; #define PG8_LDB(dst, b, h) do { _Pragma("unroll") for (int n = 0; n < 2; ++n) dst[n] = PG8_LD32(lds + PG8_SB(b, h) + boff + n * 2048); } while (0)
; #define PG8_WAIT_V(n) asm volatile("s_waitcnt vmcnt(" #n ")" ::: "memory")
; #define PG8_WAIT_L(n) asm volatile("s_waitcnt lgkmcnt(" #n ")" ::: "memory")
; #define PG8_BAR __builtin_amdgcn_s_barrier()
; #define PG8_SCHED __builtin_amdgcn_sched_barrier(0)
; #define PG8_STA(bufoff, nextflag, h, koff) do { if constexpr (Sched::GATHER) { unsigned _o[2]; _o[0] = (nextflag) ? nxtA[h][0] : curA[h][0]; _o[1] = (nextflag) ? nxtA[h][1] : curA[h][1]; PG8_STAGE(bufoff, Ab + (koff), _o); } \
;         else { PG8_STAGE(bufoff, ((nextflag) ? nA : cA) + (size_t)(h) * hstep + (koff), voffA); } } while (0)
; template <class Epi, class Sched, bool ALIGN_EPI, int DT>
; __device__ __forceinline__ void gemm_phase(LAS unsigned char* lds, const int KB, const Sched& S, const Epi& E) {
;     ...
;             PG8_LDB(B0, 1, 0); PG8_LDB(B1, 1, 1); PG8_SCHED; PG8_LDA(At, 1, 0); PG8_STA(PG8_SA(0, 1), last, 1, k2);
;             PG8_WAIT_V(8); PG8_WAIT_L(0); PG8_BAR; PG8_MMA(0, 0, At, B0); PG8_MMA(0, 1, At, B1); PG8_BAR; PG8_SCHED;
;             PG8_LDA(At, 1, 1); PG8_STAGE(PG8_SB(1, 0), b3, voffB); PG8_STAGE(PG8_SB(1, 1), b3 + hstep, voffB); PG8_STA(PG8_SA(1, 0), last, 0, k3);
;             PG8_WAIT_V(8); PG8_WAIT_L(0); PG8_BAR; PG8_MMA(1, 0, At, B0); PG8_MMA(1, 1, At, B1); PG8_BAR; PG8_SCHED;
;         }
;         if constexpr (ALIGN_EPI) { if (wr == 0) PG8_BAR; }
	s_add_i32 s74, 0, 0x18000
	s_add_i32 s75, 0, 0x1c000
	v_add_u32_e32 v14, s74, v196
	v_add_u32_e32 v30, s75, v196
	ds_read_b128 v[2:5], v14
	ds_read_b128 v[6:9], v14 offset:1024
	ds_read_b128 v[10:13], v14 offset:2048
	ds_read_b128 v[14:17], v14 offset:3072
	ds_read_b128 v[18:21], v30
	ds_read_b128 v[22:25], v30 offset:1024
	ds_read_b128 v[26:29], v30 offset:2048
	ds_read_b128 v[30:33], v30 offset:3072
	s_add_u32 s44, s44, 0x58000
	s_addc_u32 s45, s45, 0
	s_mov_b32 m0, s46
	v_lshl_add_u64 v[234:235], s[44:45], 0, v[166:167]
	ds_read_b128 v[202:205], v200 offset:32768
	ds_read_b128 v[206:209], v200 offset:33792
	ds_read_b128 v[210:213], v200 offset:34816
	ds_read_b128 v[214:217], v200 offset:35840
	ds_read_b128 v[218:221], v200 offset:36864
	ds_read_b128 v[222:225], v200 offset:37888
	ds_read_b128 v[226:229], v200 offset:38912
	ds_read_b128 v[230:233], v200 offset:39936
	global_load_lds_dwordx4 v[234:235], off
	v_lshl_add_u64 v[234:235], s[44:45], 0, v[168:169]
	s_mov_b32 m0, s47
	s_nop 0
	global_load_lds_dwordx4 v[234:235], off
	s_nop 0
	s_waitcnt vmcnt(8)
	s_waitcnt lgkmcnt(0)
	s_barrier
	s_setprio 1
	s_waitcnt lgkmcnt(0)
	v_mfma_scale_f32_16x16x128_f8f6f4 v[158:161], v[2:9], v[202:209], v[158:161], v1, v1 op_sel_hi:[0,0,0]
	v_mfma_scale_f32_16x16x128_f8f6f4 v[154:157], v[10:17], v[202:209], v[154:157], v1, v1 op_sel_hi:[0,0,0]
	v_mfma_scale_f32_16x16x128_f8f6f4 v[150:153], v[2:9], v[210:217], v[150:153], v1, v1 op_sel_hi:[0,0,0]
	v_mfma_scale_f32_16x16x128_f8f6f4 v[142:145], v[10:17], v[210:217], v[142:145], v1, v1 op_sel_hi:[0,0,0]
	v_mfma_scale_f32_16x16x128_f8f6f4 v[134:137], v[2:9], v[218:225], v[134:137], v1, v1 op_sel_hi:[0,0,0]
	v_mfma_scale_f32_16x16x128_f8f6f4 v[126:129], v[10:17], v[218:225], v[126:129], v1, v1 op_sel_hi:[0,0,0]
	v_mfma_scale_f32_16x16x128_f8f6f4 v[118:121], v[2:9], v[226:233], v[118:121], v1, v1 op_sel_hi:[0,0,0]
	v_mfma_scale_f32_16x16x128_f8f6f4 v[110:113], v[10:17], v[226:233], v[110:113], v1, v1 op_sel_hi:[0,0,0]
	s_setprio 0
	s_setprio 1
	v_mfma_scale_f32_16x16x128_f8f6f4 v[146:149], v[18:25], v[202:209], v[146:149], v1, v1 op_sel_hi:[0,0,0]
	v_mfma_scale_f32_16x16x128_f8f6f4 v[138:141], v[26:33], v[202:209], v[138:141], v1, v1 op_sel_hi:[0,0,0]
	v_mfma_scale_f32_16x16x128_f8f6f4 v[130:133], v[18:25], v[210:217], v[130:133], v1, v1 op_sel_hi:[0,0,0]
	v_mfma_scale_f32_16x16x128_f8f6f4 v[122:125], v[26:33], v[210:217], v[122:125], v1, v1 op_sel_hi:[0,0,0]
	v_mfma_scale_f32_16x16x128_f8f6f4 v[114:117], v[18:25], v[218:225], v[114:117], v1, v1 op_sel_hi:[0,0,0]
	v_mfma_scale_f32_16x16x128_f8f6f4 v[106:109], v[26:33], v[218:225], v[106:109], v1, v1 op_sel_hi:[0,0,0]
	v_mfma_scale_f32_16x16x128_f8f6f4 v[102:105], v[18:25], v[226:233], v[102:105], v1, v1 op_sel_hi:[0,0,0]
	v_mfma_scale_f32_16x16x128_f8f6f4 v[98:101], v[26:33], v[226:233], v[98:101], v1, v1 op_sel_hi:[0,0,0]
	s_setprio 0
	s_barrier
	s_add_i32 s44, s74, s4
	v_lshl_add_u64 v[188:189], v[188:189], 0, s[16:17]
	s_mov_b32 m0, s44
	ds_read_b128 v[202:205], v200 offset:49152
	ds_read_b128 v[206:209], v200 offset:50176
	ds_read_b128 v[210:213], v200 offset:51200
	ds_read_b128 v[214:217], v200 offset:52224
	ds_read_b128 v[218:221], v200 offset:53248
	ds_read_b128 v[222:225], v200 offset:54272
	ds_read_b128 v[226:229], v200 offset:55296
	ds_read_b128 v[230:233], v200 offset:56320
	global_load_lds_dwordx4 v[188:189], off
	v_lshl_add_u64 v[186:187], v[186:187], 0, s[16:17]
	s_add_i32 m0, s44, 0x2000
	v_lshl_add_u64 v[184:185], v[184:185], 0, s[18:19]
	s_add_i32 s44, s75, s4
	global_load_lds_dwordx4 v[186:187], off
	v_lshl_add_u64 v[186:187], v[184:185], 0, v[170:171]
	s_mov_b32 m0, s44
	v_lshl_add_u64 v[184:185], v[184:185], 0, v[164:165]
	global_load_lds_dwordx4 v[186:187], off
	s_add_i32 m0, s44, 0x2000
	s_nop 0
	global_load_lds_dwordx4 v[184:185], off
	v_lshl_add_u64 v[184:185], v[190:191], 0, s[16:17]
	s_mov_b32 m0, s52
	s_nop 0
	global_load_lds_dwordx4 v[184:185], off
	v_lshl_add_u64 v[184:185], v[192:193], 0, s[16:17]
	s_mov_b32 m0, s53
	s_nop 0
	global_load_lds_dwordx4 v[184:185], off
	s_waitcnt vmcnt(8)
	s_waitcnt lgkmcnt(0)
	s_barrier
	s_setprio 1
	s_waitcnt lgkmcnt(0)
	v_mfma_scale_f32_16x16x128_f8f6f4 v[94:97], v[2:9], v[202:209], v[94:97], v1, v1 op_sel_hi:[0,0,0]
	v_mfma_scale_f32_16x16x128_f8f6f4 v[90:93], v[10:17], v[202:209], v[90:93], v1, v1 op_sel_hi:[0,0,0]
	v_mfma_scale_f32_16x16x128_f8f6f4 v[86:89], v[2:9], v[210:217], v[86:89], v1, v1 op_sel_hi:[0,0,0]
	v_mfma_scale_f32_16x16x128_f8f6f4 v[78:81], v[10:17], v[210:217], v[78:81], v1, v1 op_sel_hi:[0,0,0]
	v_mfma_scale_f32_16x16x128_f8f6f4 v[62:65], v[2:9], v[218:225], v[62:65], v1, v1 op_sel_hi:[0,0,0]
	v_mfma_scale_f32_16x16x128_f8f6f4 v[54:57], v[10:17], v[218:225], v[54:57], v1, v1 op_sel_hi:[0,0,0]
	v_mfma_scale_f32_16x16x128_f8f6f4 v[46:49], v[2:9], v[226:233], v[46:49], v1, v1 op_sel_hi:[0,0,0]
	v_mfma_scale_f32_16x16x128_f8f6f4 v[38:41], v[10:17], v[226:233], v[38:41], v1, v1 op_sel_hi:[0,0,0]
	s_setprio 0
	s_setprio 1
	v_mfma_scale_f32_16x16x128_f8f6f4 v[82:85], v[18:25], v[202:209], v[82:85], v1, v1 op_sel_hi:[0,0,0]
	v_mfma_scale_f32_16x16x128_f8f6f4 v[74:77], v[26:33], v[202:209], v[74:77], v1, v1 op_sel_hi:[0,0,0]
	v_mfma_scale_f32_16x16x128_f8f6f4 v[58:61], v[18:25], v[210:217], v[58:61], v1, v1 op_sel_hi:[0,0,0]
	v_mfma_scale_f32_16x16x128_f8f6f4 v[50:53], v[26:33], v[210:217], v[50:53], v1, v1 op_sel_hi:[0,0,0]
	v_mfma_scale_f32_16x16x128_f8f6f4 v[42:45], v[18:25], v[218:225], v[42:45], v1, v1 op_sel_hi:[0,0,0]
	v_mfma_scale_f32_16x16x128_f8f6f4 v[34:37], v[26:33], v[218:225], v[34:37], v1, v1 op_sel_hi:[0,0,0]
	v_mfma_scale_f32_16x16x128_f8f6f4 v[70:73], v[18:25], v[226:233], v[70:73], v1, v1 op_sel_hi:[0,0,0]
	v_mfma_scale_f32_16x16x128_f8f6f4 v[66:69], v[26:33], v[226:233], v[66:69], v1, v1 op_sel_hi:[0,0,0]
	s_setprio 0
	s_barrier
	s_add_i32 s71, s71, 2
	s_cmp_gt_u32 s71, 19
	s_mov_b64 s[44:45], s[42:43]
	s_cbranch_scc0 .LBB0_2387
	s_and_b64 vcc, exec, s[20:21]
	s_cbranch_vccz .LBB0_2390
	s_barrier
